# dead zero-inits of fp8 pack destinations removed (both halves written by the cvt pair) in all phases, on top of v62
# speedup vs baseline: 1.0106x; 1.0073x over previous
; __device__ __forceinline__ float sat8(float x) { return __builtin_amdgcn_fmed3f(x, -448.0f, 448.0f); }
; __device__ __forceinline__ unsigned pk4_fp8(float a, float b, float c, float d) { int v = 0; v = __builtin_amdgcn_cvt_pk_fp8_f32(a, b, v, false); v = __builtin_amdgcn_cvt_pk_fp8_f32(c, d, v, true); return (unsigned)v; }
; __device__ __forceinline__ void f8_tile_load(const float* src, f32x4 (&v)[16], int lane) {
;     const float* s0 = src + (size_t)(16 * (lane >> 3)) * 2048 + 4 * (lane & 7);
; #pragma unroll
;     for (int i = 0; i < 16; ++i) v[i] = __builtin_nontemporal_load((const f32x4*)(s0 + (size_t)i * 2048));
; }
; __device__ __forceinline__ void f8_tile_store(const f32x4 (&v)[16], unsigned char* dst, int lane) {
;     unsigned d[16];
; #pragma unroll
;     for (int i = 0; i < 16; ++i) d[i] = pk4_fp8(sat8(v[i][0] * FP8_SW), sat8(v[i][1] * FP8_SW), sat8(v[i][2] * FP8_SW), sat8(v[i][3] * FP8_SW));
;     unsigned o[4][4];
; #pragma unroll
;     for (int w = 0; w < 4; ++w) {
;         const unsigned t0 = __builtin_amdgcn_perm(d[4 * w + 1], d[4 * w], 0x05010400u), t1 = __builtin_amdgcn_perm(d[4 * w + 1], d[4 * w], 0x07030602u);
;         const unsigned t2 = __builtin_amdgcn_perm(d[4 * w + 3], d[4 * w + 2], 0x05010400u), t3 = __builtin_amdgcn_perm(d[4 * w + 3], d[4 * w + 2], 0x07030602u);
;         o[0][w] = __builtin_amdgcn_perm(t2, t0, 0x05040100u); o[1][w] = __builtin_amdgcn_perm(t2, t0, 0x07060302u);
;         o[2][w] = __builtin_amdgcn_perm(t3, t1, 0x05040100u); o[3][w] = __builtin_amdgcn_perm(t3, t1, 0x07060302u);
;     }
;     unsigned char* d0 = dst + (size_t)(4 * (lane & 7)) * 2048 + 16 * (lane >> 3);
; #pragma unroll
;     for (int b = 0; b < 4; ++b) __builtin_nontemporal_store((v4u){o[b][0], o[b][1], o[b][2], o[b][3]}, (v4u*)(d0 + (size_t)b * 2048));
.Lconv_safe:
	s_waitcnt vmcnt(55)
	v_mul_f32_e32 v196, 0x43800000, v2
	v_mul_f32_e32 v201, 0x43800000, v3
	v_med3_f32 v196, v196, s28, v1
	v_med3_f32 v201, v201, s28, v1
	v_cvt_pk_fp8_f32 v204, v196, v201
	v_mul_f32_e32 v203, 0x43800000, v4
	v_mul_f32_e32 v201, 0x43800000, v5
	v_med3_f32 v196, v203, s28, v1
	v_med3_f32 v201, v201, s28, v1
	v_cvt_pk_fp8_f32 v204, v196, v201 op_sel:[0,0,1]
	s_waitcnt vmcnt(54)
	v_mul_f32_e32 v196, 0x43800000, v6
	v_mul_f32_e32 v201, 0x43800000, v7
	v_med3_f32 v196, v196, s28, v1
	v_med3_f32 v201, v201, s28, v1
	v_cvt_pk_fp8_f32 v205, v196, v201
	v_mul_f32_e32 v203, 0x43800000, v8
	v_mul_f32_e32 v201, 0x43800000, v9
	v_med3_f32 v196, v203, s28, v1
	v_med3_f32 v201, v201, s28, v1
	v_cvt_pk_fp8_f32 v205, v196, v201 op_sel:[0,0,1]
	s_waitcnt vmcnt(53)
	v_mul_f32_e32 v196, 0x43800000, v10
	v_mul_f32_e32 v201, 0x43800000, v11
	v_med3_f32 v196, v196, s28, v1
	v_med3_f32 v201, v201, s28, v1
	v_cvt_pk_fp8_f32 v206, v196, v201
	v_mul_f32_e32 v203, 0x43800000, v12
	v_mul_f32_e32 v201, 0x43800000, v13
	v_med3_f32 v196, v203, s28, v1
	v_med3_f32 v201, v201, s28, v1
	v_cvt_pk_fp8_f32 v206, v196, v201 op_sel:[0,0,1]
	s_waitcnt vmcnt(52)
	v_mul_f32_e32 v196, 0x43800000, v14
	v_mul_f32_e32 v201, 0x43800000, v15
	v_med3_f32 v196, v196, s28, v1
	v_med3_f32 v201, v201, s28, v1
	v_cvt_pk_fp8_f32 v207, v196, v201
	v_mul_f32_e32 v203, 0x43800000, v16
	v_mul_f32_e32 v201, 0x43800000, v17
	v_med3_f32 v196, v203, s28, v1
	v_med3_f32 v201, v201, s28, v1
	v_cvt_pk_fp8_f32 v207, v196, v201 op_sel:[0,0,1]
	s_waitcnt vmcnt(51)
	v_mul_f32_e32 v196, 0x43800000, v18
	v_mul_f32_e32 v201, 0x43800000, v19
	v_med3_f32 v196, v196, s28, v1
	v_med3_f32 v201, v201, s28, v1
	v_cvt_pk_fp8_f32 v209, v196, v201
	v_mul_f32_e32 v203, 0x43800000, v20
	v_mul_f32_e32 v201, 0x43800000, v21
	v_med3_f32 v196, v203, s28, v1
	v_med3_f32 v201, v201, s28, v1
	v_cvt_pk_fp8_f32 v209, v196, v201 op_sel:[0,0,1]
	s_waitcnt vmcnt(50)
	v_mul_f32_e32 v196, 0x43800000, v22
	v_mul_f32_e32 v201, 0x43800000, v23
	v_med3_f32 v196, v196, s28, v1
	v_med3_f32 v201, v201, s28, v1
	v_cvt_pk_fp8_f32 v210, v196, v201
	v_mul_f32_e32 v203, 0x43800000, v24
	v_mul_f32_e32 v201, 0x43800000, v25
	v_med3_f32 v196, v203, s28, v1
	v_med3_f32 v201, v201, s28, v1
	v_cvt_pk_fp8_f32 v210, v196, v201 op_sel:[0,0,1]
	s_waitcnt vmcnt(49)
	v_mul_f32_e32 v196, 0x43800000, v26
	v_mul_f32_e32 v201, 0x43800000, v27
	v_med3_f32 v196, v196, s28, v1
	v_med3_f32 v201, v201, s28, v1
	v_cvt_pk_fp8_f32 v211, v196, v201
	v_mul_f32_e32 v203, 0x43800000, v28
	v_mul_f32_e32 v201, 0x43800000, v29
	v_med3_f32 v196, v203, s28, v1
	v_med3_f32 v201, v201, s28, v1
	v_cvt_pk_fp8_f32 v211, v196, v201 op_sel:[0,0,1]
	s_waitcnt vmcnt(48)
	v_mul_f32_e32 v196, 0x43800000, v30
	v_mul_f32_e32 v201, 0x43800000, v31
	v_med3_f32 v196, v196, s28, v1
	v_med3_f32 v201, v201, s28, v1
	v_cvt_pk_fp8_f32 v213, v196, v201
	v_mul_f32_e32 v203, 0x43800000, v32
	v_mul_f32_e32 v201, 0x43800000, v33
	v_med3_f32 v196, v203, s28, v1
	v_med3_f32 v201, v201, s28, v1
	v_cvt_pk_fp8_f32 v213, v196, v201 op_sel:[0,0,1]
	s_waitcnt vmcnt(47)
	v_mul_f32_e32 v196, 0x43800000, v34
	v_mul_f32_e32 v201, 0x43800000, v35
	v_med3_f32 v196, v196, s28, v1
	v_med3_f32 v201, v201, s28, v1
	v_cvt_pk_fp8_f32 v216, v196, v201
	v_mul_f32_e32 v203, 0x43800000, v36
	v_mul_f32_e32 v201, 0x43800000, v37
	v_med3_f32 v196, v203, s28, v1
	v_med3_f32 v201, v201, s28, v1
	v_cvt_pk_fp8_f32 v216, v196, v201 op_sel:[0,0,1]
	s_waitcnt vmcnt(46)
	v_mul_f32_e32 v196, 0x43800000, v38
	v_mul_f32_e32 v201, 0x43800000, v39
	v_med3_f32 v196, v196, s28, v1
	v_med3_f32 v201, v201, s28, v1
	v_cvt_pk_fp8_f32 v217, v196, v201
	v_mul_f32_e32 v203, 0x43800000, v40
	v_mul_f32_e32 v201, 0x43800000, v41
	v_med3_f32 v196, v203, s28, v1
	v_med3_f32 v201, v201, s28, v1
	v_cvt_pk_fp8_f32 v217, v196, v201 op_sel:[0,0,1]
	s_waitcnt vmcnt(45)
	v_mul_f32_e32 v196, 0x43800000, v42
	v_mul_f32_e32 v201, 0x43800000, v43
	v_med3_f32 v196, v196, s28, v1
	v_med3_f32 v201, v201, s28, v1
	v_cvt_pk_fp8_f32 v220, v196, v201
	v_mul_f32_e32 v203, 0x43800000, v44
	v_mul_f32_e32 v201, 0x43800000, v45
	v_med3_f32 v196, v203, s28, v1
	v_med3_f32 v201, v201, s28, v1
	v_cvt_pk_fp8_f32 v220, v196, v201 op_sel:[0,0,1]
	s_waitcnt vmcnt(44)
	v_mul_f32_e32 v196, 0x43800000, v46
	v_mul_f32_e32 v201, 0x43800000, v47
	v_med3_f32 v196, v196, s28, v1
	v_med3_f32 v201, v201, s28, v1
	v_cvt_pk_fp8_f32 v221, v196, v201
	v_mul_f32_e32 v203, 0x43800000, v48
	v_mul_f32_e32 v201, 0x43800000, v49
	v_med3_f32 v196, v203, s28, v1
	v_med3_f32 v201, v201, s28, v1
	v_cvt_pk_fp8_f32 v221, v196, v201 op_sel:[0,0,1]
	s_waitcnt vmcnt(43)
; __device__ __forceinline__ void f8_tile_store(const f32x4 (&v)[16], unsigned char* dst, int lane) {
;     ...
;         const unsigned t0 = __builtin_amdgcn_perm(d[4 * w + 1], d[4 * w], 0x05010400u), t1 = __builtin_amdgcn_perm(d[4 * w + 1], d[4 * w], 0x07030602u);
;         const unsigned t2 = __builtin_amdgcn_perm(d[4 * w + 3], d[4 * w + 2], 0x05010400u), t3 = __builtin_amdgcn_perm(d[4 * w + 3], d[4 * w + 2], 0x07030602u);
;         o[0][w] = __builtin_amdgcn_perm(t2, t0, 0x05040100u); o[1][w] = __builtin_amdgcn_perm(t2, t0, 0x07060302u);
;         o[2][w] = __builtin_amdgcn_perm(t3, t1, 0x05040100u); o[3][w] = __builtin_amdgcn_perm(t3, t1, 0x07060302u);
;     }
;     unsigned char* d0 = dst + (size_t)(4 * (lane & 7)) * 2048 + 16 * (lane >> 3);
; #pragma unroll
;     for (int b = 0; b < 4; ++b) __builtin_nontemporal_store((v4u){o[b][0], o[b][1], o[b][2], o[b][3]}, (v4u*)(d0 + (size_t)b * 2048));
; }
; __device__ __forceinline__ void f8_item(const Params& p, int it, const float*& src, unsigned char*& dst) {
;     const int which = it >> 15, r = it & 32767, e = r >> 10, q = r & 1023, kb = q >> 6, nb = q & 63;
;     if (which == 2) { src = p.w_down + (size_t)e * FF * D + (size_t)(kb * 128) * D + nb * 32; dst = p.ws + WS_WD + ((size_t)e * D + nb * 32) * 2048 + kb * 128; }
;     else { const int f0 = nb * 32, drow = (f0 >> 7) * 256 + which * 128 + (f0 & 127);
;         src = (which == 0 ? p.w_gate : p.w_up) + (size_t)e * D * FF + (size_t)(kb * 128) * FF + f0; dst = p.ws + WS_WGU + ((size_t)e * 4096 + drow) * 2048 + kb * 128; }
; }
	v_mul_f32_e32 v196, 0x43800000, v50
	v_mul_f32_e32 v201, 0x43800000, v51
	v_med3_f32 v196, v196, s28, v1
	v_med3_f32 v201, v201, s28, v1
	v_cvt_pk_fp8_f32 v222, v196, v201
	v_mul_f32_e32 v203, 0x43800000, v52
	v_mul_f32_e32 v201, 0x43800000, v53
	v_med3_f32 v196, v203, s28, v1
	v_med3_f32 v201, v201, s28, v1
	v_cvt_pk_fp8_f32 v222, v196, v201 op_sel:[0,0,1]
	s_waitcnt vmcnt(42)
	v_mul_f32_e32 v196, 0x43800000, v54
	v_mul_f32_e32 v201, 0x43800000, v55
	v_med3_f32 v196, v196, s28, v1
	v_med3_f32 v201, v201, s28, v1
	v_cvt_pk_fp8_f32 v223, v196, v201
	v_mul_f32_e32 v203, 0x43800000, v56
	v_mul_f32_e32 v201, 0x43800000, v57
	v_med3_f32 v196, v203, s28, v1
	v_med3_f32 v201, v201, s28, v1
	v_cvt_pk_fp8_f32 v223, v196, v201 op_sel:[0,0,1]
	s_waitcnt vmcnt(41)
	v_mul_f32_e32 v196, 0x43800000, v58
	v_mul_f32_e32 v201, 0x43800000, v59
	v_med3_f32 v196, v196, s28, v1
	v_med3_f32 v201, v201, s28, v1
	v_cvt_pk_fp8_f32 v224, v196, v201
	v_mul_f32_e32 v203, 0x43800000, v60
	v_mul_f32_e32 v201, 0x43800000, v61
	v_med3_f32 v196, v203, s28, v1
	v_med3_f32 v201, v201, s28, v1
	v_cvt_pk_fp8_f32 v224, v196, v201 op_sel:[0,0,1]
	s_waitcnt vmcnt(40)
	v_mul_f32_e32 v196, 0x43800000, v62
	v_mul_f32_e32 v201, 0x43800000, v63
	v_med3_f32 v196, v196, s28, v1
	v_med3_f32 v201, v201, s28, v1
	v_cvt_pk_fp8_f32 v225, v196, v201
	v_mul_f32_e32 v203, 0x43800000, v64
	v_mul_f32_e32 v201, 0x43800000, v65
	v_med3_f32 v196, v203, s28, v1
	v_med3_f32 v201, v201, s28, v1
	v_cvt_pk_fp8_f32 v225, v196, v201 op_sel:[0,0,1]
	v_perm_b32 v196, v205, v204, s29
	v_perm_b32 v201, v205, v204, s30
	v_perm_b32 v203, v207, v206, s29
	v_perm_b32 v205, v207, v206, s30
	v_perm_b32 v204, v203, v196, s31
	v_perm_b32 v208, v203, v196, s34
	v_perm_b32 v214, v205, v201, s31
	v_perm_b32 v218, v205, v201, s34
	v_perm_b32 v196, v210, v209, s29
	v_perm_b32 v201, v210, v209, s30
	v_perm_b32 v203, v213, v211, s29
	v_perm_b32 v206, v213, v211, s30
	v_perm_b32 v205, v203, v196, s31
	v_perm_b32 v209, v203, v196, s34
	v_perm_b32 v215, v206, v201, s31
	v_perm_b32 v219, v206, v201, s34
	v_perm_b32 v196, v217, v216, s29
	v_perm_b32 v201, v217, v216, s30
	v_perm_b32 v203, v221, v220, s29
	v_perm_b32 v207, v221, v220, s30
	v_perm_b32 v206, v203, v196, s31
	v_perm_b32 v210, v203, v196, s34
	v_perm_b32 v216, v207, v201, s31
	v_perm_b32 v220, v207, v201, s34
	v_perm_b32 v196, v223, v222, s29
	v_perm_b32 v201, v223, v222, s30
	v_perm_b32 v203, v225, v224, s29
	v_lshl_add_u64 v[222:223], s[0:1], 0, v[194:195]
	s_add_i32 s36, s25, s2
	v_perm_b32 v207, v203, v196, s31
	v_lshl_add_u64 v[222:223], v[222:223], 0, v[198:199]
	v_perm_b32 v211, v203, v196, s34
	global_store_dwordx4 v[222:223], v[204:207], off nt
	global_store_dwordx4 v[222:223], v[208:211], off offset:2048 nt
	s_cmp_gt_i32 s36, 0x17fff
	v_add_co_u32_e32 v204, vcc, 0x1000, v222
	v_perm_b32 v213, v225, v224, s30
	s_nop 0
	v_addc_co_u32_e32 v205, vcc, 0, v223, vcc
	s_cselect_b64 s[14:15], -1, 0
	v_perm_b32 v217, v213, v201, s31
	s_and_b64 vcc, exec, s[14:15]
	v_perm_b32 v221, v213, v201, s34
	global_store_dwordx4 v[204:205], v[214:217], off nt
	global_store_dwordx4 v[204:205], v[218:221], off offset:2048 nt
	s_cbranch_vccnz .LBB0_179
	s_ashr_i32 s40, s36, 15
	s_bfe_u32 s37, s36, 0x5000a
	s_bfe_u32 s39, s36, 0x40006
	s_and_b32 s38, s36, 63
	s_cmp_lg_u32 s40, 2
	s_mov_b64 s[18:19], -1
	s_cbranch_scc0 .LBB0_176
	s_lshl_b32 s1, s38, 6
	s_lshl_b32 s0, s38, 5
	s_and_b32 s1, s1, 0xf00
	s_lshl_b32 s16, s40, 7
	s_add_i32 s1, s1, s16
	s_and_b32 s0, s0, 0x60
	s_or_b32 s0, s1, s0
	v_readlane_b32 s52, v255, 29
	s_cmpk_lt_u32 s36, 0x8000
	v_readlane_b32 s54, v255, 31
	v_readlane_b32 s55, v255, 32
	v_readlane_b32 s58, v255, 35
	v_readlane_b32 s59, v255, 36
	s_cselect_b32 s1, s55, s59
	s_cselect_b32 s16, s54, s58
	s_lshl_b32 s17, s37, 24
	s_add_u32 s16, s16, s17
	s_addc_u32 s1, s1, 0
	s_lshl_b32 s18, s39, 7
	s_lshl_b32 s17, s39, 20
	s_add_u32 s16, s16, s17
	s_addc_u32 s1, s1, 0
	s_lshl_b32 s17, s38, 7
	s_add_u32 s16, s16, s17
	s_addc_u32 s17, s1, 0
	s_ashr_i32 s1, s0, 31
	s_lshl_b32 s19, s37, 23
	s_lshl_b64 s[0:1], s[0:1], 11
	s_add_u32 s19, s21, s19
	s_addc_u32 s40, s22, 0
	s_add_u32 s0, s19, s0
	s_addc_u32 s1, s40, s1
	v_readlane_b32 s68, v255, 47
	s_add_u32 s0, s0, s18
	v_readlane_b32 s53, v255, 30
	v_readlane_b32 s56, v255, 33
	v_readlane_b32 s57, v255, 34
	v_readlane_b32 s60, v255, 37
	v_readlane_b32 s61, v255, 38
	v_readlane_b32 s62, v255, 39
	v_readlane_b32 s63, v255, 40
	v_readlane_b32 s64, v255, 41
	v_readlane_b32 s65, v255, 42
	v_readlane_b32 s66, v255, 43
	v_readlane_b32 s67, v255, 44
	v_readlane_b32 s69, v255, 48
	s_addc_u32 s1, s1, 0
	s_mov_b64 s[18:19], 0

; __device__ __forceinline__ float sat8(float x) { return __builtin_amdgcn_fmed3f(x, -448.0f, 448.0f); }
; __device__ __forceinline__ unsigned pk4_fp8(float a, float b, float c, float d) { int v = 0; v = __builtin_amdgcn_cvt_pk_fp8_f32(a, b, v, false); v = __builtin_amdgcn_cvt_pk_fp8_f32(c, d, v, true); return (unsigned)v; }
; __device__ __forceinline__ void f8_tile_store(const f32x4 (&v)[16], unsigned char* dst, int lane) {
;     unsigned d[16];
; #pragma unroll
;     for (int i = 0; i < 16; ++i) d[i] = pk4_fp8(sat8(v[i][0] * FP8_SW), sat8(v[i][1] * FP8_SW), sat8(v[i][2] * FP8_SW), sat8(v[i][3] * FP8_SW));
;     unsigned o[4][4];
; #pragma unroll
;     for (int w = 0; w < 4; ++w) {
;         const unsigned t0 = __builtin_amdgcn_perm(d[4 * w + 1], d[4 * w], 0x05010400u), t1 = __builtin_amdgcn_perm(d[4 * w + 1], d[4 * w], 0x07030602u);
;         const unsigned t2 = __builtin_amdgcn_perm(d[4 * w + 3], d[4 * w + 2], 0x05010400u), t3 = __builtin_amdgcn_perm(d[4 * w + 3], d[4 * w + 2], 0x07030602u);
;         o[0][w] = __builtin_amdgcn_perm(t2, t0, 0x05040100u); o[1][w] = __builtin_amdgcn_perm(t2, t0, 0x07060302u);
;         o[2][w] = __builtin_amdgcn_perm(t3, t1, 0x05040100u); o[3][w] = __builtin_amdgcn_perm(t3, t1, 0x07060302u);
.LBB0_179:
	s_andn2_b64 vcc, exec, s[8:9]
	s_mov_b64 s[16:17], -1
	s_cbranch_vccnz .LBB0_172
	s_waitcnt vmcnt(40)
	v_mul_f32_e32 v196, 0x43800000, v66
	v_mul_f32_e32 v201, 0x43800000, v67
	v_med3_f32 v196, v196, s28, v1
	v_med3_f32 v201, v201, s28, v1
	v_cvt_pk_fp8_f32 v204, v196, v201
	v_mul_f32_e32 v203, 0x43800000, v68
	v_mul_f32_e32 v201, 0x43800000, v69
	v_med3_f32 v196, v203, s28, v1
	v_med3_f32 v201, v201, s28, v1
	v_cvt_pk_fp8_f32 v204, v196, v201 op_sel:[0,0,1]
	v_mul_f32_e32 v196, 0x43800000, v70
	v_mul_f32_e32 v201, 0x43800000, v71
	v_med3_f32 v196, v196, s28, v1
	v_med3_f32 v201, v201, s28, v1
	v_cvt_pk_fp8_f32 v205, v196, v201
	v_mul_f32_e32 v203, 0x43800000, v72
	v_mul_f32_e32 v201, 0x43800000, v73
	v_med3_f32 v196, v203, s28, v1
	v_med3_f32 v201, v201, s28, v1
	v_cvt_pk_fp8_f32 v205, v196, v201 op_sel:[0,0,1]
	v_mul_f32_e32 v196, 0x43800000, v74
	v_mul_f32_e32 v201, 0x43800000, v75
	v_med3_f32 v196, v196, s28, v1
	v_med3_f32 v201, v201, s28, v1
	v_cvt_pk_fp8_f32 v206, v196, v201
	v_mul_f32_e32 v203, 0x43800000, v76
	v_mul_f32_e32 v201, 0x43800000, v77
	v_med3_f32 v196, v203, s28, v1
	v_med3_f32 v201, v201, s28, v1
	v_cvt_pk_fp8_f32 v206, v196, v201 op_sel:[0,0,1]
	v_mul_f32_e32 v196, 0x43800000, v78
	v_mul_f32_e32 v201, 0x43800000, v79
	v_med3_f32 v196, v196, s28, v1
	v_med3_f32 v201, v201, s28, v1
	v_cvt_pk_fp8_f32 v207, v196, v201
	v_mul_f32_e32 v203, 0x43800000, v80
	v_mul_f32_e32 v201, 0x43800000, v81
	v_med3_f32 v196, v203, s28, v1
	v_med3_f32 v201, v201, s28, v1
	v_cvt_pk_fp8_f32 v207, v196, v201 op_sel:[0,0,1]
	v_mul_f32_e32 v196, 0x43800000, v82
	v_mul_f32_e32 v201, 0x43800000, v83
	v_med3_f32 v196, v196, s28, v1
	v_med3_f32 v201, v201, s28, v1
	v_cvt_pk_fp8_f32 v209, v196, v201
	v_mul_f32_e32 v203, 0x43800000, v84
	v_mul_f32_e32 v201, 0x43800000, v85
	v_med3_f32 v196, v203, s28, v1
	v_med3_f32 v201, v201, s28, v1
	v_cvt_pk_fp8_f32 v209, v196, v201 op_sel:[0,0,1]
	v_mul_f32_e32 v196, 0x43800000, v86
	v_mul_f32_e32 v201, 0x43800000, v87
	v_med3_f32 v196, v196, s28, v1
	v_med3_f32 v201, v201, s28, v1
	v_cvt_pk_fp8_f32 v210, v196, v201
	v_mul_f32_e32 v203, 0x43800000, v88
	v_mul_f32_e32 v201, 0x43800000, v89
	v_med3_f32 v196, v203, s28, v1
	v_med3_f32 v201, v201, s28, v1
	v_cvt_pk_fp8_f32 v210, v196, v201 op_sel:[0,0,1]
	v_mul_f32_e32 v196, 0x43800000, v90
	v_mul_f32_e32 v201, 0x43800000, v91
	v_med3_f32 v196, v196, s28, v1
	v_med3_f32 v201, v201, s28, v1
	v_cvt_pk_fp8_f32 v211, v196, v201
	v_mul_f32_e32 v203, 0x43800000, v92
	v_mul_f32_e32 v201, 0x43800000, v93
	v_med3_f32 v196, v203, s28, v1
	v_med3_f32 v201, v201, s28, v1
	v_cvt_pk_fp8_f32 v211, v196, v201 op_sel:[0,0,1]
	v_mul_f32_e32 v196, 0x43800000, v94
	v_mul_f32_e32 v201, 0x43800000, v95
	v_med3_f32 v196, v196, s28, v1
	v_med3_f32 v201, v201, s28, v1
	v_cvt_pk_fp8_f32 v213, v196, v201
	v_mul_f32_e32 v203, 0x43800000, v96
	v_mul_f32_e32 v201, 0x43800000, v97
	v_med3_f32 v196, v203, s28, v1
	v_med3_f32 v201, v201, s28, v1
	v_cvt_pk_fp8_f32 v213, v196, v201 op_sel:[0,0,1]
	v_mul_f32_e32 v196, 0x43800000, v98
	v_mul_f32_e32 v201, 0x43800000, v99
	v_med3_f32 v196, v196, s28, v1
	v_med3_f32 v201, v201, s28, v1
	v_cvt_pk_fp8_f32 v216, v196, v201
	v_mul_f32_e32 v203, 0x43800000, v100
	v_mul_f32_e32 v201, 0x43800000, v101
	v_med3_f32 v196, v203, s28, v1
	v_med3_f32 v201, v201, s28, v1
	v_cvt_pk_fp8_f32 v216, v196, v201 op_sel:[0,0,1]
	v_mul_f32_e32 v196, 0x43800000, v102
	v_mul_f32_e32 v201, 0x43800000, v103
	v_med3_f32 v196, v196, s28, v1
	v_med3_f32 v201, v201, s28, v1
	v_cvt_pk_fp8_f32 v217, v196, v201
	v_mul_f32_e32 v203, 0x43800000, v104
	v_mul_f32_e32 v201, 0x43800000, v105
	v_med3_f32 v196, v203, s28, v1
	v_med3_f32 v201, v201, s28, v1
	v_cvt_pk_fp8_f32 v217, v196, v201 op_sel:[0,0,1]
	v_mul_f32_e32 v196, 0x43800000, v106
	v_mul_f32_e32 v201, 0x43800000, v107
	v_med3_f32 v196, v196, s28, v1
	v_med3_f32 v201, v201, s28, v1
	v_cvt_pk_fp8_f32 v220, v196, v201
	v_mul_f32_e32 v203, 0x43800000, v108
	v_mul_f32_e32 v201, 0x43800000, v109
	v_med3_f32 v196, v203, s28, v1
	v_med3_f32 v201, v201, s28, v1
	v_cvt_pk_fp8_f32 v220, v196, v201 op_sel:[0,0,1]
	v_mul_f32_e32 v196, 0x43800000, v110
	v_mul_f32_e32 v201, 0x43800000, v111
	v_med3_f32 v196, v196, s28, v1
	v_med3_f32 v201, v201, s28, v1
	v_cvt_pk_fp8_f32 v221, v196, v201
	v_mul_f32_e32 v203, 0x43800000, v112
	v_mul_f32_e32 v201, 0x43800000, v113
	v_med3_f32 v196, v203, s28, v1
	v_med3_f32 v201, v201, s28, v1
	v_cvt_pk_fp8_f32 v221, v196, v201 op_sel:[0,0,1]
	v_mul_f32_e32 v196, 0x43800000, v114
; __device__ __forceinline__ float sat8(float x) { return __builtin_amdgcn_fmed3f(x, -448.0f, 448.0f); }
; __device__ __forceinline__ unsigned pk4_fp8(float a, float b, float c, float d) { int v = 0; v = __builtin_amdgcn_cvt_pk_fp8_f32(a, b, v, false); v = __builtin_amdgcn_cvt_pk_fp8_f32(c, d, v, true); return (unsigned)v; }
; __device__ __forceinline__ void f8_tile_store(const f32x4 (&v)[16], unsigned char* dst, int lane) {
;     ...
;     for (int i = 0; i < 16; ++i) d[i] = pk4_fp8(sat8(v[i][0] * FP8_SW), sat8(v[i][1] * FP8_SW), sat8(v[i][2] * FP8_SW), sat8(v[i][3] * FP8_SW));
;     unsigned o[4][4];
; #pragma unroll
;     for (int w = 0; w < 4; ++w) {
;         const unsigned t0 = __builtin_amdgcn_perm(d[4 * w + 1], d[4 * w], 0x05010400u), t1 = __builtin_amdgcn_perm(d[4 * w + 1], d[4 * w], 0x07030602u);
;         const unsigned t2 = __builtin_amdgcn_perm(d[4 * w + 3], d[4 * w + 2], 0x05010400u), t3 = __builtin_amdgcn_perm(d[4 * w + 3], d[4 * w + 2], 0x07030602u);
;         o[0][w] = __builtin_amdgcn_perm(t2, t0, 0x05040100u); o[1][w] = __builtin_amdgcn_perm(t2, t0, 0x07060302u);
;         o[2][w] = __builtin_amdgcn_perm(t3, t1, 0x05040100u); o[3][w] = __builtin_amdgcn_perm(t3, t1, 0x07060302u);
;     }
;     unsigned char* d0 = dst + (size_t)(4 * (lane & 7)) * 2048 + 16 * (lane >> 3);
; #pragma unroll
;     for (int b = 0; b < 4; ++b) __builtin_nontemporal_store((v4u){o[b][0], o[b][1], o[b][2], o[b][3]}, (v4u*)(d0 + (size_t)b * 2048));
; }
; __device__ __forceinline__ void f8_item(const Params& p, int it, const float*& src, unsigned char*& dst) {
;     const int which = it >> 15, r = it & 32767, e = r >> 10, q = r & 1023, kb = q >> 6, nb = q & 63;
;     if (which == 2) { src = p.w_down + (size_t)e * FF * D + (size_t)(kb * 128) * D + nb * 32; dst = p.ws + WS_WD + ((size_t)e * D + nb * 32) * 2048 + kb * 128; }
;     else { const int f0 = nb * 32, drow = (f0 >> 7) * 256 + which * 128 + (f0 & 127);
;         src = (which == 0 ? p.w_gate : p.w_up) + (size_t)e * D * FF + (size_t)(kb * 128) * FF + f0; dst = p.ws + WS_WGU + ((size_t)e * 4096 + drow) * 2048 + kb * 128; }
; }
	v_mul_f32_e32 v201, 0x43800000, v115
	v_med3_f32 v196, v196, s28, v1
	v_med3_f32 v201, v201, s28, v1
	v_cvt_pk_fp8_f32 v222, v196, v201
	v_mul_f32_e32 v203, 0x43800000, v116
	v_mul_f32_e32 v201, 0x43800000, v117
	v_med3_f32 v196, v203, s28, v1
	v_med3_f32 v201, v201, s28, v1
	v_cvt_pk_fp8_f32 v222, v196, v201 op_sel:[0,0,1]
	v_mul_f32_e32 v196, 0x43800000, v118
	v_mul_f32_e32 v201, 0x43800000, v119
	v_med3_f32 v196, v196, s28, v1
	v_med3_f32 v201, v201, s28, v1
	v_cvt_pk_fp8_f32 v223, v196, v201
	v_mul_f32_e32 v203, 0x43800000, v120
	v_mul_f32_e32 v201, 0x43800000, v121
	v_med3_f32 v196, v203, s28, v1
	v_med3_f32 v201, v201, s28, v1
	v_cvt_pk_fp8_f32 v223, v196, v201 op_sel:[0,0,1]
	v_mul_f32_e32 v196, 0x43800000, v122
	v_mul_f32_e32 v201, 0x43800000, v123
	v_med3_f32 v196, v196, s28, v1
	v_med3_f32 v201, v201, s28, v1
	v_cvt_pk_fp8_f32 v224, v196, v201
	v_mul_f32_e32 v203, 0x43800000, v124
	v_mul_f32_e32 v201, 0x43800000, v125
	v_med3_f32 v196, v203, s28, v1
	v_med3_f32 v201, v201, s28, v1
	v_cvt_pk_fp8_f32 v224, v196, v201 op_sel:[0,0,1]
	v_mul_f32_e32 v196, 0x43800000, v126
	v_mul_f32_e32 v201, 0x43800000, v127
	v_med3_f32 v196, v196, s28, v1
	v_med3_f32 v201, v201, s28, v1
	v_cvt_pk_fp8_f32 v225, v196, v201
	v_mul_f32_e32 v203, 0x43800000, v128
	v_mul_f32_e32 v201, 0x43800000, v129
	v_med3_f32 v196, v203, s28, v1
	v_med3_f32 v201, v201, s28, v1
	v_cvt_pk_fp8_f32 v225, v196, v201 op_sel:[0,0,1]
	v_perm_b32 v196, v205, v204, s29
	v_perm_b32 v201, v205, v204, s30
	v_perm_b32 v203, v207, v206, s29
	v_perm_b32 v205, v207, v206, s30
	v_perm_b32 v204, v203, v196, s31
	v_perm_b32 v208, v203, v196, s34
	v_perm_b32 v214, v205, v201, s31
	v_perm_b32 v218, v205, v201, s34
	v_perm_b32 v196, v210, v209, s29
	v_perm_b32 v201, v210, v209, s30
	v_perm_b32 v203, v213, v211, s29
	v_perm_b32 v206, v213, v211, s30
	v_perm_b32 v205, v203, v196, s31
	v_perm_b32 v209, v203, v196, s34
	v_perm_b32 v215, v206, v201, s31
	v_perm_b32 v219, v206, v201, s34
	v_perm_b32 v196, v217, v216, s29
	v_perm_b32 v201, v217, v216, s30
	v_perm_b32 v203, v221, v220, s29
	v_perm_b32 v207, v221, v220, s30
	v_perm_b32 v206, v203, v196, s31
	v_perm_b32 v210, v203, v196, s34
	v_perm_b32 v216, v207, v201, s31
	v_perm_b32 v220, v207, v201, s34
	v_perm_b32 v196, v223, v222, s29
	v_perm_b32 v201, v223, v222, s30
	v_perm_b32 v203, v225, v224, s29
	v_lshl_add_u64 v[222:223], s[6:7], 0, v[194:195]
	s_add_i32 s37, s26, s2
	v_perm_b32 v207, v203, v196, s31
	v_lshl_add_u64 v[222:223], v[222:223], 0, v[198:199]
	v_perm_b32 v213, v225, v224, s30
	v_perm_b32 v211, v203, v196, s34
	global_store_dwordx4 v[222:223], v[204:207], off nt
	global_store_dwordx4 v[222:223], v[208:211], off offset:2048 nt
	s_cmp_lt_i32 s37, 0x18000
	v_add_co_u32_e32 v204, vcc, 0x1000, v222
	v_perm_b32 v217, v213, v201, s31
	v_perm_b32 v221, v213, v201, s34
	v_addc_co_u32_e32 v205, vcc, 0, v223, vcc
	s_cselect_b64 s[8:9], -1, 0
	s_cmp_gt_i32 s37, 0x17fff
	global_store_dwordx4 v[204:205], v[214:217], off nt
	global_store_dwordx4 v[204:205], v[218:221], off offset:2048 nt
	s_cbranch_scc1 .LBB0_186
	s_ashr_i32 s41, s37, 15
	s_bfe_u32 s38, s37, 0x5000a
	s_bfe_u32 s40, s37, 0x40006
	s_and_b32 s39, s37, 63
	s_cmp_lg_u32 s41, 2
	s_mov_b64 s[18:19], -1
	s_cbranch_scc0 .LBB0_183
	s_lshl_b32 s7, s39, 6
	s_lshl_b32 s6, s39, 5
	s_and_b32 s7, s7, 0xf00
	s_lshl_b32 s16, s41, 7
	s_add_i32 s7, s7, s16
	s_and_b32 s6, s6, 0x60
	s_or_b32 s6, s7, s6
	v_readlane_b32 s52, v255, 29
	s_cmpk_lt_u32 s37, 0x8000
	v_readlane_b32 s54, v255, 31
	v_readlane_b32 s55, v255, 32
	v_readlane_b32 s58, v255, 35
	v_readlane_b32 s59, v255, 36
	s_cselect_b32 s7, s55, s59
	s_cselect_b32 s16, s54, s58
	s_lshl_b32 s17, s38, 24
	s_add_u32 s16, s16, s17
	s_addc_u32 s7, s7, 0
	s_lshl_b32 s18, s40, 7
	s_lshl_b32 s17, s40, 20
	s_add_u32 s16, s16, s17
	s_addc_u32 s7, s7, 0
	s_lshl_b32 s17, s39, 7
	s_add_u32 s16, s16, s17
	s_addc_u32 s17, s7, 0
	s_ashr_i32 s7, s6, 31
	s_lshl_b32 s19, s38, 23
	s_lshl_b64 s[6:7], s[6:7], 11
	s_add_u32 s19, s21, s19
	s_addc_u32 s37, s22, 0
	s_add_u32 s6, s19, s6
	s_addc_u32 s7, s37, s7
	v_readlane_b32 s68, v255, 47
	s_add_u32 s6, s6, s18
	v_readlane_b32 s53, v255, 30
	v_readlane_b32 s56, v255, 33
	v_readlane_b32 s57, v255, 34
	v_readlane_b32 s60, v255, 37
	v_readlane_b32 s61, v255, 38
	v_readlane_b32 s62, v255, 39
	v_readlane_b32 s63, v255, 40
	v_readlane_b32 s64, v255, 41
	v_readlane_b32 s65, v255, 42
	v_readlane_b32 s66, v255, 43
	v_readlane_b32 s67, v255, 44
	v_readlane_b32 s69, v255, 48
	s_addc_u32 s7, s7, 0
	s_mov_b64 s[18:19], 0

; __device__ __forceinline__ float sat8(float x) { return __builtin_amdgcn_fmed3f(x, -448.0f, 448.0f); }
; __device__ __forceinline__ unsigned pk4_fp8(float a, float b, float c, float d) { int v = 0; v = __builtin_amdgcn_cvt_pk_fp8_f32(a, b, v, false); v = __builtin_amdgcn_cvt_pk_fp8_f32(c, d, v, true); return (unsigned)v; }
; __device__ __forceinline__ void f8_tile_store(const f32x4 (&v)[16], unsigned char* dst, int lane) {
;     unsigned d[16];
; #pragma unroll
;     for (int i = 0; i < 16; ++i) d[i] = pk4_fp8(sat8(v[i][0] * FP8_SW), sat8(v[i][1] * FP8_SW), sat8(v[i][2] * FP8_SW), sat8(v[i][3] * FP8_SW));
;     unsigned o[4][4];
; #pragma unroll
;     for (int w = 0; w < 4; ++w) {
;         const unsigned t0 = __builtin_amdgcn_perm(d[4 * w + 1], d[4 * w], 0x05010400u), t1 = __builtin_amdgcn_perm(d[4 * w + 1], d[4 * w], 0x07030602u);
;         const unsigned t2 = __builtin_amdgcn_perm(d[4 * w + 3], d[4 * w + 2], 0x05010400u), t3 = __builtin_amdgcn_perm(d[4 * w + 3], d[4 * w + 2], 0x07030602u);
;         o[0][w] = __builtin_amdgcn_perm(t2, t0, 0x05040100u); o[1][w] = __builtin_amdgcn_perm(t2, t0, 0x07060302u);
;         o[2][w] = __builtin_amdgcn_perm(t3, t1, 0x05040100u); o[3][w] = __builtin_amdgcn_perm(t3, t1, 0x07060302u);
.LBB0_186:
	s_andn2_b64 vcc, exec, s[12:13]
	s_mov_b64 s[16:17], -1
	s_cbranch_vccnz .LBB0_172
	s_waitcnt vmcnt(40)
	v_mul_f32_e32 v196, 0x43800000, v130
	v_mul_f32_e32 v201, 0x43800000, v131
	v_med3_f32 v196, v196, s28, v1
	v_med3_f32 v201, v201, s28, v1
	v_cvt_pk_fp8_f32 v204, v196, v201
	v_mul_f32_e32 v203, 0x43800000, v132
	v_mul_f32_e32 v201, 0x43800000, v133
	v_med3_f32 v196, v203, s28, v1
	v_med3_f32 v201, v201, s28, v1
	v_cvt_pk_fp8_f32 v204, v196, v201 op_sel:[0,0,1]
	v_mul_f32_e32 v196, 0x43800000, v134
	v_mul_f32_e32 v201, 0x43800000, v135
	v_med3_f32 v196, v196, s28, v1
	v_med3_f32 v201, v201, s28, v1
	v_cvt_pk_fp8_f32 v205, v196, v201
	v_mul_f32_e32 v203, 0x43800000, v136
	v_mul_f32_e32 v201, 0x43800000, v137
	v_med3_f32 v196, v203, s28, v1
	v_med3_f32 v201, v201, s28, v1
	v_cvt_pk_fp8_f32 v205, v196, v201 op_sel:[0,0,1]
	v_mul_f32_e32 v196, 0x43800000, v138
	v_mul_f32_e32 v201, 0x43800000, v139
	v_med3_f32 v196, v196, s28, v1
	v_med3_f32 v201, v201, s28, v1
	v_cvt_pk_fp8_f32 v206, v196, v201
	v_mul_f32_e32 v203, 0x43800000, v140
	v_mul_f32_e32 v201, 0x43800000, v141
	v_med3_f32 v196, v203, s28, v1
	v_med3_f32 v201, v201, s28, v1
	v_cvt_pk_fp8_f32 v206, v196, v201 op_sel:[0,0,1]
	v_mul_f32_e32 v196, 0x43800000, v142
	v_mul_f32_e32 v201, 0x43800000, v143
	v_med3_f32 v196, v196, s28, v1
	v_med3_f32 v201, v201, s28, v1
	v_cvt_pk_fp8_f32 v207, v196, v201
	v_mul_f32_e32 v203, 0x43800000, v144
	v_mul_f32_e32 v201, 0x43800000, v145
	v_med3_f32 v196, v203, s28, v1
	v_med3_f32 v201, v201, s28, v1
	v_cvt_pk_fp8_f32 v207, v196, v201 op_sel:[0,0,1]
	v_mul_f32_e32 v196, 0x43800000, v146
	v_mul_f32_e32 v201, 0x43800000, v147
	v_med3_f32 v196, v196, s28, v1
	v_med3_f32 v201, v201, s28, v1
	v_cvt_pk_fp8_f32 v209, v196, v201
	v_mul_f32_e32 v203, 0x43800000, v148
	v_mul_f32_e32 v201, 0x43800000, v149
	v_med3_f32 v196, v203, s28, v1
	v_med3_f32 v201, v201, s28, v1
	v_cvt_pk_fp8_f32 v209, v196, v201 op_sel:[0,0,1]
	v_mul_f32_e32 v196, 0x43800000, v150
	v_mul_f32_e32 v201, 0x43800000, v151
	v_med3_f32 v196, v196, s28, v1
	v_med3_f32 v201, v201, s28, v1
	v_cvt_pk_fp8_f32 v210, v196, v201
	v_mul_f32_e32 v203, 0x43800000, v152
	v_mul_f32_e32 v201, 0x43800000, v153
	v_med3_f32 v196, v203, s28, v1
	v_med3_f32 v201, v201, s28, v1
	v_cvt_pk_fp8_f32 v210, v196, v201 op_sel:[0,0,1]
	v_mul_f32_e32 v196, 0x43800000, v154
	v_mul_f32_e32 v201, 0x43800000, v155
	v_med3_f32 v196, v196, s28, v1
	v_med3_f32 v201, v201, s28, v1
	v_cvt_pk_fp8_f32 v211, v196, v201
	v_mul_f32_e32 v203, 0x43800000, v156
	v_mul_f32_e32 v201, 0x43800000, v157
	v_med3_f32 v196, v203, s28, v1
	v_med3_f32 v201, v201, s28, v1
	v_cvt_pk_fp8_f32 v211, v196, v201 op_sel:[0,0,1]
	v_mul_f32_e32 v196, 0x43800000, v158
	v_mul_f32_e32 v201, 0x43800000, v159
	v_med3_f32 v196, v196, s28, v1
	v_med3_f32 v201, v201, s28, v1
	v_cvt_pk_fp8_f32 v213, v196, v201
	v_mul_f32_e32 v203, 0x43800000, v160
	v_mul_f32_e32 v201, 0x43800000, v161
	v_med3_f32 v196, v203, s28, v1
	v_med3_f32 v201, v201, s28, v1
	v_cvt_pk_fp8_f32 v213, v196, v201 op_sel:[0,0,1]
	v_mul_f32_e32 v196, 0x43800000, v162
	v_mul_f32_e32 v201, 0x43800000, v163
	v_med3_f32 v196, v196, s28, v1
	v_med3_f32 v201, v201, s28, v1
	v_cvt_pk_fp8_f32 v216, v196, v201
	v_mul_f32_e32 v203, 0x43800000, v164
	v_mul_f32_e32 v201, 0x43800000, v165
	v_med3_f32 v196, v203, s28, v1
	v_med3_f32 v201, v201, s28, v1
	v_cvt_pk_fp8_f32 v216, v196, v201 op_sel:[0,0,1]
	v_mul_f32_e32 v196, 0x43800000, v166
	v_mul_f32_e32 v201, 0x43800000, v167
	v_med3_f32 v196, v196, s28, v1
	v_med3_f32 v201, v201, s28, v1
	v_cvt_pk_fp8_f32 v217, v196, v201
	v_mul_f32_e32 v203, 0x43800000, v168
	v_mul_f32_e32 v201, 0x43800000, v169
	v_med3_f32 v196, v203, s28, v1
	v_med3_f32 v201, v201, s28, v1
	v_cvt_pk_fp8_f32 v217, v196, v201 op_sel:[0,0,1]
	v_mul_f32_e32 v196, 0x43800000, v170
	v_mul_f32_e32 v201, 0x43800000, v171
	v_med3_f32 v196, v196, s28, v1
	v_med3_f32 v201, v201, s28, v1
	v_cvt_pk_fp8_f32 v220, v196, v201
	v_mul_f32_e32 v203, 0x43800000, v172
	v_mul_f32_e32 v201, 0x43800000, v173
	v_med3_f32 v196, v203, s28, v1
	v_med3_f32 v201, v201, s28, v1
	v_cvt_pk_fp8_f32 v220, v196, v201 op_sel:[0,0,1]
	v_mul_f32_e32 v196, 0x43800000, v174
	v_mul_f32_e32 v201, 0x43800000, v175
	v_med3_f32 v196, v196, s28, v1
	v_med3_f32 v201, v201, s28, v1
	v_cvt_pk_fp8_f32 v221, v196, v201
	v_mul_f32_e32 v203, 0x43800000, v176
	v_mul_f32_e32 v201, 0x43800000, v177
	v_med3_f32 v196, v203, s28, v1
	v_med3_f32 v201, v201, s28, v1
	v_cvt_pk_fp8_f32 v221, v196, v201 op_sel:[0,0,1]
	v_mul_f32_e32 v196, 0x43800000, v178
; __device__ __forceinline__ float sat8(float x) { return __builtin_amdgcn_fmed3f(x, -448.0f, 448.0f); }
; __device__ __forceinline__ unsigned pk4_fp8(float a, float b, float c, float d) { int v = 0; v = __builtin_amdgcn_cvt_pk_fp8_f32(a, b, v, false); v = __builtin_amdgcn_cvt_pk_fp8_f32(c, d, v, true); return (unsigned)v; }
; __device__ __forceinline__ void f8_tile_store(const f32x4 (&v)[16], unsigned char* dst, int lane) {
;     ...
;     for (int i = 0; i < 16; ++i) d[i] = pk4_fp8(sat8(v[i][0] * FP8_SW), sat8(v[i][1] * FP8_SW), sat8(v[i][2] * FP8_SW), sat8(v[i][3] * FP8_SW));
;     unsigned o[4][4];
; #pragma unroll
;     for (int w = 0; w < 4; ++w) {
;         const unsigned t0 = __builtin_amdgcn_perm(d[4 * w + 1], d[4 * w], 0x05010400u), t1 = __builtin_amdgcn_perm(d[4 * w + 1], d[4 * w], 0x07030602u);
;         const unsigned t2 = __builtin_amdgcn_perm(d[4 * w + 3], d[4 * w + 2], 0x05010400u), t3 = __builtin_amdgcn_perm(d[4 * w + 3], d[4 * w + 2], 0x07030602u);
;         o[0][w] = __builtin_amdgcn_perm(t2, t0, 0x05040100u); o[1][w] = __builtin_amdgcn_perm(t2, t0, 0x07060302u);
;         o[2][w] = __builtin_amdgcn_perm(t3, t1, 0x05040100u); o[3][w] = __builtin_amdgcn_perm(t3, t1, 0x07060302u);
;     }
;     unsigned char* d0 = dst + (size_t)(4 * (lane & 7)) * 2048 + 16 * (lane >> 3);
; #pragma unroll
;     for (int b = 0; b < 4; ++b) __builtin_nontemporal_store((v4u){o[b][0], o[b][1], o[b][2], o[b][3]}, (v4u*)(d0 + (size_t)b * 2048));
; }
; __device__ __forceinline__ void f8_item(const Params& p, int it, const float*& src, unsigned char*& dst) {
;     const int which = it >> 15, r = it & 32767, e = r >> 10, q = r & 1023, kb = q >> 6, nb = q & 63;
;     if (which == 2) { src = p.w_down + (size_t)e * FF * D + (size_t)(kb * 128) * D + nb * 32; dst = p.ws + WS_WD + ((size_t)e * D + nb * 32) * 2048 + kb * 128; }
;     else { const int f0 = nb * 32, drow = (f0 >> 7) * 256 + which * 128 + (f0 & 127);
;         src = (which == 0 ? p.w_gate : p.w_up) + (size_t)e * D * FF + (size_t)(kb * 128) * FF + f0; dst = p.ws + WS_WGU + ((size_t)e * 4096 + drow) * 2048 + kb * 128; }
; }
	v_mul_f32_e32 v201, 0x43800000, v179
	v_med3_f32 v196, v196, s28, v1
	v_med3_f32 v201, v201, s28, v1
	v_cvt_pk_fp8_f32 v222, v196, v201
	v_mul_f32_e32 v203, 0x43800000, v180
	v_mul_f32_e32 v201, 0x43800000, v181
	v_med3_f32 v196, v203, s28, v1
	v_med3_f32 v201, v201, s28, v1
	v_cvt_pk_fp8_f32 v222, v196, v201 op_sel:[0,0,1]
	v_mul_f32_e32 v196, 0x43800000, v182
	v_mul_f32_e32 v201, 0x43800000, v183
	v_med3_f32 v196, v196, s28, v1
	v_med3_f32 v201, v201, s28, v1
	v_cvt_pk_fp8_f32 v223, v196, v201
	v_mul_f32_e32 v203, 0x43800000, v184
	v_mul_f32_e32 v201, 0x43800000, v185
	v_med3_f32 v196, v203, s28, v1
	v_med3_f32 v201, v201, s28, v1
	v_cvt_pk_fp8_f32 v223, v196, v201 op_sel:[0,0,1]
	v_mul_f32_e32 v196, 0x43800000, v186
	v_mul_f32_e32 v201, 0x43800000, v187
	v_med3_f32 v196, v196, s28, v1
	v_med3_f32 v201, v201, s28, v1
	v_cvt_pk_fp8_f32 v224, v196, v201
	v_mul_f32_e32 v203, 0x43800000, v188
	v_mul_f32_e32 v201, 0x43800000, v189
	v_med3_f32 v196, v203, s28, v1
	v_med3_f32 v201, v201, s28, v1
	v_cvt_pk_fp8_f32 v224, v196, v201 op_sel:[0,0,1]
	v_mul_f32_e32 v196, 0x43800000, v190
	v_mul_f32_e32 v201, 0x43800000, v191
	v_med3_f32 v196, v196, s28, v1
	v_med3_f32 v201, v201, s28, v1
	v_cvt_pk_fp8_f32 v225, v196, v201
	v_mul_f32_e32 v203, 0x43800000, v192
	v_mul_f32_e32 v201, 0x43800000, v193
	v_med3_f32 v196, v203, s28, v1
	v_med3_f32 v201, v201, s28, v1
	v_cvt_pk_fp8_f32 v225, v196, v201 op_sel:[0,0,1]
	v_perm_b32 v196, v205, v204, s29
	v_perm_b32 v201, v205, v204, s30
	v_perm_b32 v203, v207, v206, s29
	v_perm_b32 v205, v207, v206, s30
	v_perm_b32 v204, v203, v196, s31
	v_perm_b32 v208, v203, v196, s34
	v_perm_b32 v214, v205, v201, s31
	v_perm_b32 v218, v205, v201, s34
	v_perm_b32 v196, v210, v209, s29
	v_perm_b32 v201, v210, v209, s30
	v_perm_b32 v203, v213, v211, s29
	v_perm_b32 v206, v213, v211, s30
	v_perm_b32 v205, v203, v196, s31
	v_perm_b32 v209, v203, v196, s34
	v_perm_b32 v215, v206, v201, s31
	v_perm_b32 v219, v206, v201, s34
	v_perm_b32 v196, v217, v216, s29
	v_perm_b32 v201, v217, v216, s30
	v_perm_b32 v203, v221, v220, s29
	v_perm_b32 v207, v221, v220, s30
	v_perm_b32 v206, v203, v196, s31
	v_perm_b32 v210, v203, v196, s34
	v_perm_b32 v216, v207, v201, s31
	v_perm_b32 v220, v207, v201, s34
	v_perm_b32 v196, v223, v222, s29
	v_perm_b32 v201, v223, v222, s30
	v_perm_b32 v203, v225, v224, s29
	v_lshl_add_u64 v[222:223], s[10:11], 0, v[194:195]
	s_add_i32 s2, s27, s2
	v_perm_b32 v207, v203, v196, s31
	v_lshl_add_u64 v[222:223], v[222:223], 0, v[198:199]
	v_perm_b32 v213, v225, v224, s30
	v_perm_b32 v211, v203, v196, s34
	global_store_dwordx4 v[222:223], v[204:207], off nt
	global_store_dwordx4 v[222:223], v[208:211], off offset:2048 nt
	s_cmp_lt_i32 s2, 0x18000
	v_add_co_u32_e32 v204, vcc, 0x1000, v222
	v_perm_b32 v217, v213, v201, s31
	v_perm_b32 v221, v213, v201, s34
	v_addc_co_u32_e32 v205, vcc, 0, v223, vcc
	s_cselect_b64 s[12:13], -1, 0
	s_cmp_gt_i32 s2, 0x17fff
	global_store_dwordx4 v[204:205], v[214:217], off nt
	global_store_dwordx4 v[204:205], v[218:221], off offset:2048 nt
	s_cbranch_scc1 .LBB0_171
	s_ashr_i32 s40, s2, 15
	s_bfe_u32 s37, s2, 0x5000a
	s_bfe_u32 s39, s2, 0x40006
	s_and_b32 s38, s2, 63
	s_cmp_lg_u32 s40, 2
	s_mov_b64 s[18:19], -1
	s_cbranch_scc0 .LBB0_190
	s_lshl_b32 s11, s38, 6
	s_lshl_b32 s10, s38, 5
	s_and_b32 s11, s11, 0xf00
	s_lshl_b32 s16, s40, 7
	s_add_i32 s11, s11, s16
	s_and_b32 s10, s10, 0x60
	s_or_b32 s10, s11, s10
	v_readlane_b32 s52, v255, 29
	s_cmpk_lt_u32 s2, 0x8000
	v_readlane_b32 s54, v255, 31
	v_readlane_b32 s55, v255, 32
	v_readlane_b32 s58, v255, 35
	v_readlane_b32 s59, v255, 36
	s_cselect_b32 s2, s55, s59
	s_cselect_b32 s11, s54, s58
	s_lshl_b32 s16, s37, 24
	s_add_u32 s11, s11, s16
	s_addc_u32 s2, s2, 0
	s_lshl_b32 s18, s39, 7
	s_lshl_b32 s16, s39, 20
	s_add_u32 s11, s11, s16
	s_addc_u32 s2, s2, 0
	s_lshl_b32 s16, s38, 7
	s_add_u32 s16, s11, s16
	s_addc_u32 s17, s2, 0
	s_ashr_i32 s11, s10, 31
	s_lshl_b32 s2, s37, 23
	s_lshl_b64 s[10:11], s[10:11], 11
	s_add_u32 s2, s21, s2
	s_addc_u32 s19, s22, 0
	s_add_u32 s2, s2, s10
	s_addc_u32 s11, s19, s11
	v_readlane_b32 s68, v255, 47
	s_add_u32 s10, s2, s18
	v_readlane_b32 s53, v255, 30
	v_readlane_b32 s56, v255, 33
	v_readlane_b32 s57, v255, 34
	v_readlane_b32 s60, v255, 37
	v_readlane_b32 s61, v255, 38
	v_readlane_b32 s62, v255, 39
	v_readlane_b32 s63, v255, 40
	v_readlane_b32 s64, v255, 41
	v_readlane_b32 s65, v255, 42
	v_readlane_b32 s66, v255, 43
	v_readlane_b32 s67, v255, 44
	v_readlane_b32 s69, v255, 48
	s_addc_u32 s11, s11, 0
	s_mov_b64 s[18:19], 0

; __device__ __forceinline__ void phase_attn(const Params& p, LAS unsigned char* lds, int G) {
;     ...
;             int tz = threadIdx.x; asm volatile("" : "+v"(tz));
;             const int wave = __builtin_amdgcn_readfirstlane(tz >> 6), r = tz & 31, hf = (tz >> 5) & 1, hk = wave >> 2, wl = wave & 3;
;             for (int qt = 0; qt < 4; ++qt) {
;                 const size_t tok = (size_t)b * SEQ + n * 128 + qt * 32 + r;
;                 float tot = 0.f;
; #pragma unroll
;                 for (int hd = 0; hd < 16; ++hd) tot += ssqp[hd * 128 + qt * 32 + r];
;                 const float rstd = rsqrtf(tot * (1.f / 1024.f) + EPS);
;                 v4u uu[2][2][2];
; #pragma unroll
;                 for (int hsel = 0; hsel < 2; ++hsel)
; #pragma unroll
;                     for (int dt = 0; dt < 2; ++dt)
; #pragma unroll
;                         for (int pp = 0; pp < 2; ++pp) uu[hsel][dt][pp] = *(const v4u*)(att + tok * ALD + (hk * 8 + wl * 2 + hsel) * 64 + dt * 32 + 16 * pp + 8 * hf);
; #pragma unroll
;                 for (int hsel = 0; hsel < 2; ++hsel)
; #pragma unroll
;                     for (int dt = 0; dt < 2; ++dt) { asm volatile("" : "+v"(uu[hsel][dt][0]), "+v"(uu[hsel][dt][1])); }
;     ...
; #pragma unroll
;                 for (int hsel = 0; hsel < 2; ++hsel)
; #pragma unroll
;                     for (int dt = 0; dt < 2; ++dt) { unsigned fa[2], fb[2]; const float rs = rstd * FP8_SA;
; #pragma unroll
;                         for (int pp = 0; pp < 2; ++pp) { const int col = (hk * 8 + wl * 2 + hsel) * 64 + dt * 32 + 16 * pp + 8 * hf;
;                             const v4u u = uu[hsel][dt][pp]; const f32x4 w0 = *(const f32x4*)(p.attn_out_norm_w + col), w1 = *(const f32x4*)(p.attn_out_norm_w + col + 4);
;                             const unsigned d0 = pk4_fp8(sat8(bflo(u.x) * rs * w0[0]), sat8(bfhi(u.x) * rs * w0[1]), sat8(bflo(u.y) * rs * w0[2]), sat8(bfhi(u.y) * rs * w0[3]));
;                             const unsigned d1 = pk4_fp8(sat8(bflo(u.z) * rs * w1[0]), sat8(bfhi(u.z) * rs * w1[1]), sat8(bflo(u.w) * rs * w1[2]), sat8(bfhi(u.w) * rs * w1[3]));
;                             if (pp == 0) { fa[0] = d0; fa[1] = d1; } else { fb[0] = d0; fb[1] = d1; } }
;                         const v2u r0 = __builtin_amdgcn_permlane32_swap(fa[0], fb[0], false, false), r1 = __builtin_amdgcn_permlane32_swap(fa[1], fb[1], false, false);
.LBB0_307:
	v_mov_b32_e32 v2, v0
	s_barrier
	v_mov_b32_e32 v35, s71
	v_readfirstlane_b32 s0, v2
	v_and_b32_e32 v26, 31, v2
	v_bfe_u32 v27, v2, 5, 1
	s_lshl_b32 s0, s0, 1
	v_lshlrev_b32_e32 v130, 4, v27
	v_or_b32_e32 v34, s70, v26
	s_and_b32 s0, s0, 0xffffff80
	v_lshl_add_u64 v[32:33], s[66:67], 0, v[130:131]
	v_lshlrev_b64 v[36:37], 11, v[34:35]
	s_ashr_i32 s1, s0, 31
	v_lshl_add_u64 v[2:3], v[32:33], 0, v[36:37]
	s_lshl_b64 s[4:5], s[0:1], 1
	v_lshl_add_u64 v[2:3], v[2:3], 0, s[4:5]
	global_load_dwordx4 v[40:43], v[2:3], off
	global_load_dwordx4 v[44:47], v[2:3], off offset:32
	global_load_dwordx4 v[22:25], v[2:3], off offset:64
	global_load_dwordx4 v[18:21], v[2:3], off offset:96
	global_load_dwordx4 v[14:17], v[2:3], off offset:128
	global_load_dwordx4 v[10:13], v[2:3], off offset:160
	global_load_dwordx4 v[6:9], v[2:3], off offset:192
	s_nop 0
	global_load_dwordx4 v[2:5], v[2:3], off offset:224
	v_lshl_add_u32 v26, v26, 2, 0
	v_lshlrev_b32_e32 v27, 3, v27
	v_add_u32_e32 v38, 0x22400, v26
	v_or_b32_e32 v26, s0, v27
	v_readlane_b32 s8, v255, 6
	v_ashrrev_i32_e32 v27, 31, v26
	v_readlane_b32 s16, v255, 14
	v_readlane_b32 s17, v255, 15
	ds_read2st64_b32 v[30:31], v38 offset1:2
	ds_read2st64_b32 v[68:69], v38 offset0:4 offset1:6
	ds_read2st64_b32 v[70:71], v38 offset0:8 offset1:10
	ds_read2st64_b32 v[72:73], v38 offset0:12 offset1:14
	ds_read2st64_b32 v[74:75], v38 offset0:16 offset1:18
	ds_read2st64_b32 v[76:77], v38 offset0:20 offset1:22
	ds_read2st64_b32 v[78:79], v38 offset0:24 offset1:26
	ds_read2st64_b32 v[80:81], v38 offset0:28 offset1:30
	v_lshl_add_u64 v[28:29], v[26:27], 2, s[16:17]
	s_waitcnt lgkmcnt(7)
	v_add_f32_e32 v27, 0, v30
	v_add_f32_e32 v27, v27, v31
	s_waitcnt lgkmcnt(6)
	v_add_f32_e32 v27, v27, v68
	v_add_f32_e32 v27, v27, v69
	s_waitcnt lgkmcnt(5)
	v_add_f32_e32 v27, v27, v70
	v_add_f32_e32 v27, v27, v71
	s_waitcnt lgkmcnt(4)
	v_add_f32_e32 v27, v27, v72
	v_add_f32_e32 v27, v27, v73
	s_waitcnt lgkmcnt(3)
	v_add_f32_e32 v27, v27, v74
	v_add_f32_e32 v27, v27, v75
	s_waitcnt lgkmcnt(2)
	v_add_f32_e32 v27, v27, v76
	v_add_f32_e32 v27, v27, v77
	s_waitcnt lgkmcnt(1)
	v_add_f32_e32 v27, v27, v78
	v_add_f32_e32 v27, v27, v79
	s_waitcnt lgkmcnt(0)
	v_add_f32_e32 v27, v27, v80
	v_add_f32_e32 v27, v27, v81
	v_fmamk_f32 v27, v27, 0x3a800000, v1
	v_mul_f32_e32 v30, 0x4b800000, v27
	v_cmp_gt_f32_e32 vcc, s43, v27
	v_mov_b32_e32 v64, v131
	v_mov_b32_e32 v65, v131
	v_cndmask_b32_e32 v27, v27, v30, vcc
	v_rsq_f32_e32 v27, v27
	v_mov_b32_e32 v66, v131
	v_mov_b32_e32 v67, v131
	v_lshl_add_u64 v[30:31], s[50:51], 0, v[130:131]
	v_mul_f32_e32 v39, 0x45800000, v27
	v_cndmask_b32_e32 v27, v27, v39, vcc
	v_mul_f32_e32 v39, 0x41800000, v27
	v_lshl_add_u64 v[36:37], v[30:31], 0, v[36:37]
	v_lshl_add_u64 v[36:37], v[36:37], 0, s[0:1]
	s_add_i32 s97, s97, s96
	s_cmpk_gt_i32 s97, 0xff
	v_readlane_b32 s9, v255, 7
	v_readlane_b32 s10, v255, 8
	v_readlane_b32 s11, v255, 9
	v_readlane_b32 s12, v255, 10
	v_readlane_b32 s13, v255, 11
	v_readlane_b32 s14, v255, 12
	v_readlane_b32 s15, v255, 13
	v_readlane_b32 s18, v255, 16
	v_readlane_b32 s19, v255, 17
	v_readlane_b32 s20, v255, 18
	v_readlane_b32 s21, v255, 19
	v_readlane_b32 s22, v255, 20
	v_readlane_b32 s23, v255, 21
	s_waitcnt vmcnt(6)
	s_waitcnt vmcnt(4)
	s_waitcnt vmcnt(2)
	s_waitcnt vmcnt(0)
	global_load_dwordx4 v[48:51], v[28:29], off
	global_load_dwordx4 v[52:55], v[28:29], off offset:16
	global_load_dwordx4 v[56:59], v[28:29], off offset:64
	global_load_dwordx4 v[60:63], v[28:29], off offset:80
	v_lshlrev_b32_e32 v27, 16, v40
	v_and_b32_e32 v40, 0xffff0000, v40
	v_lshlrev_b32_e32 v68, 16, v41
	v_and_b32_e32 v41, 0xffff0000, v41
	v_lshlrev_b32_e32 v69, 16, v42
	v_and_b32_e32 v42, 0xffff0000, v42
	v_lshlrev_b32_e32 v71, 16, v44
	v_and_b32_e32 v44, 0xffff0000, v44
	v_lshlrev_b32_e32 v73, 16, v46
	v_and_b32_e32 v46, 0xffff0000, v46
	v_mul_f32_e32 v27, v39, v27
	v_mul_f32_e32 v40, v39, v40
	v_mul_f32_e32 v41, v39, v41
	v_mul_f32_e32 v69, v39, v69
	v_mul_f32_e32 v42, v39, v42
	v_mul_f32_e32 v71, v39, v71
	v_mul_f32_e32 v44, v39, v44
	v_mul_f32_e32 v73, v39, v73
	v_mul_f32_e32 v46, v39, v46
	v_lshlrev_b32_e32 v70, 16, v43
	v_and_b32_e32 v43, 0xffff0000, v43
	v_lshlrev_b32_e32 v72, 16, v45
	v_and_b32_e32 v45, 0xffff0000, v45
	v_lshlrev_b32_e32 v74, 16, v47
	v_and_b32_e32 v47, 0xffff0000, v47
	v_mul_f32_e32 v68, v39, v68
	v_mul_f32_e32 v70, v39, v70
	v_mul_f32_e32 v43, v39, v43
	v_mul_f32_e32 v72, v39, v72
	v_mul_f32_e32 v45, v39, v45
	v_mul_f32_e32 v74, v39, v74
	v_mul_f32_e32 v47, v39, v47
	s_waitcnt vmcnt(3)
	v_mul_f32_e32 v27, v48, v27
	v_mul_f32_e32 v40, v49, v40
	v_mul_f32_e32 v41, v51, v41
	s_waitcnt vmcnt(2)
	v_mul_f32_e32 v49, v69, v52
	v_mul_f32_e32 v42, v42, v53
	s_waitcnt vmcnt(1)
	v_mul_f32_e32 v51, v71, v56
	v_mul_f32_e32 v44, v44, v57
	s_waitcnt vmcnt(0)
; __device__ __forceinline__ float sat8(float x) { return __builtin_amdgcn_fmed3f(x, -448.0f, 448.0f); }
; __device__ __forceinline__ unsigned pk4_fp8(float a, float b, float c, float d) { int v = 0; v = __builtin_amdgcn_cvt_pk_fp8_f32(a, b, v, false); v = __builtin_amdgcn_cvt_pk_fp8_f32(c, d, v, true); return (unsigned)v; }
; __device__ __forceinline__ void phase_attn(const Params& p, LAS unsigned char* lds, int G) {
;     ...
; #pragma unroll
;                 for (int hsel = 0; hsel < 2; ++hsel)
; #pragma unroll
;                     for (int dt = 0; dt < 2; ++dt) { unsigned fa[2], fb[2]; const float rs = rstd * FP8_SA;
; #pragma unroll
;                         for (int pp = 0; pp < 2; ++pp) { const int col = (hk * 8 + wl * 2 + hsel) * 64 + dt * 32 + 16 * pp + 8 * hf;
;                             const v4u u = uu[hsel][dt][pp]; const f32x4 w0 = *(const f32x4*)(p.attn_out_norm_w + col), w1 = *(const f32x4*)(p.attn_out_norm_w + col + 4);
;                             const unsigned d0 = pk4_fp8(sat8(bflo(u.x) * rs * w0[0]), sat8(bfhi(u.x) * rs * w0[1]), sat8(bflo(u.y) * rs * w0[2]), sat8(bfhi(u.y) * rs * w0[3]));
;                             const unsigned d1 = pk4_fp8(sat8(bflo(u.z) * rs * w1[0]), sat8(bfhi(u.z) * rs * w1[1]), sat8(bflo(u.w) * rs * w1[2]), sat8(bfhi(u.w) * rs * w1[3]));
;                             if (pp == 0) { fa[0] = d0; fa[1] = d1; } else { fb[0] = d0; fb[1] = d1; } }
;                         const v2u r0 = __builtin_amdgcn_permlane32_swap(fa[0], fb[0], false, false), r1 = __builtin_amdgcn_permlane32_swap(fa[1], fb[1], false, false);
;                         *(v4u*)((unsigned char*)mix + tok * 2048 + (hk * 8 + wl * 2 + hsel) * 64 + dt * 32 + 16 * hf) = (v4u){r0.x, r1.x, r0.y, r1.y}; }
	v_mul_f32_e32 v53, v73, v60
	v_mul_f32_e32 v46, v46, v61
	v_med3_f32 v27, v27, s91, v135
	v_med3_f32 v40, v40, s91, v135
	v_med3_f32 v49, v49, s91, v135
	v_med3_f32 v42, v42, s91, v135
	v_med3_f32 v51, v51, s91, v135
	v_med3_f32 v44, v44, s91, v135
	v_med3_f32 v53, v53, s91, v135
	v_med3_f32 v46, v46, s91, v135
	v_cvt_pk_fp8_f32 v64, v27, v40
	v_cvt_pk_fp8_f32 v66, v51, v44
	v_cvt_pk_fp8_f32 v65, v49, v42
	v_cvt_pk_fp8_f32 v67, v53, v46
	v_mul_f32_e32 v48, v50, v68
	v_mul_f32_e32 v50, v70, v54
	v_mul_f32_e32 v43, v43, v55
	v_mul_f32_e32 v52, v72, v58
	v_mul_f32_e32 v45, v45, v59
	v_mul_f32_e32 v54, v74, v62
	v_mul_f32_e32 v47, v47, v63
	v_med3_f32 v48, v48, s91, v135
	v_med3_f32 v41, v41, s91, v135
	v_med3_f32 v50, v50, s91, v135
	v_med3_f32 v43, v43, s91, v135
	v_med3_f32 v52, v52, s91, v135
	v_med3_f32 v45, v45, s91, v135
	v_med3_f32 v54, v54, s91, v135
	v_med3_f32 v47, v47, s91, v135
	v_cvt_pk_fp8_f32 v64, v48, v41 op_sel:[0,0,1]
	v_cvt_pk_fp8_f32 v66, v52, v45 op_sel:[0,0,1]
	v_cvt_pk_fp8_f32 v65, v50, v43 op_sel:[0,0,1]
	v_cvt_pk_fp8_f32 v67, v54, v47 op_sel:[0,0,1]
	v_lshlrev_b32_e32 v60, 16, v22
	v_permlane32_swap_b32_e32 v64, v66
	v_permlane32_swap_b32_e32 v65, v67
	global_store_dwordx4 v[36:37], v[64:67], off
	global_load_dwordx4 v[40:43], v[28:29], off offset:128
	global_load_dwordx4 v[44:47], v[28:29], off offset:144
	global_load_dwordx4 v[48:51], v[28:29], off offset:192
	global_load_dwordx4 v[52:55], v[28:29], off offset:208
	v_and_b32_e32 v22, 0xffff0000, v22
	v_lshlrev_b32_e32 v61, 16, v23
	v_and_b32_e32 v23, 0xffff0000, v23
	v_lshlrev_b32_e32 v62, 16, v24
	v_and_b32_e32 v24, 0xffff0000, v24
	v_lshlrev_b32_e32 v63, 16, v25
	v_lshlrev_b32_e32 v64, 16, v18
	v_and_b32_e32 v18, 0xffff0000, v18
	v_lshlrev_b32_e32 v66, 16, v20
	v_and_b32_e32 v20, 0xffff0000, v20
	v_mul_f32_e32 v60, v39, v60
	v_mul_f32_e32 v22, v39, v22
	v_mul_f32_e32 v61, v39, v61
	v_mul_f32_e32 v23, v39, v23
	v_mul_f32_e32 v62, v39, v62
	v_mul_f32_e32 v24, v39, v24
	v_mul_f32_e32 v63, v39, v63
	v_mul_f32_e32 v64, v39, v64
	v_mul_f32_e32 v18, v39, v18
	v_mul_f32_e32 v66, v39, v66
	v_mul_f32_e32 v20, v39, v20
	v_and_b32_e32 v25, 0xffff0000, v25
	v_lshlrev_b32_e32 v65, 16, v19
	v_and_b32_e32 v19, 0xffff0000, v19
	v_lshlrev_b32_e32 v67, 16, v21
	v_and_b32_e32 v21, 0xffff0000, v21
	v_mul_f32_e32 v25, v39, v25
	v_mul_f32_e32 v65, v39, v65
	v_mul_f32_e32 v19, v39, v19
	v_mul_f32_e32 v67, v39, v67
	v_mul_f32_e32 v21, v39, v21
	v_mov_b32_e32 v27, s1
	v_lshl_add_u64 v[26:27], v[26:27], 2, s[16:17]
	v_mov_b32_e32 v68, v131
	v_mov_b32_e32 v69, v131
	s_waitcnt vmcnt(3)
	v_mul_f32_e32 v40, v60, v40
	v_mul_f32_e32 v22, v22, v41
	v_mul_f32_e32 v41, v61, v42
	v_mul_f32_e32 v23, v23, v43
	s_waitcnt vmcnt(2)
	v_mul_f32_e32 v42, v62, v44
	v_mul_f32_e32 v24, v24, v45
	v_mul_f32_e32 v43, v63, v46
	s_waitcnt vmcnt(1)
	v_mul_f32_e32 v44, v64, v48
	v_mul_f32_e32 v18, v18, v49
	s_waitcnt vmcnt(0)
	v_mul_f32_e32 v46, v66, v52
	v_mul_f32_e32 v20, v20, v53
	v_med3_f32 v40, v40, s91, v135
	v_med3_f32 v22, v22, s91, v135
	v_med3_f32 v42, v42, s91, v135
	v_med3_f32 v24, v24, s91, v135
	v_med3_f32 v44, v44, s91, v135
	v_med3_f32 v18, v18, s91, v135
	v_med3_f32 v46, v46, s91, v135
	v_med3_f32 v20, v20, s91, v135
	v_cvt_pk_fp8_f32 v56, v40, v22
	v_cvt_pk_fp8_f32 v58, v44, v18
	v_cvt_pk_fp8_f32 v57, v42, v24
	v_cvt_pk_fp8_f32 v59, v46, v20
	v_mul_f32_e32 v25, v25, v47
	v_mul_f32_e32 v45, v65, v50
	v_mul_f32_e32 v19, v19, v51
	v_mul_f32_e32 v47, v67, v54
	v_mul_f32_e32 v21, v21, v55
	v_med3_f32 v41, v41, s91, v135
	v_med3_f32 v23, v23, s91, v135
	v_med3_f32 v43, v43, s91, v135
	v_med3_f32 v25, v25, s91, v135
	v_med3_f32 v45, v45, s91, v135
	v_med3_f32 v19, v19, s91, v135
	v_med3_f32 v47, v47, s91, v135
	v_med3_f32 v21, v21, s91, v135
	v_cvt_pk_fp8_f32 v56, v41, v23 op_sel:[0,0,1]
	v_cvt_pk_fp8_f32 v58, v45, v19 op_sel:[0,0,1]
	v_cvt_pk_fp8_f32 v57, v43, v25 op_sel:[0,0,1]
	v_cvt_pk_fp8_f32 v59, v47, v21 op_sel:[0,0,1]
	v_lshlrev_b32_e32 v52, 16, v14
	v_permlane32_swap_b32_e32 v56, v58
	v_permlane32_swap_b32_e32 v57, v59
	global_store_dwordx4 v[36:37], v[56:59], off offset:32
	global_load_dwordx4 v[18:21], v[26:27], off offset:256
	global_load_dwordx4 v[22:25], v[26:27], off offset:272
	global_load_dwordx4 v[40:43], v[26:27], off offset:320
	global_load_dwordx4 v[44:47], v[26:27], off offset:336
	v_and_b32_e32 v14, 0xffff0000, v14
	v_lshlrev_b32_e32 v53, 16, v15
	v_and_b32_e32 v15, 0xffff0000, v15
	v_lshlrev_b32_e32 v54, 16, v16
	v_and_b32_e32 v16, 0xffff0000, v16
	v_lshlrev_b32_e32 v55, 16, v17
	v_lshlrev_b32_e32 v56, 16, v10
	v_and_b32_e32 v10, 0xffff0000, v10
	v_lshlrev_b32_e32 v58, 16, v12
	v_and_b32_e32 v12, 0xffff0000, v12
	v_mul_f32_e32 v52, v39, v52
	v_mul_f32_e32 v14, v39, v14
	v_mul_f32_e32 v53, v39, v53
	v_mul_f32_e32 v15, v39, v15
	v_mul_f32_e32 v54, v39, v54
	v_mul_f32_e32 v16, v39, v16
	v_mul_f32_e32 v55, v39, v55
	v_mul_f32_e32 v56, v39, v56
	v_mul_f32_e32 v10, v39, v10
	v_mul_f32_e32 v58, v39, v58
	v_mul_f32_e32 v12, v39, v12
	v_and_b32_e32 v17, 0xffff0000, v17
	v_lshlrev_b32_e32 v57, 16, v11
	v_and_b32_e32 v11, 0xffff0000, v11
	v_lshlrev_b32_e32 v59, 16, v13
	v_and_b32_e32 v13, 0xffff0000, v13
	v_mul_f32_e32 v17, v39, v17
	v_mul_f32_e32 v57, v39, v57
	v_mul_f32_e32 v11, v39, v11
	v_mul_f32_e32 v59, v39, v59
	v_mul_f32_e32 v13, v39, v13
	v_mov_b32_e32 v66, v131
	v_mov_b32_e32 v67, v131
	s_waitcnt vmcnt(3)
	v_mul_f32_e32 v18, v52, v18
	v_mul_f32_e32 v14, v14, v19
	v_mul_f32_e32 v19, v53, v20
	v_mul_f32_e32 v15, v15, v21
	s_waitcnt vmcnt(2)
	v_mul_f32_e32 v20, v54, v22
	v_mul_f32_e32 v16, v16, v23
	v_mul_f32_e32 v21, v55, v24
	s_waitcnt vmcnt(1)
; __device__ __forceinline__ float sat8(float x) { return __builtin_amdgcn_fmed3f(x, -448.0f, 448.0f); }
; __device__ __forceinline__ unsigned pk4_fp8(float a, float b, float c, float d) { int v = 0; v = __builtin_amdgcn_cvt_pk_fp8_f32(a, b, v, false); v = __builtin_amdgcn_cvt_pk_fp8_f32(c, d, v, true); return (unsigned)v; }
; __device__ __forceinline__ void phase_attn(const Params& p, LAS unsigned char* lds, int G) {
;     ...
;             for (int qt = 0; qt < 4; ++qt) {
;                 const size_t tok = (size_t)b * SEQ + n * 128 + qt * 32 + r;
;                 float tot = 0.f;
; #pragma unroll
;                 for (int hd = 0; hd < 16; ++hd) tot += ssqp[hd * 128 + qt * 32 + r];
;                 const float rstd = rsqrtf(tot * (1.f / 1024.f) + EPS);
;     ...
; #pragma unroll
;                 for (int hsel = 0; hsel < 2; ++hsel)
; #pragma unroll
;                     for (int dt = 0; dt < 2; ++dt) { unsigned fa[2], fb[2]; const float rs = rstd * FP8_SA;
; #pragma unroll
;                         for (int pp = 0; pp < 2; ++pp) { const int col = (hk * 8 + wl * 2 + hsel) * 64 + dt * 32 + 16 * pp + 8 * hf;
;                             const v4u u = uu[hsel][dt][pp]; const f32x4 w0 = *(const f32x4*)(p.attn_out_norm_w + col), w1 = *(const f32x4*)(p.attn_out_norm_w + col + 4);
;                             const unsigned d0 = pk4_fp8(sat8(bflo(u.x) * rs * w0[0]), sat8(bfhi(u.x) * rs * w0[1]), sat8(bflo(u.y) * rs * w0[2]), sat8(bfhi(u.y) * rs * w0[3]));
;                             const unsigned d1 = pk4_fp8(sat8(bflo(u.z) * rs * w1[0]), sat8(bfhi(u.z) * rs * w1[1]), sat8(bflo(u.w) * rs * w1[2]), sat8(bfhi(u.w) * rs * w1[3]));
;                             if (pp == 0) { fa[0] = d0; fa[1] = d1; } else { fb[0] = d0; fb[1] = d1; } }
;                         const v2u r0 = __builtin_amdgcn_permlane32_swap(fa[0], fb[0], false, false), r1 = __builtin_amdgcn_permlane32_swap(fa[1], fb[1], false, false);
;                         *(v4u*)((unsigned char*)mix + tok * 2048 + (hk * 8 + wl * 2 + hsel) * 64 + dt * 32 + 16 * hf) = (v4u){r0.x, r1.x, r0.y, r1.y}; }
	v_mul_f32_e32 v22, v56, v40
	v_mul_f32_e32 v10, v10, v41
	s_waitcnt vmcnt(0)
	v_mul_f32_e32 v24, v58, v44
	v_mul_f32_e32 v12, v12, v45
	v_med3_f32 v18, v18, s91, v135
	v_med3_f32 v14, v14, s91, v135
	v_med3_f32 v20, v20, s91, v135
	v_med3_f32 v16, v16, s91, v135
	v_med3_f32 v22, v22, s91, v135
	v_med3_f32 v10, v10, s91, v135
	v_med3_f32 v24, v24, s91, v135
	v_med3_f32 v12, v12, s91, v135
	v_cvt_pk_fp8_f32 v48, v18, v14
	v_cvt_pk_fp8_f32 v50, v22, v10
	v_cvt_pk_fp8_f32 v49, v20, v16
	v_cvt_pk_fp8_f32 v51, v24, v12
	v_mul_f32_e32 v17, v17, v25
	v_mul_f32_e32 v23, v57, v42
	v_mul_f32_e32 v11, v11, v43
	v_mul_f32_e32 v25, v59, v46
	v_mul_f32_e32 v13, v13, v47
	v_med3_f32 v19, v19, s91, v135
	v_med3_f32 v15, v15, s91, v135
	v_med3_f32 v21, v21, s91, v135
	v_med3_f32 v17, v17, s91, v135
	v_med3_f32 v23, v23, s91, v135
	v_med3_f32 v11, v11, s91, v135
	v_med3_f32 v25, v25, s91, v135
	v_med3_f32 v13, v13, s91, v135
	v_cvt_pk_fp8_f32 v48, v19, v15 op_sel:[0,0,1]
	v_cvt_pk_fp8_f32 v50, v23, v11 op_sel:[0,0,1]
	v_cvt_pk_fp8_f32 v49, v21, v17 op_sel:[0,0,1]
	v_cvt_pk_fp8_f32 v51, v25, v13 op_sel:[0,0,1]
	v_mov_b32_e32 v45, s71
	v_permlane32_swap_b32_e32 v48, v50
	v_permlane32_swap_b32_e32 v49, v51
	global_store_dwordx4 v[36:37], v[48:51], off offset:64
	global_load_dwordx4 v[10:13], v[26:27], off offset:384
	global_load_dwordx4 v[14:17], v[26:27], off offset:400
	global_load_dwordx4 v[18:21], v[26:27], off offset:448
	global_load_dwordx4 v[22:25], v[26:27], off offset:464
	v_or_b32_e32 v44, 32, v34
	v_lshlrev_b64 v[70:71], 11, v[44:45]
	v_lshl_add_u64 v[44:45], v[32:33], 0, v[70:71]
	v_lshl_add_u64 v[50:51], v[44:45], 0, s[4:5]
	v_lshlrev_b32_e32 v44, 16, v6
	v_and_b32_e32 v6, 0xffff0000, v6
	v_lshlrev_b32_e32 v45, 16, v7
	v_and_b32_e32 v7, 0xffff0000, v7
	v_lshlrev_b32_e32 v46, 16, v8
	v_and_b32_e32 v8, 0xffff0000, v8
	v_lshlrev_b32_e32 v47, 16, v9
	v_lshlrev_b32_e32 v48, 16, v2
	v_and_b32_e32 v2, 0xffff0000, v2
	v_lshlrev_b32_e32 v52, 16, v4
	v_and_b32_e32 v4, 0xffff0000, v4
	v_mul_f32_e32 v44, v39, v44
	v_mul_f32_e32 v6, v39, v6
	v_mul_f32_e32 v45, v39, v45
	v_mul_f32_e32 v7, v39, v7
	v_mul_f32_e32 v46, v39, v46
	v_mul_f32_e32 v8, v39, v8
	v_mul_f32_e32 v47, v39, v47
	v_mul_f32_e32 v48, v39, v48
	v_mul_f32_e32 v2, v39, v2
	v_mul_f32_e32 v52, v39, v52
	v_mul_f32_e32 v4, v39, v4
	v_and_b32_e32 v9, 0xffff0000, v9
	v_lshlrev_b32_e32 v49, 16, v3
	v_and_b32_e32 v3, 0xffff0000, v3
	v_lshlrev_b32_e32 v53, 16, v5
	v_and_b32_e32 v5, 0xffff0000, v5
	v_mul_f32_e32 v9, v39, v9
	v_mul_f32_e32 v49, v39, v49
	v_mul_f32_e32 v3, v39, v3
	v_mul_f32_e32 v53, v39, v53
	v_mul_f32_e32 v5, v39, v5
	v_add_u32_e32 v39, 0x80, v38
	s_waitcnt vmcnt(3)
	v_mul_f32_e32 v10, v44, v10
	v_mul_f32_e32 v6, v6, v11
	v_mul_f32_e32 v11, v45, v12
	v_mul_f32_e32 v7, v7, v13
	s_waitcnt vmcnt(2)
	v_mul_f32_e32 v12, v46, v14
	v_mul_f32_e32 v8, v8, v15
	v_mul_f32_e32 v13, v47, v16
	s_waitcnt vmcnt(1)
	v_mul_f32_e32 v14, v48, v18
	v_mul_f32_e32 v2, v2, v19
	s_waitcnt vmcnt(0)
	v_mul_f32_e32 v16, v52, v22
	v_mul_f32_e32 v4, v4, v23
	v_med3_f32 v10, v10, s91, v135
	v_med3_f32 v6, v6, s91, v135
	v_med3_f32 v12, v12, s91, v135
	v_med3_f32 v8, v8, s91, v135
	v_med3_f32 v14, v14, s91, v135
	v_med3_f32 v2, v2, s91, v135
	v_med3_f32 v16, v16, s91, v135
	v_med3_f32 v4, v4, s91, v135
	v_cvt_pk_fp8_f32 v40, v10, v6
	v_cvt_pk_fp8_f32 v42, v14, v2
	v_cvt_pk_fp8_f32 v41, v12, v8
	v_cvt_pk_fp8_f32 v43, v16, v4
	v_mul_f32_e32 v9, v9, v17
	v_mul_f32_e32 v15, v49, v20
	v_mul_f32_e32 v3, v3, v21
	v_mul_f32_e32 v17, v53, v24
	v_mul_f32_e32 v5, v5, v25
	v_med3_f32 v11, v11, s91, v135
	v_med3_f32 v7, v7, s91, v135
	v_med3_f32 v13, v13, s91, v135
	v_med3_f32 v9, v9, s91, v135
	v_med3_f32 v15, v15, s91, v135
	v_med3_f32 v3, v3, s91, v135
	v_med3_f32 v17, v17, s91, v135
	v_med3_f32 v5, v5, s91, v135
	v_cvt_pk_fp8_f32 v40, v11, v7 op_sel:[0,0,1]
	v_cvt_pk_fp8_f32 v42, v15, v3 op_sel:[0,0,1]
	v_cvt_pk_fp8_f32 v41, v13, v9 op_sel:[0,0,1]
	v_cvt_pk_fp8_f32 v43, v17, v5 op_sel:[0,0,1]
	v_permlane32_swap_b32_e32 v40, v42
	s_nop 0
	v_permlane32_swap_b32_e32 v41, v43
	global_store_dwordx4 v[36:37], v[40:43], off offset:96
	global_load_dwordx4 v[42:45], v[50:51], off
	s_nop 0
	global_load_dwordx4 v[46:49], v[50:51], off offset:32
	global_load_dwordx4 v[22:25], v[50:51], off offset:64
	global_load_dwordx4 v[18:21], v[50:51], off offset:96
	global_load_dwordx4 v[14:17], v[50:51], off offset:128
	global_load_dwordx4 v[10:13], v[50:51], off offset:160
	global_load_dwordx4 v[6:9], v[50:51], off offset:192
	global_load_dwordx4 v[2:5], v[50:51], off offset:224
	ds_read2_b32 v[36:37], v38 offset0:32 offset1:160
	ds_read2st64_b32 v[40:41], v39 offset0:4 offset1:6
	ds_read2st64_b32 v[72:73], v39 offset0:8 offset1:10
	ds_read2st64_b32 v[74:75], v39 offset0:12 offset1:14
	ds_read2st64_b32 v[76:77], v39 offset0:16 offset1:18
	ds_read2st64_b32 v[78:79], v39 offset0:20 offset1:22
	ds_read2st64_b32 v[80:81], v39 offset0:24 offset1:26
	ds_read2st64_b32 v[82:83], v39 offset0:28 offset1:30
	s_waitcnt vmcnt(6)
	s_waitcnt vmcnt(4)
	s_waitcnt vmcnt(2)
	s_waitcnt vmcnt(0)
	global_load_dwordx4 v[50:53], v[28:29], off
	global_load_dwordx4 v[54:57], v[28:29], off offset:16
	global_load_dwordx4 v[58:61], v[28:29], off offset:64
	global_load_dwordx4 v[62:65], v[28:29], off offset:80
	s_waitcnt lgkmcnt(7)
	v_add_f32_e32 v36, 0, v36
	v_add_f32_e32 v36, v36, v37
	s_waitcnt lgkmcnt(6)
	v_add_f32_e32 v36, v36, v40
	v_add_f32_e32 v36, v36, v41
	s_waitcnt lgkmcnt(5)
	v_add_f32_e32 v36, v36, v72
	v_add_f32_e32 v36, v36, v73
	s_waitcnt lgkmcnt(4)
	v_add_f32_e32 v36, v36, v74
	v_add_f32_e32 v36, v36, v75
	s_waitcnt lgkmcnt(3)
; __device__ __forceinline__ void phase_attn(const Params& p, LAS unsigned char* lds, int G) {
;     ...
;             for (int qt = 0; qt < 4; ++qt) {
;                 const size_t tok = (size_t)b * SEQ + n * 128 + qt * 32 + r;
;                 float tot = 0.f;
; #pragma unroll
;                 for (int hd = 0; hd < 16; ++hd) tot += ssqp[hd * 128 + qt * 32 + r];
;                 const float rstd = rsqrtf(tot * (1.f / 1024.f) + EPS);
;                 v4u uu[2][2][2];
; #pragma unroll
;                 for (int hsel = 0; hsel < 2; ++hsel)
; #pragma unroll
;                     for (int dt = 0; dt < 2; ++dt)
; #pragma unroll
;                         for (int pp = 0; pp < 2; ++pp) uu[hsel][dt][pp] = *(const v4u*)(att + tok * ALD + (hk * 8 + wl * 2 + hsel) * 64 + dt * 32 + 16 * pp + 8 * hf);
; #pragma unroll
;                 for (int hsel = 0; hsel < 2; ++hsel)
; #pragma unroll
;                     for (int dt = 0; dt < 2; ++dt) { asm volatile("" : "+v"(uu[hsel][dt][0]), "+v"(uu[hsel][dt][1])); }
;     ...
; #pragma unroll
;                 for (int hsel = 0; hsel < 2; ++hsel)
; #pragma unroll
;                     for (int dt = 0; dt < 2; ++dt) { unsigned fa[2], fb[2]; const float rs = rstd * FP8_SA;
; #pragma unroll
;                         for (int pp = 0; pp < 2; ++pp) { const int col = (hk * 8 + wl * 2 + hsel) * 64 + dt * 32 + 16 * pp + 8 * hf;
;                             const v4u u = uu[hsel][dt][pp]; const f32x4 w0 = *(const f32x4*)(p.attn_out_norm_w + col), w1 = *(const f32x4*)(p.attn_out_norm_w + col + 4);
;                             const unsigned d0 = pk4_fp8(sat8(bflo(u.x) * rs * w0[0]), sat8(bfhi(u.x) * rs * w0[1]), sat8(bflo(u.y) * rs * w0[2]), sat8(bfhi(u.y) * rs * w0[3]));
;                             const unsigned d1 = pk4_fp8(sat8(bflo(u.z) * rs * w1[0]), sat8(bfhi(u.z) * rs * w1[1]), sat8(bflo(u.w) * rs * w1[2]), sat8(bfhi(u.w) * rs * w1[3]));
;                             if (pp == 0) { fa[0] = d0; fa[1] = d1; } else { fb[0] = d0; fb[1] = d1; } }
;                         const v2u r0 = __builtin_amdgcn_permlane32_swap(fa[0], fb[0], false, false), r1 = __builtin_amdgcn_permlane32_swap(fa[1], fb[1], false, false);
;                         *(v4u*)((unsigned char*)mix + tok * 2048 + (hk * 8 + wl * 2 + hsel) * 64 + dt * 32 + 16 * hf) = (v4u){r0.x, r1.x, r0.y, r1.y}; }
	v_add_f32_e32 v36, v36, v76
	v_add_f32_e32 v36, v36, v77
	s_waitcnt lgkmcnt(2)
	v_add_f32_e32 v36, v36, v78
	v_add_f32_e32 v36, v36, v79
	s_waitcnt lgkmcnt(1)
	v_add_f32_e32 v36, v36, v80
	v_add_f32_e32 v36, v36, v81
	s_waitcnt lgkmcnt(0)
	v_add_f32_e32 v36, v36, v82
	v_add_f32_e32 v36, v36, v83
	v_fmamk_f32 v36, v36, 0x3a800000, v1
	v_mul_f32_e32 v37, 0x4b800000, v36
	v_cmp_gt_f32_e32 vcc, s43, v36
	v_lshlrev_b32_e32 v73, 16, v46
	v_and_b32_e32 v46, 0xffff0000, v46
	v_cndmask_b32_e32 v36, v36, v37, vcc
	v_rsq_f32_e32 v40, v36
	v_lshl_add_u64 v[36:37], v[30:31], 0, v[70:71]
	v_lshlrev_b32_e32 v70, 16, v43
	v_and_b32_e32 v43, 0xffff0000, v43
	v_mul_f32_e32 v41, 0x45800000, v40
	v_cndmask_b32_e32 v40, v40, v41, vcc
	v_mul_f32_e32 v40, 0x41800000, v40
	v_lshlrev_b32_e32 v41, 16, v42
	v_and_b32_e32 v42, 0xffff0000, v42
	v_lshlrev_b32_e32 v71, 16, v44
	v_and_b32_e32 v44, 0xffff0000, v44
	v_lshlrev_b32_e32 v75, 16, v48
	v_and_b32_e32 v48, 0xffff0000, v48
	v_mul_f32_e32 v41, v40, v41
	v_mul_f32_e32 v42, v40, v42
	v_mul_f32_e32 v43, v40, v43
	v_mul_f32_e32 v71, v40, v71
	v_mul_f32_e32 v44, v40, v44
	v_mul_f32_e32 v73, v40, v73
	v_mul_f32_e32 v46, v40, v46
	v_mul_f32_e32 v75, v40, v75
	v_mul_f32_e32 v48, v40, v48
	v_lshlrev_b32_e32 v72, 16, v45
	v_and_b32_e32 v45, 0xffff0000, v45
	v_lshlrev_b32_e32 v74, 16, v47
	v_and_b32_e32 v47, 0xffff0000, v47
	v_lshlrev_b32_e32 v76, 16, v49
	v_and_b32_e32 v49, 0xffff0000, v49
	v_mul_f32_e32 v70, v40, v70
	v_mul_f32_e32 v72, v40, v72
	v_mul_f32_e32 v45, v40, v45
	v_mul_f32_e32 v74, v40, v74
	v_mul_f32_e32 v47, v40, v47
	v_mul_f32_e32 v76, v40, v76
	v_mul_f32_e32 v49, v40, v49
	v_lshl_add_u64 v[36:37], v[36:37], 0, s[0:1]
	s_waitcnt vmcnt(3)
	v_mul_f32_e32 v41, v50, v41
	v_mul_f32_e32 v42, v51, v42
	v_mul_f32_e32 v43, v53, v43
	s_waitcnt vmcnt(2)
	v_mul_f32_e32 v51, v71, v54
	v_mul_f32_e32 v44, v44, v55
	s_waitcnt vmcnt(1)
	v_mul_f32_e32 v53, v73, v58
	v_mul_f32_e32 v46, v46, v59
	s_waitcnt vmcnt(0)
	v_mul_f32_e32 v55, v75, v62
	v_mul_f32_e32 v48, v48, v63
	v_med3_f32 v41, v41, s91, v135
	v_med3_f32 v42, v42, s91, v135
	v_med3_f32 v51, v51, s91, v135
	v_med3_f32 v44, v44, s91, v135
	v_med3_f32 v53, v53, s91, v135
	v_med3_f32 v46, v46, s91, v135
	v_med3_f32 v55, v55, s91, v135
	v_med3_f32 v48, v48, s91, v135
	v_cvt_pk_fp8_f32 v66, v41, v42
	v_cvt_pk_fp8_f32 v68, v53, v46
	v_cvt_pk_fp8_f32 v67, v51, v44
	v_cvt_pk_fp8_f32 v69, v55, v48
	v_mul_f32_e32 v50, v52, v70
	v_mul_f32_e32 v52, v72, v56
	v_mul_f32_e32 v45, v45, v57
	v_mul_f32_e32 v54, v74, v60
	v_mul_f32_e32 v47, v47, v61
	v_mul_f32_e32 v56, v76, v64
	v_mul_f32_e32 v49, v49, v65
	v_med3_f32 v50, v50, s91, v135
	v_med3_f32 v43, v43, s91, v135
	v_med3_f32 v52, v52, s91, v135
	v_med3_f32 v45, v45, s91, v135
	v_med3_f32 v54, v54, s91, v135
	v_med3_f32 v47, v47, s91, v135
	v_med3_f32 v56, v56, s91, v135
	v_med3_f32 v49, v49, s91, v135
	v_cvt_pk_fp8_f32 v66, v50, v43 op_sel:[0,0,1]
	v_cvt_pk_fp8_f32 v68, v54, v47 op_sel:[0,0,1]
	v_cvt_pk_fp8_f32 v67, v52, v45 op_sel:[0,0,1]
	v_cvt_pk_fp8_f32 v69, v56, v49 op_sel:[0,0,1]
	v_lshlrev_b32_e32 v41, 16, v22
	v_permlane32_swap_b32_e32 v66, v68
	v_permlane32_swap_b32_e32 v67, v69
	global_store_dwordx4 v[36:37], v[66:69], off
	global_load_dwordx4 v[42:45], v[28:29], off offset:128
	global_load_dwordx4 v[46:49], v[28:29], off offset:144
	global_load_dwordx4 v[50:53], v[28:29], off offset:192
	global_load_dwordx4 v[54:57], v[28:29], off offset:208
	v_and_b32_e32 v22, 0xffff0000, v22
	v_lshlrev_b32_e32 v62, 16, v23
	v_and_b32_e32 v23, 0xffff0000, v23
	v_lshlrev_b32_e32 v63, 16, v24
	v_and_b32_e32 v24, 0xffff0000, v24
	v_lshlrev_b32_e32 v65, 16, v18
	v_and_b32_e32 v18, 0xffff0000, v18
	v_lshlrev_b32_e32 v67, 16, v20
	v_and_b32_e32 v20, 0xffff0000, v20
	v_mul_f32_e32 v41, v40, v41
	v_mul_f32_e32 v22, v40, v22
	v_mul_f32_e32 v23, v40, v23
	v_mul_f32_e32 v63, v40, v63
	v_mul_f32_e32 v24, v40, v24
	v_mul_f32_e32 v65, v40, v65
	v_mul_f32_e32 v18, v40, v18
	v_mul_f32_e32 v67, v40, v67
	v_mul_f32_e32 v20, v40, v20
	v_lshlrev_b32_e32 v64, 16, v25
	v_and_b32_e32 v25, 0xffff0000, v25
	v_lshlrev_b32_e32 v66, 16, v19
	v_and_b32_e32 v19, 0xffff0000, v19
	v_lshlrev_b32_e32 v68, 16, v21
	v_and_b32_e32 v21, 0xffff0000, v21
	v_mul_f32_e32 v62, v40, v62
	v_mul_f32_e32 v64, v40, v64
	v_mul_f32_e32 v25, v40, v25
	v_mul_f32_e32 v66, v40, v66
	v_mul_f32_e32 v19, v40, v19
	v_mul_f32_e32 v68, v40, v68
	v_mul_f32_e32 v21, v40, v21
	v_mov_b32_e32 v69, v131
	s_waitcnt vmcnt(3)
	v_mul_f32_e32 v41, v41, v42
	v_mul_f32_e32 v22, v22, v43
	v_mul_f32_e32 v23, v23, v45
	s_waitcnt vmcnt(2)
	v_mul_f32_e32 v43, v63, v46
	v_mul_f32_e32 v24, v24, v47
	s_waitcnt vmcnt(1)
	v_mul_f32_e32 v45, v65, v50
	v_mul_f32_e32 v18, v18, v51
	s_waitcnt vmcnt(0)
; __device__ __forceinline__ float sat8(float x) { return __builtin_amdgcn_fmed3f(x, -448.0f, 448.0f); }
; __device__ __forceinline__ unsigned pk4_fp8(float a, float b, float c, float d) { int v = 0; v = __builtin_amdgcn_cvt_pk_fp8_f32(a, b, v, false); v = __builtin_amdgcn_cvt_pk_fp8_f32(c, d, v, true); return (unsigned)v; }
; __device__ __forceinline__ void phase_attn(const Params& p, LAS unsigned char* lds, int G) {
;     ...
; #pragma unroll
;                 for (int hsel = 0; hsel < 2; ++hsel)
; #pragma unroll
;                     for (int dt = 0; dt < 2; ++dt) { unsigned fa[2], fb[2]; const float rs = rstd * FP8_SA;
; #pragma unroll
;                         for (int pp = 0; pp < 2; ++pp) { const int col = (hk * 8 + wl * 2 + hsel) * 64 + dt * 32 + 16 * pp + 8 * hf;
;                             const v4u u = uu[hsel][dt][pp]; const f32x4 w0 = *(const f32x4*)(p.attn_out_norm_w + col), w1 = *(const f32x4*)(p.attn_out_norm_w + col + 4);
;                             const unsigned d0 = pk4_fp8(sat8(bflo(u.x) * rs * w0[0]), sat8(bfhi(u.x) * rs * w0[1]), sat8(bflo(u.y) * rs * w0[2]), sat8(bfhi(u.y) * rs * w0[3]));
;                             const unsigned d1 = pk4_fp8(sat8(bflo(u.z) * rs * w1[0]), sat8(bfhi(u.z) * rs * w1[1]), sat8(bflo(u.w) * rs * w1[2]), sat8(bfhi(u.w) * rs * w1[3]));
;                             if (pp == 0) { fa[0] = d0; fa[1] = d1; } else { fb[0] = d0; fb[1] = d1; } }
;                         const v2u r0 = __builtin_amdgcn_permlane32_swap(fa[0], fb[0], false, false), r1 = __builtin_amdgcn_permlane32_swap(fa[1], fb[1], false, false);
;                         *(v4u*)((unsigned char*)mix + tok * 2048 + (hk * 8 + wl * 2 + hsel) * 64 + dt * 32 + 16 * hf) = (v4u){r0.x, r1.x, r0.y, r1.y}; }
	v_mul_f32_e32 v47, v67, v54
	v_mul_f32_e32 v20, v20, v55
	v_med3_f32 v41, v41, s91, v135
	v_med3_f32 v22, v22, s91, v135
	v_med3_f32 v43, v43, s91, v135
	v_med3_f32 v24, v24, s91, v135
	v_med3_f32 v45, v45, s91, v135
	v_med3_f32 v18, v18, s91, v135
	v_med3_f32 v47, v47, s91, v135
	v_med3_f32 v20, v20, s91, v135
	v_cvt_pk_fp8_f32 v58, v41, v22
	v_cvt_pk_fp8_f32 v60, v45, v18
	v_cvt_pk_fp8_f32 v59, v43, v24
	v_cvt_pk_fp8_f32 v61, v47, v20
	v_mul_f32_e32 v42, v62, v44
	v_mul_f32_e32 v44, v64, v48
	v_mul_f32_e32 v25, v25, v49
	v_mul_f32_e32 v46, v66, v52
	v_mul_f32_e32 v19, v19, v53
	v_mul_f32_e32 v48, v68, v56
	v_mul_f32_e32 v21, v21, v57
	v_med3_f32 v42, v42, s91, v135
	v_med3_f32 v23, v23, s91, v135
	v_med3_f32 v44, v44, s91, v135
	v_med3_f32 v25, v25, s91, v135
	v_med3_f32 v46, v46, s91, v135
	v_med3_f32 v19, v19, s91, v135
	v_med3_f32 v48, v48, s91, v135
	v_med3_f32 v21, v21, s91, v135
	v_cvt_pk_fp8_f32 v58, v42, v23 op_sel:[0,0,1]
	v_cvt_pk_fp8_f32 v60, v46, v19 op_sel:[0,0,1]
	v_cvt_pk_fp8_f32 v59, v44, v25 op_sel:[0,0,1]
	v_cvt_pk_fp8_f32 v61, v48, v21 op_sel:[0,0,1]
	v_lshlrev_b32_e32 v41, 16, v14
	v_permlane32_swap_b32_e32 v58, v60
	v_permlane32_swap_b32_e32 v59, v61
	global_store_dwordx4 v[36:37], v[58:61], off offset:32
	global_load_dwordx4 v[18:21], v[26:27], off offset:256
	global_load_dwordx4 v[22:25], v[26:27], off offset:272
	global_load_dwordx4 v[42:45], v[26:27], off offset:320
	global_load_dwordx4 v[46:49], v[26:27], off offset:336
	v_and_b32_e32 v14, 0xffff0000, v14
	v_lshlrev_b32_e32 v54, 16, v15
	v_and_b32_e32 v15, 0xffff0000, v15
	v_lshlrev_b32_e32 v55, 16, v16
	v_and_b32_e32 v16, 0xffff0000, v16
	v_lshlrev_b32_e32 v56, 16, v17
	v_lshlrev_b32_e32 v57, 16, v10
	v_and_b32_e32 v10, 0xffff0000, v10
	v_lshlrev_b32_e32 v59, 16, v12
	v_and_b32_e32 v12, 0xffff0000, v12
	v_mul_f32_e32 v41, v40, v41
	v_mul_f32_e32 v14, v40, v14
	v_mul_f32_e32 v54, v40, v54
	v_mul_f32_e32 v15, v40, v15
	v_mul_f32_e32 v55, v40, v55
	v_mul_f32_e32 v16, v40, v16
	v_mul_f32_e32 v56, v40, v56
	v_mul_f32_e32 v57, v40, v57
	v_mul_f32_e32 v10, v40, v10
	v_mul_f32_e32 v59, v40, v59
	v_mul_f32_e32 v12, v40, v12
	v_and_b32_e32 v17, 0xffff0000, v17
	v_lshlrev_b32_e32 v58, 16, v11
	v_and_b32_e32 v11, 0xffff0000, v11
	v_lshlrev_b32_e32 v60, 16, v13
	v_and_b32_e32 v13, 0xffff0000, v13
	v_mul_f32_e32 v17, v40, v17
	v_mul_f32_e32 v58, v40, v58
	v_mul_f32_e32 v11, v40, v11
	v_mul_f32_e32 v60, v40, v60
	v_mul_f32_e32 v13, v40, v13
	v_mov_b32_e32 v66, v131
	v_mov_b32_e32 v67, v131
	v_mov_b32_e32 v68, v131
	s_waitcnt vmcnt(3)
	v_mul_f32_e32 v18, v41, v18
	v_mul_f32_e32 v14, v14, v19
	v_mul_f32_e32 v19, v54, v20
	v_mul_f32_e32 v15, v15, v21
	s_waitcnt vmcnt(2)
	v_mul_f32_e32 v20, v55, v22
	v_mul_f32_e32 v16, v16, v23
	v_mul_f32_e32 v21, v56, v24
	s_waitcnt vmcnt(1)
	v_mul_f32_e32 v22, v57, v42
	v_mul_f32_e32 v10, v10, v43
	s_waitcnt vmcnt(0)
	v_mul_f32_e32 v24, v59, v46
	v_mul_f32_e32 v12, v12, v47
	v_med3_f32 v18, v18, s91, v135
	v_med3_f32 v14, v14, s91, v135
	v_med3_f32 v20, v20, s91, v135
	v_med3_f32 v16, v16, s91, v135
	v_med3_f32 v22, v22, s91, v135
	v_med3_f32 v10, v10, s91, v135
	v_med3_f32 v24, v24, s91, v135
	v_med3_f32 v12, v12, s91, v135
	v_cvt_pk_fp8_f32 v50, v18, v14
	v_cvt_pk_fp8_f32 v52, v22, v10
	v_cvt_pk_fp8_f32 v51, v20, v16
	v_cvt_pk_fp8_f32 v53, v24, v12
	v_mul_f32_e32 v17, v17, v25
	v_mul_f32_e32 v23, v58, v44
	v_mul_f32_e32 v11, v11, v45
	v_mul_f32_e32 v25, v60, v48
	v_mul_f32_e32 v13, v13, v49
	v_med3_f32 v19, v19, s91, v135
	v_med3_f32 v15, v15, s91, v135
	v_med3_f32 v21, v21, s91, v135
	v_med3_f32 v17, v17, s91, v135
	v_med3_f32 v23, v23, s91, v135
	v_med3_f32 v11, v11, s91, v135
	v_med3_f32 v25, v25, s91, v135
	v_med3_f32 v13, v13, s91, v135
	v_cvt_pk_fp8_f32 v50, v19, v15 op_sel:[0,0,1]
	v_cvt_pk_fp8_f32 v52, v23, v11 op_sel:[0,0,1]
	v_cvt_pk_fp8_f32 v51, v21, v17 op_sel:[0,0,1]
	v_cvt_pk_fp8_f32 v53, v25, v13 op_sel:[0,0,1]
	v_mov_b32_e32 v47, s71
	v_permlane32_swap_b32_e32 v50, v52
	v_permlane32_swap_b32_e32 v51, v53
	global_store_dwordx4 v[36:37], v[50:53], off offset:64
	global_load_dwordx4 v[10:13], v[26:27], off offset:384
	global_load_dwordx4 v[14:17], v[26:27], off offset:400
	global_load_dwordx4 v[18:21], v[26:27], off offset:448
	global_load_dwordx4 v[22:25], v[26:27], off offset:464
	v_or_b32_e32 v46, 64, v34
	v_lshlrev_b64 v[70:71], 11, v[46:47]
	v_lshl_add_u64 v[46:47], v[32:33], 0, v[70:71]
	v_lshl_add_u64 v[50:51], v[46:47], 0, s[4:5]
	v_lshlrev_b32_e32 v41, 16, v6
	v_and_b32_e32 v6, 0xffff0000, v6
	v_lshlrev_b32_e32 v46, 16, v7
	v_and_b32_e32 v7, 0xffff0000, v7
	v_lshlrev_b32_e32 v47, 16, v8
	v_and_b32_e32 v8, 0xffff0000, v8
	v_lshlrev_b32_e32 v48, 16, v9
	v_lshlrev_b32_e32 v49, 16, v2
	v_and_b32_e32 v2, 0xffff0000, v2
	v_lshlrev_b32_e32 v53, 16, v4
	v_and_b32_e32 v4, 0xffff0000, v4
	v_mul_f32_e32 v41, v40, v41
	v_mul_f32_e32 v6, v40, v6
	v_mul_f32_e32 v46, v40, v46
	v_mul_f32_e32 v7, v40, v7
	v_mul_f32_e32 v47, v40, v47
	v_mul_f32_e32 v8, v40, v8
	v_mul_f32_e32 v48, v40, v48
	v_mul_f32_e32 v49, v40, v49
	v_mul_f32_e32 v2, v40, v2
	v_mul_f32_e32 v53, v40, v53
	v_mul_f32_e32 v4, v40, v4
	v_and_b32_e32 v9, 0xffff0000, v9
	v_lshlrev_b32_e32 v52, 16, v3
	v_and_b32_e32 v3, 0xffff0000, v3
	v_lshlrev_b32_e32 v54, 16, v5
	v_and_b32_e32 v5, 0xffff0000, v5
	v_mul_f32_e32 v9, v40, v9
	v_mul_f32_e32 v52, v40, v52
	v_mul_f32_e32 v3, v40, v3
	v_mul_f32_e32 v54, v40, v54
	v_mul_f32_e32 v5, v40, v5
	v_or_b32_e32 v34, 0x60, v34
	s_waitcnt vmcnt(3)
	v_mul_f32_e32 v10, v41, v10
	v_mul_f32_e32 v6, v6, v11
	v_mul_f32_e32 v11, v46, v12
	v_mul_f32_e32 v7, v7, v13
	s_waitcnt vmcnt(2)
	v_mul_f32_e32 v12, v47, v14
	v_mul_f32_e32 v8, v8, v15
	v_mul_f32_e32 v13, v48, v16
	s_waitcnt vmcnt(1)
; __device__ __forceinline__ float sat8(float x) { return __builtin_amdgcn_fmed3f(x, -448.0f, 448.0f); }
; __device__ __forceinline__ unsigned pk4_fp8(float a, float b, float c, float d) { int v = 0; v = __builtin_amdgcn_cvt_pk_fp8_f32(a, b, v, false); v = __builtin_amdgcn_cvt_pk_fp8_f32(c, d, v, true); return (unsigned)v; }
; __device__ __forceinline__ void phase_attn(const Params& p, LAS unsigned char* lds, int G) {
;     ...
;             for (int qt = 0; qt < 4; ++qt) {
;                 const size_t tok = (size_t)b * SEQ + n * 128 + qt * 32 + r;
;                 float tot = 0.f;
; #pragma unroll
;                 for (int hd = 0; hd < 16; ++hd) tot += ssqp[hd * 128 + qt * 32 + r];
;                 const float rstd = rsqrtf(tot * (1.f / 1024.f) + EPS);
;     ...
; #pragma unroll
;                 for (int hsel = 0; hsel < 2; ++hsel)
; #pragma unroll
;                     for (int dt = 0; dt < 2; ++dt) { unsigned fa[2], fb[2]; const float rs = rstd * FP8_SA;
; #pragma unroll
;                         for (int pp = 0; pp < 2; ++pp) { const int col = (hk * 8 + wl * 2 + hsel) * 64 + dt * 32 + 16 * pp + 8 * hf;
;                             const v4u u = uu[hsel][dt][pp]; const f32x4 w0 = *(const f32x4*)(p.attn_out_norm_w + col), w1 = *(const f32x4*)(p.attn_out_norm_w + col + 4);
;                             const unsigned d0 = pk4_fp8(sat8(bflo(u.x) * rs * w0[0]), sat8(bfhi(u.x) * rs * w0[1]), sat8(bflo(u.y) * rs * w0[2]), sat8(bfhi(u.y) * rs * w0[3]));
;                             const unsigned d1 = pk4_fp8(sat8(bflo(u.z) * rs * w1[0]), sat8(bfhi(u.z) * rs * w1[1]), sat8(bflo(u.w) * rs * w1[2]), sat8(bfhi(u.w) * rs * w1[3]));
;                             if (pp == 0) { fa[0] = d0; fa[1] = d1; } else { fb[0] = d0; fb[1] = d1; } }
;                         const v2u r0 = __builtin_amdgcn_permlane32_swap(fa[0], fb[0], false, false), r1 = __builtin_amdgcn_permlane32_swap(fa[1], fb[1], false, false);
;                         *(v4u*)((unsigned char*)mix + tok * 2048 + (hk * 8 + wl * 2 + hsel) * 64 + dt * 32 + 16 * hf) = (v4u){r0.x, r1.x, r0.y, r1.y}; }
	v_mul_f32_e32 v14, v49, v18
	v_mul_f32_e32 v2, v2, v19
	s_waitcnt vmcnt(0)
	v_mul_f32_e32 v16, v53, v22
	v_mul_f32_e32 v4, v4, v23
	v_med3_f32 v10, v10, s91, v135
	v_med3_f32 v6, v6, s91, v135
	v_med3_f32 v12, v12, s91, v135
	v_med3_f32 v8, v8, s91, v135
	v_med3_f32 v14, v14, s91, v135
	v_med3_f32 v2, v2, s91, v135
	v_med3_f32 v16, v16, s91, v135
	v_med3_f32 v4, v4, s91, v135
	v_cvt_pk_fp8_f32 v42, v10, v6
	v_cvt_pk_fp8_f32 v44, v14, v2
	v_cvt_pk_fp8_f32 v43, v12, v8
	v_cvt_pk_fp8_f32 v45, v16, v4
	v_mul_f32_e32 v9, v9, v17
	v_mul_f32_e32 v15, v52, v20
	v_mul_f32_e32 v3, v3, v21
	v_mul_f32_e32 v17, v54, v24
	v_mul_f32_e32 v5, v5, v25
	v_med3_f32 v11, v11, s91, v135
	v_med3_f32 v7, v7, s91, v135
	v_med3_f32 v13, v13, s91, v135
	v_med3_f32 v9, v9, s91, v135
	v_med3_f32 v15, v15, s91, v135
	v_med3_f32 v3, v3, s91, v135
	v_med3_f32 v17, v17, s91, v135
	v_med3_f32 v5, v5, s91, v135
	v_cvt_pk_fp8_f32 v42, v11, v7 op_sel:[0,0,1]
	v_cvt_pk_fp8_f32 v44, v15, v3 op_sel:[0,0,1]
	v_cvt_pk_fp8_f32 v43, v13, v9 op_sel:[0,0,1]
	v_cvt_pk_fp8_f32 v45, v17, v5 op_sel:[0,0,1]
	v_permlane32_swap_b32_e32 v42, v44
	s_nop 0
	v_permlane32_swap_b32_e32 v43, v45
	global_store_dwordx4 v[36:37], v[42:45], off offset:96
	global_load_dwordx4 v[42:45], v[50:51], off
	s_nop 0
	global_load_dwordx4 v[46:49], v[50:51], off offset:32
	global_load_dwordx4 v[22:25], v[50:51], off offset:64
	global_load_dwordx4 v[18:21], v[50:51], off offset:96
	global_load_dwordx4 v[14:17], v[50:51], off offset:128
	global_load_dwordx4 v[10:13], v[50:51], off offset:160
	global_load_dwordx4 v[6:9], v[50:51], off offset:192
	global_load_dwordx4 v[2:5], v[50:51], off offset:224
	ds_read2st64_b32 v[36:37], v38 offset0:1 offset1:3
	ds_read2st64_b32 v[40:41], v38 offset0:5 offset1:7
	ds_read2st64_b32 v[72:73], v38 offset0:9 offset1:11
	ds_read2st64_b32 v[74:75], v38 offset0:13 offset1:15
	ds_read2st64_b32 v[76:77], v38 offset0:17 offset1:19
	ds_read2st64_b32 v[78:79], v38 offset0:21 offset1:23
	ds_read2st64_b32 v[80:81], v38 offset0:25 offset1:27
	ds_read2st64_b32 v[82:83], v38 offset0:29 offset1:31
	s_waitcnt vmcnt(6)
	s_waitcnt vmcnt(4)
	s_waitcnt vmcnt(2)
	s_waitcnt vmcnt(0)
	global_load_dwordx4 v[50:53], v[28:29], off
	global_load_dwordx4 v[54:57], v[28:29], off offset:16
	global_load_dwordx4 v[58:61], v[28:29], off offset:64
	global_load_dwordx4 v[62:65], v[28:29], off offset:80
	s_waitcnt lgkmcnt(7)
	v_add_f32_e32 v36, 0, v36
	v_add_f32_e32 v36, v36, v37
	s_waitcnt lgkmcnt(6)
	v_add_f32_e32 v36, v36, v40
	v_add_f32_e32 v36, v36, v41
	s_waitcnt lgkmcnt(5)
	v_add_f32_e32 v36, v36, v72
	v_add_f32_e32 v36, v36, v73
	s_waitcnt lgkmcnt(4)
	v_add_f32_e32 v36, v36, v74
	v_add_f32_e32 v36, v36, v75
	s_waitcnt lgkmcnt(3)
	v_add_f32_e32 v36, v36, v76
	v_add_f32_e32 v36, v36, v77
	s_waitcnt lgkmcnt(2)
	v_add_f32_e32 v36, v36, v78
	v_add_f32_e32 v36, v36, v79
	s_waitcnt lgkmcnt(1)
	v_add_f32_e32 v36, v36, v80
	v_add_f32_e32 v36, v36, v81
	s_waitcnt lgkmcnt(0)
	v_add_f32_e32 v36, v36, v82
	v_add_f32_e32 v36, v36, v83
	v_fmamk_f32 v36, v36, 0x3a800000, v1
	v_mul_f32_e32 v37, 0x4b800000, v36
	v_cmp_gt_f32_e32 vcc, s43, v36
	v_lshlrev_b32_e32 v73, 16, v46
	v_and_b32_e32 v46, 0xffff0000, v46
	v_cndmask_b32_e32 v36, v36, v37, vcc
	v_rsq_f32_e32 v40, v36
	v_lshl_add_u64 v[36:37], v[30:31], 0, v[70:71]
	v_lshlrev_b32_e32 v70, 16, v43
	v_and_b32_e32 v43, 0xffff0000, v43
	v_mul_f32_e32 v41, 0x45800000, v40
	v_cndmask_b32_e32 v40, v40, v41, vcc
	v_mul_f32_e32 v40, 0x41800000, v40
	v_lshlrev_b32_e32 v41, 16, v42
	v_and_b32_e32 v42, 0xffff0000, v42
	v_lshlrev_b32_e32 v71, 16, v44
	v_and_b32_e32 v44, 0xffff0000, v44
	v_lshlrev_b32_e32 v75, 16, v48
	v_and_b32_e32 v48, 0xffff0000, v48
	v_mul_f32_e32 v41, v40, v41
	v_mul_f32_e32 v42, v40, v42
	v_mul_f32_e32 v43, v40, v43
	v_mul_f32_e32 v71, v40, v71
	v_mul_f32_e32 v44, v40, v44
	v_mul_f32_e32 v73, v40, v73
	v_mul_f32_e32 v46, v40, v46
	v_mul_f32_e32 v75, v40, v75
	v_mul_f32_e32 v48, v40, v48
	v_lshlrev_b32_e32 v72, 16, v45
	v_and_b32_e32 v45, 0xffff0000, v45
	v_lshlrev_b32_e32 v74, 16, v47
	v_and_b32_e32 v47, 0xffff0000, v47
	v_lshlrev_b32_e32 v76, 16, v49
	v_and_b32_e32 v49, 0xffff0000, v49
	v_mul_f32_e32 v70, v40, v70
	v_mul_f32_e32 v72, v40, v72
	v_mul_f32_e32 v45, v40, v45
	v_mul_f32_e32 v74, v40, v74
	v_mul_f32_e32 v47, v40, v47
	v_mul_f32_e32 v76, v40, v76
	v_mul_f32_e32 v49, v40, v49
	v_lshl_add_u64 v[36:37], v[36:37], 0, s[0:1]
	s_waitcnt vmcnt(3)
	v_mul_f32_e32 v41, v50, v41
	v_mul_f32_e32 v42, v51, v42
	v_mul_f32_e32 v43, v53, v43
	s_waitcnt vmcnt(2)
	v_mul_f32_e32 v51, v71, v54
	v_mul_f32_e32 v44, v44, v55
	s_waitcnt vmcnt(1)
	v_mul_f32_e32 v53, v73, v58
	v_mul_f32_e32 v46, v46, v59
	s_waitcnt vmcnt(0)
; __device__ __forceinline__ float sat8(float x) { return __builtin_amdgcn_fmed3f(x, -448.0f, 448.0f); }
; __device__ __forceinline__ unsigned pk4_fp8(float a, float b, float c, float d) { int v = 0; v = __builtin_amdgcn_cvt_pk_fp8_f32(a, b, v, false); v = __builtin_amdgcn_cvt_pk_fp8_f32(c, d, v, true); return (unsigned)v; }
; __device__ __forceinline__ void phase_attn(const Params& p, LAS unsigned char* lds, int G) {
;     ...
; #pragma unroll
;                 for (int hsel = 0; hsel < 2; ++hsel)
; #pragma unroll
;                     for (int dt = 0; dt < 2; ++dt) { unsigned fa[2], fb[2]; const float rs = rstd * FP8_SA;
; #pragma unroll
;                         for (int pp = 0; pp < 2; ++pp) { const int col = (hk * 8 + wl * 2 + hsel) * 64 + dt * 32 + 16 * pp + 8 * hf;
;                             const v4u u = uu[hsel][dt][pp]; const f32x4 w0 = *(const f32x4*)(p.attn_out_norm_w + col), w1 = *(const f32x4*)(p.attn_out_norm_w + col + 4);
;                             const unsigned d0 = pk4_fp8(sat8(bflo(u.x) * rs * w0[0]), sat8(bfhi(u.x) * rs * w0[1]), sat8(bflo(u.y) * rs * w0[2]), sat8(bfhi(u.y) * rs * w0[3]));
;                             const unsigned d1 = pk4_fp8(sat8(bflo(u.z) * rs * w1[0]), sat8(bfhi(u.z) * rs * w1[1]), sat8(bflo(u.w) * rs * w1[2]), sat8(bfhi(u.w) * rs * w1[3]));
;                             if (pp == 0) { fa[0] = d0; fa[1] = d1; } else { fb[0] = d0; fb[1] = d1; } }
;                         const v2u r0 = __builtin_amdgcn_permlane32_swap(fa[0], fb[0], false, false), r1 = __builtin_amdgcn_permlane32_swap(fa[1], fb[1], false, false);
;                         *(v4u*)((unsigned char*)mix + tok * 2048 + (hk * 8 + wl * 2 + hsel) * 64 + dt * 32 + 16 * hf) = (v4u){r0.x, r1.x, r0.y, r1.y}; }
	v_mul_f32_e32 v55, v75, v62
	v_mul_f32_e32 v48, v48, v63
	v_med3_f32 v41, v41, s91, v135
	v_med3_f32 v42, v42, s91, v135
	v_med3_f32 v51, v51, s91, v135
	v_med3_f32 v44, v44, s91, v135
	v_med3_f32 v53, v53, s91, v135
	v_med3_f32 v46, v46, s91, v135
	v_med3_f32 v55, v55, s91, v135
	v_med3_f32 v48, v48, s91, v135
	v_cvt_pk_fp8_f32 v66, v41, v42
	v_cvt_pk_fp8_f32 v68, v53, v46
	v_cvt_pk_fp8_f32 v67, v51, v44
	v_cvt_pk_fp8_f32 v69, v55, v48
	v_mul_f32_e32 v50, v52, v70
	v_mul_f32_e32 v52, v72, v56
	v_mul_f32_e32 v45, v45, v57
	v_mul_f32_e32 v54, v74, v60
	v_mul_f32_e32 v47, v47, v61
	v_mul_f32_e32 v56, v76, v64
	v_mul_f32_e32 v49, v49, v65
	v_med3_f32 v50, v50, s91, v135
	v_med3_f32 v43, v43, s91, v135
	v_med3_f32 v52, v52, s91, v135
	v_med3_f32 v45, v45, s91, v135
	v_med3_f32 v54, v54, s91, v135
	v_med3_f32 v47, v47, s91, v135
	v_med3_f32 v56, v56, s91, v135
	v_med3_f32 v49, v49, s91, v135
	v_cvt_pk_fp8_f32 v66, v50, v43 op_sel:[0,0,1]
	v_cvt_pk_fp8_f32 v68, v54, v47 op_sel:[0,0,1]
	v_cvt_pk_fp8_f32 v67, v52, v45 op_sel:[0,0,1]
	v_cvt_pk_fp8_f32 v69, v56, v49 op_sel:[0,0,1]
	v_lshlrev_b32_e32 v41, 16, v22
	v_permlane32_swap_b32_e32 v66, v68
	v_permlane32_swap_b32_e32 v67, v69
	global_store_dwordx4 v[36:37], v[66:69], off
	global_load_dwordx4 v[42:45], v[28:29], off offset:128
	global_load_dwordx4 v[46:49], v[28:29], off offset:144
	global_load_dwordx4 v[50:53], v[28:29], off offset:192
	global_load_dwordx4 v[54:57], v[28:29], off offset:208
	v_and_b32_e32 v22, 0xffff0000, v22
	v_lshlrev_b32_e32 v62, 16, v23
	v_and_b32_e32 v23, 0xffff0000, v23
	v_lshlrev_b32_e32 v63, 16, v24
	v_and_b32_e32 v24, 0xffff0000, v24
	v_lshlrev_b32_e32 v65, 16, v18
	v_and_b32_e32 v18, 0xffff0000, v18
	v_lshlrev_b32_e32 v67, 16, v20
	v_and_b32_e32 v20, 0xffff0000, v20
	v_mul_f32_e32 v41, v40, v41
	v_mul_f32_e32 v22, v40, v22
	v_mul_f32_e32 v23, v40, v23
	v_mul_f32_e32 v63, v40, v63
	v_mul_f32_e32 v24, v40, v24
	v_mul_f32_e32 v65, v40, v65
	v_mul_f32_e32 v18, v40, v18
	v_mul_f32_e32 v67, v40, v67
	v_mul_f32_e32 v20, v40, v20
	v_lshlrev_b32_e32 v64, 16, v25
	v_and_b32_e32 v25, 0xffff0000, v25
	v_lshlrev_b32_e32 v66, 16, v19
	v_and_b32_e32 v19, 0xffff0000, v19
	v_lshlrev_b32_e32 v68, 16, v21
	v_and_b32_e32 v21, 0xffff0000, v21
	v_mul_f32_e32 v62, v40, v62
	v_mul_f32_e32 v64, v40, v64
	v_mul_f32_e32 v25, v40, v25
	v_mul_f32_e32 v66, v40, v66
	v_mul_f32_e32 v19, v40, v19
	v_mul_f32_e32 v68, v40, v68
	v_mul_f32_e32 v21, v40, v21
	s_waitcnt vmcnt(3)
	v_mul_f32_e32 v41, v41, v42
	v_mul_f32_e32 v22, v22, v43
	v_mul_f32_e32 v23, v23, v45
	s_waitcnt vmcnt(2)
	v_mul_f32_e32 v43, v63, v46
	v_mul_f32_e32 v24, v24, v47
	s_waitcnt vmcnt(1)
	v_mul_f32_e32 v45, v65, v50
	v_mul_f32_e32 v18, v18, v51
	s_waitcnt vmcnt(0)
	v_mul_f32_e32 v47, v67, v54
	v_mul_f32_e32 v20, v20, v55
	v_med3_f32 v41, v41, s91, v135
	v_med3_f32 v22, v22, s91, v135
	v_med3_f32 v43, v43, s91, v135
	v_med3_f32 v24, v24, s91, v135
	v_med3_f32 v45, v45, s91, v135
	v_med3_f32 v18, v18, s91, v135
	v_med3_f32 v47, v47, s91, v135
	v_med3_f32 v20, v20, s91, v135
	v_cvt_pk_fp8_f32 v58, v41, v22
	v_cvt_pk_fp8_f32 v60, v45, v18
	v_cvt_pk_fp8_f32 v59, v43, v24
	v_cvt_pk_fp8_f32 v61, v47, v20
	v_mul_f32_e32 v42, v62, v44
	v_mul_f32_e32 v44, v64, v48
	v_mul_f32_e32 v25, v25, v49
	v_mul_f32_e32 v46, v66, v52
	v_mul_f32_e32 v19, v19, v53
	v_mul_f32_e32 v48, v68, v56
	v_mul_f32_e32 v21, v21, v57
	v_med3_f32 v42, v42, s91, v135
	v_med3_f32 v23, v23, s91, v135
	v_med3_f32 v44, v44, s91, v135
	v_med3_f32 v25, v25, s91, v135
	v_med3_f32 v46, v46, s91, v135
	v_med3_f32 v19, v19, s91, v135
	v_med3_f32 v48, v48, s91, v135
	v_med3_f32 v21, v21, s91, v135
	v_cvt_pk_fp8_f32 v58, v42, v23 op_sel:[0,0,1]
	v_cvt_pk_fp8_f32 v60, v46, v19 op_sel:[0,0,1]
	v_cvt_pk_fp8_f32 v59, v44, v25 op_sel:[0,0,1]
	v_cvt_pk_fp8_f32 v61, v48, v21 op_sel:[0,0,1]
	v_lshlrev_b32_e32 v41, 16, v14
	v_permlane32_swap_b32_e32 v58, v60
	v_permlane32_swap_b32_e32 v59, v61
	global_store_dwordx4 v[36:37], v[58:61], off offset:32
	global_load_dwordx4 v[18:21], v[26:27], off offset:256
	global_load_dwordx4 v[22:25], v[26:27], off offset:272
	global_load_dwordx4 v[42:45], v[26:27], off offset:320
	global_load_dwordx4 v[46:49], v[26:27], off offset:336
	v_and_b32_e32 v14, 0xffff0000, v14
	v_lshlrev_b32_e32 v54, 16, v15
	v_and_b32_e32 v15, 0xffff0000, v15
	v_lshlrev_b32_e32 v55, 16, v16
	v_and_b32_e32 v16, 0xffff0000, v16
	v_lshlrev_b32_e32 v56, 16, v17
	v_lshlrev_b32_e32 v57, 16, v10
	v_and_b32_e32 v10, 0xffff0000, v10
	v_lshlrev_b32_e32 v59, 16, v12
	v_and_b32_e32 v12, 0xffff0000, v12
	v_mul_f32_e32 v41, v40, v41
	v_mul_f32_e32 v14, v40, v14
	v_mul_f32_e32 v54, v40, v54
	v_mul_f32_e32 v15, v40, v15
	v_mul_f32_e32 v55, v40, v55
	v_mul_f32_e32 v16, v40, v16
	v_mul_f32_e32 v56, v40, v56
	v_mul_f32_e32 v57, v40, v57
	v_mul_f32_e32 v10, v40, v10
	v_mul_f32_e32 v59, v40, v59
	v_mul_f32_e32 v12, v40, v12
	v_and_b32_e32 v17, 0xffff0000, v17
	v_lshlrev_b32_e32 v58, 16, v11
	v_and_b32_e32 v11, 0xffff0000, v11
	v_lshlrev_b32_e32 v60, 16, v13
	v_and_b32_e32 v13, 0xffff0000, v13
	v_mul_f32_e32 v17, v40, v17
	v_mul_f32_e32 v58, v40, v58
	v_mul_f32_e32 v11, v40, v11
	v_mul_f32_e32 v60, v40, v60
	v_mul_f32_e32 v13, v40, v13
	v_lshlrev_b64 v[64:65], 11, v[34:35]
	v_lshlrev_b32_e32 v34, 16, v6
	v_and_b32_e32 v6, 0xffff0000, v6
	v_lshlrev_b32_e32 v35, 16, v7
	v_and_b32_e32 v7, 0xffff0000, v7
	v_mul_f32_e32 v34, v40, v34
	v_mul_f32_e32 v6, v40, v6
	v_mul_f32_e32 v35, v40, v35
	v_mul_f32_e32 v7, v40, v7
	v_lshl_add_u64 v[32:33], v[32:33], 0, v[64:65]
	v_lshl_add_u64 v[32:33], v[32:33], 0, s[4:5]
	v_lshl_add_u64 v[30:31], v[30:31], 0, v[64:65]
	v_mov_b32_e32 v61, v131
	v_mov_b32_e32 v62, v131
	v_mov_b32_e32 v63, v131
	v_lshl_add_u64 v[30:31], v[30:31], 0, s[0:1]
	s_waitcnt vmcnt(3)
; __device__ __forceinline__ float sat8(float x) { return __builtin_amdgcn_fmed3f(x, -448.0f, 448.0f); }
; __device__ __forceinline__ unsigned pk4_fp8(float a, float b, float c, float d) { int v = 0; v = __builtin_amdgcn_cvt_pk_fp8_f32(a, b, v, false); v = __builtin_amdgcn_cvt_pk_fp8_f32(c, d, v, true); return (unsigned)v; }
; __device__ __forceinline__ void phase_attn(const Params& p, LAS unsigned char* lds, int G) {
;     ...
;             for (int qt = 0; qt < 4; ++qt) {
;                 const size_t tok = (size_t)b * SEQ + n * 128 + qt * 32 + r;
;                 float tot = 0.f;
; #pragma unroll
;                 for (int hd = 0; hd < 16; ++hd) tot += ssqp[hd * 128 + qt * 32 + r];
;                 const float rstd = rsqrtf(tot * (1.f / 1024.f) + EPS);
;     ...
; #pragma unroll
;                 for (int hsel = 0; hsel < 2; ++hsel)
; #pragma unroll
;                     for (int dt = 0; dt < 2; ++dt) { unsigned fa[2], fb[2]; const float rs = rstd * FP8_SA;
; #pragma unroll
;                         for (int pp = 0; pp < 2; ++pp) { const int col = (hk * 8 + wl * 2 + hsel) * 64 + dt * 32 + 16 * pp + 8 * hf;
;                             const v4u u = uu[hsel][dt][pp]; const f32x4 w0 = *(const f32x4*)(p.attn_out_norm_w + col), w1 = *(const f32x4*)(p.attn_out_norm_w + col + 4);
;                             const unsigned d0 = pk4_fp8(sat8(bflo(u.x) * rs * w0[0]), sat8(bfhi(u.x) * rs * w0[1]), sat8(bflo(u.y) * rs * w0[2]), sat8(bfhi(u.y) * rs * w0[3]));
;                             const unsigned d1 = pk4_fp8(sat8(bflo(u.z) * rs * w1[0]), sat8(bfhi(u.z) * rs * w1[1]), sat8(bflo(u.w) * rs * w1[2]), sat8(bfhi(u.w) * rs * w1[3]));
;                             if (pp == 0) { fa[0] = d0; fa[1] = d1; } else { fb[0] = d0; fb[1] = d1; } }
;                         const v2u r0 = __builtin_amdgcn_permlane32_swap(fa[0], fb[0], false, false), r1 = __builtin_amdgcn_permlane32_swap(fa[1], fb[1], false, false);
;                         *(v4u*)((unsigned char*)mix + tok * 2048 + (hk * 8 + wl * 2 + hsel) * 64 + dt * 32 + 16 * hf) = (v4u){r0.x, r1.x, r0.y, r1.y}; }
	v_mul_f32_e32 v18, v41, v18
	v_mul_f32_e32 v14, v14, v19
	v_mul_f32_e32 v19, v54, v20
	v_mul_f32_e32 v15, v15, v21
	s_waitcnt vmcnt(2)
	v_mul_f32_e32 v20, v55, v22
	v_mul_f32_e32 v16, v16, v23
	v_mul_f32_e32 v21, v56, v24
	s_waitcnt vmcnt(1)
	v_mul_f32_e32 v22, v57, v42
	v_mul_f32_e32 v10, v10, v43
	s_waitcnt vmcnt(0)
	v_mul_f32_e32 v24, v59, v46
	v_mul_f32_e32 v12, v12, v47
	v_med3_f32 v18, v18, s91, v135
	v_med3_f32 v14, v14, s91, v135
	v_med3_f32 v20, v20, s91, v135
	v_med3_f32 v16, v16, s91, v135
	v_med3_f32 v22, v22, s91, v135
	v_med3_f32 v10, v10, s91, v135
	v_med3_f32 v24, v24, s91, v135
	v_med3_f32 v12, v12, s91, v135
	v_cvt_pk_fp8_f32 v50, v18, v14
	v_cvt_pk_fp8_f32 v52, v22, v10
	v_cvt_pk_fp8_f32 v51, v20, v16
	v_cvt_pk_fp8_f32 v53, v24, v12
	v_mul_f32_e32 v17, v17, v25
	v_mul_f32_e32 v23, v58, v44
	v_mul_f32_e32 v11, v11, v45
	v_mul_f32_e32 v25, v60, v48
	v_mul_f32_e32 v13, v13, v49
	v_med3_f32 v19, v19, s91, v135
	v_med3_f32 v15, v15, s91, v135
	v_med3_f32 v21, v21, s91, v135
	v_med3_f32 v17, v17, s91, v135
	v_med3_f32 v23, v23, s91, v135
	v_med3_f32 v11, v11, s91, v135
	v_med3_f32 v25, v25, s91, v135
	v_med3_f32 v13, v13, s91, v135
	v_cvt_pk_fp8_f32 v50, v19, v15 op_sel:[0,0,1]
	v_cvt_pk_fp8_f32 v52, v23, v11 op_sel:[0,0,1]
	v_cvt_pk_fp8_f32 v51, v21, v17 op_sel:[0,0,1]
	v_cvt_pk_fp8_f32 v53, v25, v13 op_sel:[0,0,1]
	v_lshlrev_b32_e32 v41, 16, v8
	v_permlane32_swap_b32_e32 v50, v52
	v_permlane32_swap_b32_e32 v51, v53
	global_store_dwordx4 v[36:37], v[50:53], off offset:64
	global_load_dwordx4 v[10:13], v[26:27], off offset:384
	global_load_dwordx4 v[14:17], v[26:27], off offset:400
	global_load_dwordx4 v[18:21], v[26:27], off offset:448
	global_load_dwordx4 v[22:25], v[26:27], off offset:464
	v_and_b32_e32 v8, 0xffff0000, v8
	v_lshlrev_b32_e32 v46, 16, v9
	v_lshlrev_b32_e32 v47, 16, v2
	v_and_b32_e32 v2, 0xffff0000, v2
	v_lshlrev_b32_e32 v49, 16, v4
	v_and_b32_e32 v4, 0xffff0000, v4
	v_mul_f32_e32 v41, v40, v41
	v_mul_f32_e32 v8, v40, v8
	v_mul_f32_e32 v46, v40, v46
	v_mul_f32_e32 v47, v40, v47
	v_mul_f32_e32 v2, v40, v2
	v_mul_f32_e32 v49, v40, v49
	v_mul_f32_e32 v4, v40, v4
	v_and_b32_e32 v9, 0xffff0000, v9
	v_lshlrev_b32_e32 v48, 16, v3
	v_and_b32_e32 v3, 0xffff0000, v3
	v_lshlrev_b32_e32 v50, 16, v5
	v_and_b32_e32 v5, 0xffff0000, v5
	v_mul_f32_e32 v9, v40, v9
	v_mul_f32_e32 v48, v40, v48
	v_mul_f32_e32 v3, v40, v3
	v_mul_f32_e32 v50, v40, v50
	v_mul_f32_e32 v5, v40, v5
	v_mov_b32_e32 v60, v131
	s_waitcnt vmcnt(3)
	v_mul_f32_e32 v10, v34, v10
	v_mul_f32_e32 v6, v6, v11
	v_mul_f32_e32 v11, v35, v12
	v_mul_f32_e32 v7, v7, v13
	s_waitcnt vmcnt(2)
	v_mul_f32_e32 v12, v41, v14
	v_mul_f32_e32 v8, v8, v15
	v_mul_f32_e32 v13, v46, v16
	s_waitcnt vmcnt(1)
	v_mul_f32_e32 v14, v47, v18
	v_mul_f32_e32 v2, v2, v19
	s_waitcnt vmcnt(0)
	v_mul_f32_e32 v16, v49, v22
	v_mul_f32_e32 v4, v4, v23
	v_med3_f32 v10, v10, s91, v135
	v_med3_f32 v6, v6, s91, v135
	v_med3_f32 v12, v12, s91, v135
	v_med3_f32 v8, v8, s91, v135
	v_med3_f32 v14, v14, s91, v135
	v_med3_f32 v2, v2, s91, v135
	v_med3_f32 v16, v16, s91, v135
	v_med3_f32 v4, v4, s91, v135
	v_cvt_pk_fp8_f32 v42, v10, v6
	v_cvt_pk_fp8_f32 v44, v14, v2
	v_cvt_pk_fp8_f32 v43, v12, v8
	v_cvt_pk_fp8_f32 v45, v16, v4
	v_mul_f32_e32 v9, v9, v17
	v_mul_f32_e32 v15, v48, v20
	v_mul_f32_e32 v3, v3, v21
	v_mul_f32_e32 v17, v50, v24
	v_mul_f32_e32 v5, v5, v25
	v_med3_f32 v11, v11, s91, v135
	v_med3_f32 v7, v7, s91, v135
	v_med3_f32 v13, v13, s91, v135
	v_med3_f32 v9, v9, s91, v135
	v_med3_f32 v15, v15, s91, v135
	v_med3_f32 v3, v3, s91, v135
	v_med3_f32 v17, v17, s91, v135
	v_med3_f32 v5, v5, s91, v135
	v_cvt_pk_fp8_f32 v42, v11, v7 op_sel:[0,0,1]
	v_cvt_pk_fp8_f32 v44, v15, v3 op_sel:[0,0,1]
	v_cvt_pk_fp8_f32 v43, v13, v9 op_sel:[0,0,1]
	v_cvt_pk_fp8_f32 v45, v17, v5 op_sel:[0,0,1]
	v_permlane32_swap_b32_e32 v42, v44
	s_nop 0
	v_permlane32_swap_b32_e32 v43, v45
	global_store_dwordx4 v[36:37], v[42:45], off offset:96
	global_load_dwordx4 v[34:37], v[32:33], off
	s_nop 0
	global_load_dwordx4 v[40:43], v[32:33], off offset:32
	global_load_dwordx4 v[22:25], v[32:33], off offset:64
	global_load_dwordx4 v[18:21], v[32:33], off offset:96
	global_load_dwordx4 v[14:17], v[32:33], off offset:128
	global_load_dwordx4 v[10:13], v[32:33], off offset:160
	global_load_dwordx4 v[6:9], v[32:33], off offset:192
	global_load_dwordx4 v[2:5], v[32:33], off offset:224
	ds_read2_b32 v[32:33], v38 offset0:96 offset1:224
	ds_read2st64_b32 v[66:67], v39 offset0:5 offset1:7
	ds_read2st64_b32 v[68:69], v39 offset0:9 offset1:11
	ds_read2st64_b32 v[70:71], v39 offset0:13 offset1:15
	ds_read2st64_b32 v[72:73], v39 offset0:17 offset1:19
	ds_read2st64_b32 v[74:75], v39 offset0:21 offset1:23
	ds_read2st64_b32 v[76:77], v39 offset0:25 offset1:27
	ds_read2st64_b32 v[38:39], v39 offset0:29 offset1:31
	s_waitcnt vmcnt(6)
	s_waitcnt vmcnt(4)
	s_waitcnt vmcnt(2)
	s_waitcnt vmcnt(0)
	global_load_dwordx4 v[44:47], v[28:29], off
	global_load_dwordx4 v[48:51], v[28:29], off offset:16
	global_load_dwordx4 v[52:55], v[28:29], off offset:64
	global_load_dwordx4 v[56:59], v[28:29], off offset:80
	s_waitcnt lgkmcnt(7)
	v_add_f32_e32 v32, 0, v32
	v_add_f32_e32 v32, v32, v33
	s_waitcnt lgkmcnt(6)
	v_add_f32_e32 v32, v32, v66
	v_add_f32_e32 v32, v32, v67
	s_waitcnt lgkmcnt(5)
	v_add_f32_e32 v32, v32, v68
	v_add_f32_e32 v32, v32, v69
	s_waitcnt lgkmcnt(4)
	v_add_f32_e32 v32, v32, v70
	v_add_f32_e32 v32, v32, v71
	s_waitcnt lgkmcnt(3)
	v_add_f32_e32 v32, v32, v72
	v_add_f32_e32 v32, v32, v73
	s_waitcnt lgkmcnt(2)
	v_add_f32_e32 v32, v32, v74
	v_add_f32_e32 v32, v32, v75
	s_waitcnt lgkmcnt(1)
	v_add_f32_e32 v32, v32, v76
	v_add_f32_e32 v32, v32, v77
	s_waitcnt lgkmcnt(0)
; __device__ __forceinline__ void phase_attn(const Params& p, LAS unsigned char* lds, int G) {
;     ...
;             for (int qt = 0; qt < 4; ++qt) {
;                 const size_t tok = (size_t)b * SEQ + n * 128 + qt * 32 + r;
;                 float tot = 0.f;
; #pragma unroll
;                 for (int hd = 0; hd < 16; ++hd) tot += ssqp[hd * 128 + qt * 32 + r];
;                 const float rstd = rsqrtf(tot * (1.f / 1024.f) + EPS);
;                 v4u uu[2][2][2];
; #pragma unroll
;                 for (int hsel = 0; hsel < 2; ++hsel)
; #pragma unroll
;                     for (int dt = 0; dt < 2; ++dt)
; #pragma unroll
;                         for (int pp = 0; pp < 2; ++pp) uu[hsel][dt][pp] = *(const v4u*)(att + tok * ALD + (hk * 8 + wl * 2 + hsel) * 64 + dt * 32 + 16 * pp + 8 * hf);
; #pragma unroll
;                 for (int hsel = 0; hsel < 2; ++hsel)
; #pragma unroll
;                     for (int dt = 0; dt < 2; ++dt) { asm volatile("" : "+v"(uu[hsel][dt][0]), "+v"(uu[hsel][dt][1])); }
;     ...
; #pragma unroll
;                 for (int hsel = 0; hsel < 2; ++hsel)
; #pragma unroll
;                     for (int dt = 0; dt < 2; ++dt) { unsigned fa[2], fb[2]; const float rs = rstd * FP8_SA;
; #pragma unroll
;                         for (int pp = 0; pp < 2; ++pp) { const int col = (hk * 8 + wl * 2 + hsel) * 64 + dt * 32 + 16 * pp + 8 * hf;
;                             const v4u u = uu[hsel][dt][pp]; const f32x4 w0 = *(const f32x4*)(p.attn_out_norm_w + col), w1 = *(const f32x4*)(p.attn_out_norm_w + col + 4);
;                             const unsigned d0 = pk4_fp8(sat8(bflo(u.x) * rs * w0[0]), sat8(bfhi(u.x) * rs * w0[1]), sat8(bflo(u.y) * rs * w0[2]), sat8(bfhi(u.y) * rs * w0[3]));
;                             const unsigned d1 = pk4_fp8(sat8(bflo(u.z) * rs * w1[0]), sat8(bfhi(u.z) * rs * w1[1]), sat8(bflo(u.w) * rs * w1[2]), sat8(bfhi(u.w) * rs * w1[3]));
;                             if (pp == 0) { fa[0] = d0; fa[1] = d1; } else { fb[0] = d0; fb[1] = d1; } }
;                         const v2u r0 = __builtin_amdgcn_permlane32_swap(fa[0], fb[0], false, false), r1 = __builtin_amdgcn_permlane32_swap(fa[1], fb[1], false, false);
;                         *(v4u*)((unsigned char*)mix + tok * 2048 + (hk * 8 + wl * 2 + hsel) * 64 + dt * 32 + 16 * hf) = (v4u){r0.x, r1.x, r0.y, r1.y}; }
	v_add_f32_e32 v32, v32, v38
	v_add_f32_e32 v32, v32, v39
	v_fmamk_f32 v32, v32, 0x3a800000, v1
	v_mul_f32_e32 v33, 0x4b800000, v32
	v_cmp_gt_f32_e32 vcc, s43, v32
	v_lshlrev_b32_e32 v38, 16, v35
	v_and_b32_e32 v35, 0xffff0000, v35
	v_cndmask_b32_e32 v32, v32, v33, vcc
	v_rsq_f32_e32 v32, v32
	v_lshlrev_b32_e32 v39, 16, v36
	v_and_b32_e32 v36, 0xffff0000, v36
	v_lshlrev_b32_e32 v65, 16, v40
	v_mul_f32_e32 v33, 0x45800000, v32
	v_cndmask_b32_e32 v32, v32, v33, vcc
	v_mul_f32_e32 v32, 0x41800000, v32
	v_lshlrev_b32_e32 v33, 16, v34
	v_and_b32_e32 v34, 0xffff0000, v34
	v_and_b32_e32 v40, 0xffff0000, v40
	v_lshlrev_b32_e32 v67, 16, v42
	v_and_b32_e32 v42, 0xffff0000, v42
	v_mul_f32_e32 v33, v32, v33
	v_mul_f32_e32 v34, v32, v34
	v_mul_f32_e32 v35, v32, v35
	v_mul_f32_e32 v39, v32, v39
	v_mul_f32_e32 v36, v32, v36
	v_mul_f32_e32 v65, v32, v65
	v_mul_f32_e32 v40, v32, v40
	v_mul_f32_e32 v67, v32, v67
	v_mul_f32_e32 v42, v32, v42
	v_lshlrev_b32_e32 v64, 16, v37
	v_and_b32_e32 v37, 0xffff0000, v37
	v_lshlrev_b32_e32 v66, 16, v41
	v_and_b32_e32 v41, 0xffff0000, v41
	v_lshlrev_b32_e32 v68, 16, v43
	v_and_b32_e32 v43, 0xffff0000, v43
	v_mul_f32_e32 v38, v32, v38
	v_mul_f32_e32 v64, v32, v64
	v_mul_f32_e32 v37, v32, v37
	v_mul_f32_e32 v66, v32, v66
	v_mul_f32_e32 v41, v32, v41
	v_mul_f32_e32 v68, v32, v68
	v_mul_f32_e32 v43, v32, v43
	s_waitcnt vmcnt(3)
	v_mul_f32_e32 v33, v44, v33
	v_mul_f32_e32 v34, v45, v34
	v_mul_f32_e32 v35, v47, v35
	s_waitcnt vmcnt(2)
	v_mul_f32_e32 v39, v39, v48
	v_mul_f32_e32 v36, v36, v49
	s_waitcnt vmcnt(1)
	v_mul_f32_e32 v45, v65, v52
	v_mul_f32_e32 v40, v40, v53
	s_waitcnt vmcnt(0)
	v_mul_f32_e32 v47, v67, v56
	v_mul_f32_e32 v42, v42, v57
	v_med3_f32 v33, v33, s91, v135
	v_med3_f32 v34, v34, s91, v135
	v_med3_f32 v39, v39, s91, v135
	v_med3_f32 v36, v36, s91, v135
	v_med3_f32 v45, v45, s91, v135
	v_med3_f32 v40, v40, s91, v135
	v_med3_f32 v47, v47, s91, v135
	v_med3_f32 v42, v42, s91, v135
	v_cvt_pk_fp8_f32 v60, v33, v34
	v_cvt_pk_fp8_f32 v62, v45, v40
	v_cvt_pk_fp8_f32 v61, v39, v36
	v_cvt_pk_fp8_f32 v63, v47, v42
	v_mul_f32_e32 v38, v46, v38
	v_mul_f32_e32 v44, v64, v50
	v_mul_f32_e32 v37, v37, v51
	v_mul_f32_e32 v46, v66, v54
	v_mul_f32_e32 v41, v41, v55
	v_mul_f32_e32 v48, v68, v58
	v_mul_f32_e32 v43, v43, v59
	v_med3_f32 v38, v38, s91, v135
	v_med3_f32 v35, v35, s91, v135
	v_med3_f32 v44, v44, s91, v135
	v_med3_f32 v37, v37, s91, v135
	v_med3_f32 v46, v46, s91, v135
	v_med3_f32 v41, v41, s91, v135
	v_med3_f32 v48, v48, s91, v135
	v_med3_f32 v43, v43, s91, v135
	v_cvt_pk_fp8_f32 v60, v38, v35 op_sel:[0,0,1]
	v_cvt_pk_fp8_f32 v62, v46, v41 op_sel:[0,0,1]
	v_cvt_pk_fp8_f32 v61, v44, v37 op_sel:[0,0,1]
	v_cvt_pk_fp8_f32 v63, v48, v43 op_sel:[0,0,1]
	v_lshlrev_b32_e32 v33, 16, v24
	v_permlane32_swap_b32_e32 v60, v62
	v_permlane32_swap_b32_e32 v61, v63
	global_store_dwordx4 v[30:31], v[60:63], off
	global_load_dwordx4 v[34:37], v[28:29], off offset:128
	global_load_dwordx4 v[38:41], v[28:29], off offset:144
	global_load_dwordx4 v[42:45], v[28:29], off offset:192
	global_load_dwordx4 v[46:49], v[28:29], off offset:208
	v_lshlrev_b32_e32 v28, 16, v22
	v_and_b32_e32 v22, 0xffff0000, v22
	v_lshlrev_b32_e32 v29, 16, v23
	v_and_b32_e32 v23, 0xffff0000, v23
	v_and_b32_e32 v24, 0xffff0000, v24
	v_lshlrev_b32_e32 v55, 16, v18
	v_and_b32_e32 v18, 0xffff0000, v18
	v_lshlrev_b32_e32 v57, 16, v20
	v_and_b32_e32 v20, 0xffff0000, v20
	v_mul_f32_e32 v28, v32, v28
	v_mul_f32_e32 v22, v32, v22
	v_mul_f32_e32 v23, v32, v23
	v_mul_f32_e32 v33, v32, v33
	v_mul_f32_e32 v24, v32, v24
	v_mul_f32_e32 v55, v32, v55
	v_mul_f32_e32 v18, v32, v18
	v_mul_f32_e32 v57, v32, v57
	v_mul_f32_e32 v20, v32, v20
	v_lshlrev_b32_e32 v54, 16, v25
	v_and_b32_e32 v25, 0xffff0000, v25
	v_lshlrev_b32_e32 v56, 16, v19
	v_and_b32_e32 v19, 0xffff0000, v19
	v_lshlrev_b32_e32 v58, 16, v21
	v_and_b32_e32 v21, 0xffff0000, v21
	v_mul_f32_e32 v29, v32, v29
	v_mul_f32_e32 v54, v32, v54
	v_mul_f32_e32 v25, v32, v25
	v_mul_f32_e32 v56, v32, v56
	v_mul_f32_e32 v19, v32, v19
	v_mul_f32_e32 v58, v32, v58
	v_mul_f32_e32 v21, v32, v21
	s_waitcnt vmcnt(3)
	v_mul_f32_e32 v28, v28, v34
	v_mul_f32_e32 v22, v22, v35
	v_mul_f32_e32 v23, v23, v37
	s_waitcnt vmcnt(2)
	v_mul_f32_e32 v33, v33, v38
	v_mul_f32_e32 v24, v24, v39
	s_waitcnt vmcnt(1)
	v_mul_f32_e32 v35, v55, v42
	v_mul_f32_e32 v18, v18, v43
	s_waitcnt vmcnt(0)
; __device__ __forceinline__ float sat8(float x) { return __builtin_amdgcn_fmed3f(x, -448.0f, 448.0f); }
; __device__ __forceinline__ unsigned pk4_fp8(float a, float b, float c, float d) { int v = 0; v = __builtin_amdgcn_cvt_pk_fp8_f32(a, b, v, false); v = __builtin_amdgcn_cvt_pk_fp8_f32(c, d, v, true); return (unsigned)v; }
; __device__ __forceinline__ void phase_attn(const Params& p, LAS unsigned char* lds, int G) {
;     ...
; #pragma unroll
;                 for (int hsel = 0; hsel < 2; ++hsel)
; #pragma unroll
;                     for (int dt = 0; dt < 2; ++dt) { unsigned fa[2], fb[2]; const float rs = rstd * FP8_SA;
; #pragma unroll
;                         for (int pp = 0; pp < 2; ++pp) { const int col = (hk * 8 + wl * 2 + hsel) * 64 + dt * 32 + 16 * pp + 8 * hf;
;                             const v4u u = uu[hsel][dt][pp]; const f32x4 w0 = *(const f32x4*)(p.attn_out_norm_w + col), w1 = *(const f32x4*)(p.attn_out_norm_w + col + 4);
;                             const unsigned d0 = pk4_fp8(sat8(bflo(u.x) * rs * w0[0]), sat8(bfhi(u.x) * rs * w0[1]), sat8(bflo(u.y) * rs * w0[2]), sat8(bfhi(u.y) * rs * w0[3]));
;                             const unsigned d1 = pk4_fp8(sat8(bflo(u.z) * rs * w1[0]), sat8(bfhi(u.z) * rs * w1[1]), sat8(bflo(u.w) * rs * w1[2]), sat8(bfhi(u.w) * rs * w1[3]));
;                             if (pp == 0) { fa[0] = d0; fa[1] = d1; } else { fb[0] = d0; fb[1] = d1; } }
;                         const v2u r0 = __builtin_amdgcn_permlane32_swap(fa[0], fb[0], false, false), r1 = __builtin_amdgcn_permlane32_swap(fa[1], fb[1], false, false);
;                         *(v4u*)((unsigned char*)mix + tok * 2048 + (hk * 8 + wl * 2 + hsel) * 64 + dt * 32 + 16 * hf) = (v4u){r0.x, r1.x, r0.y, r1.y}; }
	v_mul_f32_e32 v37, v57, v46
	v_mul_f32_e32 v20, v20, v47
	v_med3_f32 v28, v28, s91, v135
	v_med3_f32 v22, v22, s91, v135
	v_med3_f32 v33, v33, s91, v135
	v_med3_f32 v24, v24, s91, v135
	v_med3_f32 v35, v35, s91, v135
	v_med3_f32 v18, v18, s91, v135
	v_med3_f32 v37, v37, s91, v135
	v_med3_f32 v20, v20, s91, v135
	v_cvt_pk_fp8_f32 v50, v28, v22
	v_cvt_pk_fp8_f32 v52, v35, v18
	v_cvt_pk_fp8_f32 v51, v33, v24
	v_cvt_pk_fp8_f32 v53, v37, v20
	v_mul_f32_e32 v29, v29, v36
	v_mul_f32_e32 v34, v54, v40
	v_mul_f32_e32 v25, v25, v41
	v_mul_f32_e32 v36, v56, v44
	v_mul_f32_e32 v19, v19, v45
	v_mul_f32_e32 v38, v58, v48
	v_mul_f32_e32 v21, v21, v49
	v_med3_f32 v29, v29, s91, v135
	v_med3_f32 v23, v23, s91, v135
	v_med3_f32 v34, v34, s91, v135
	v_med3_f32 v25, v25, s91, v135
	v_med3_f32 v36, v36, s91, v135
	v_med3_f32 v19, v19, s91, v135
	v_med3_f32 v38, v38, s91, v135
	v_med3_f32 v21, v21, s91, v135
	v_cvt_pk_fp8_f32 v50, v29, v23 op_sel:[0,0,1]
	v_cvt_pk_fp8_f32 v52, v36, v19 op_sel:[0,0,1]
	v_cvt_pk_fp8_f32 v51, v34, v25 op_sel:[0,0,1]
	v_cvt_pk_fp8_f32 v53, v38, v21 op_sel:[0,0,1]
	v_lshlrev_b32_e32 v28, 16, v14
	v_permlane32_swap_b32_e32 v50, v52
	v_permlane32_swap_b32_e32 v51, v53
	global_store_dwordx4 v[30:31], v[50:53], off offset:32
	global_load_dwordx4 v[18:21], v[26:27], off offset:256
	global_load_dwordx4 v[22:25], v[26:27], off offset:272
	global_load_dwordx4 v[34:37], v[26:27], off offset:320
	global_load_dwordx4 v[38:41], v[26:27], off offset:336
	v_and_b32_e32 v14, 0xffff0000, v14
	v_lshlrev_b32_e32 v29, 16, v15
	v_and_b32_e32 v15, 0xffff0000, v15
	v_lshlrev_b32_e32 v33, 16, v16
	v_and_b32_e32 v16, 0xffff0000, v16
	v_lshlrev_b32_e32 v46, 16, v17
	v_lshlrev_b32_e32 v47, 16, v10
	v_and_b32_e32 v10, 0xffff0000, v10
	v_lshlrev_b32_e32 v49, 16, v12
	v_and_b32_e32 v12, 0xffff0000, v12
	v_mul_f32_e32 v28, v32, v28
	v_mul_f32_e32 v14, v32, v14
	v_mul_f32_e32 v29, v32, v29
	v_mul_f32_e32 v15, v32, v15
	v_mul_f32_e32 v33, v32, v33
	v_mul_f32_e32 v16, v32, v16
	v_mul_f32_e32 v46, v32, v46
	v_mul_f32_e32 v47, v32, v47
	v_mul_f32_e32 v10, v32, v10
	v_mul_f32_e32 v49, v32, v49
	v_mul_f32_e32 v12, v32, v12
	v_and_b32_e32 v17, 0xffff0000, v17
	v_lshlrev_b32_e32 v48, 16, v11
	v_and_b32_e32 v11, 0xffff0000, v11
	v_lshlrev_b32_e32 v50, 16, v13
	v_and_b32_e32 v13, 0xffff0000, v13
	v_mul_f32_e32 v17, v32, v17
	v_mul_f32_e32 v48, v32, v48
	v_mul_f32_e32 v11, v32, v11
	v_mul_f32_e32 v50, v32, v50
	v_mul_f32_e32 v13, v32, v13
	s_waitcnt vmcnt(3)
	v_mul_f32_e32 v18, v28, v18
	v_mul_f32_e32 v14, v14, v19
	v_mul_f32_e32 v19, v29, v20
	v_mul_f32_e32 v15, v15, v21
	s_waitcnt vmcnt(2)
	v_mul_f32_e32 v20, v33, v22
	v_mul_f32_e32 v16, v16, v23
	v_mul_f32_e32 v21, v46, v24
	s_waitcnt vmcnt(1)
	v_mul_f32_e32 v22, v47, v34
	v_mul_f32_e32 v10, v10, v35
	s_waitcnt vmcnt(0)
	v_mul_f32_e32 v24, v49, v38
	v_mul_f32_e32 v12, v12, v39
	v_med3_f32 v18, v18, s91, v135
	v_med3_f32 v14, v14, s91, v135
	v_med3_f32 v20, v20, s91, v135
	v_med3_f32 v16, v16, s91, v135
	v_med3_f32 v22, v22, s91, v135
	v_med3_f32 v10, v10, s91, v135
	v_med3_f32 v24, v24, s91, v135
	v_med3_f32 v12, v12, s91, v135
	v_cvt_pk_fp8_f32 v42, v18, v14
	v_cvt_pk_fp8_f32 v44, v22, v10
	v_cvt_pk_fp8_f32 v43, v20, v16
	v_cvt_pk_fp8_f32 v45, v24, v12
	v_mul_f32_e32 v17, v17, v25
	v_mul_f32_e32 v23, v48, v36
	v_mul_f32_e32 v11, v11, v37
	v_mul_f32_e32 v25, v50, v40
	v_mul_f32_e32 v13, v13, v41
	v_med3_f32 v19, v19, s91, v135
	v_med3_f32 v15, v15, s91, v135
	v_med3_f32 v21, v21, s91, v135
	v_med3_f32 v17, v17, s91, v135
	v_med3_f32 v23, v23, s91, v135
	v_med3_f32 v11, v11, s91, v135
	v_med3_f32 v25, v25, s91, v135
	v_med3_f32 v13, v13, s91, v135
	v_cvt_pk_fp8_f32 v42, v19, v15 op_sel:[0,0,1]
	v_cvt_pk_fp8_f32 v44, v23, v11 op_sel:[0,0,1]
	v_cvt_pk_fp8_f32 v43, v21, v17 op_sel:[0,0,1]
	v_cvt_pk_fp8_f32 v45, v25, v13 op_sel:[0,0,1]
	v_lshlrev_b32_e32 v33, 16, v6
	v_permlane32_swap_b32_e32 v42, v44
	v_permlane32_swap_b32_e32 v43, v45
	global_store_dwordx4 v[30:31], v[42:45], off offset:64
	global_load_dwordx4 v[10:13], v[26:27], off offset:384
	global_load_dwordx4 v[14:17], v[26:27], off offset:400
	global_load_dwordx4 v[18:21], v[26:27], off offset:448
	global_load_dwordx4 v[22:25], v[26:27], off offset:464
	v_and_b32_e32 v6, 0xffff0000, v6
	v_lshlrev_b32_e32 v34, 16, v7
	v_and_b32_e32 v7, 0xffff0000, v7
	v_lshlrev_b32_e32 v35, 16, v8
	v_and_b32_e32 v8, 0xffff0000, v8
	v_lshlrev_b32_e32 v36, 16, v9
	v_lshlrev_b32_e32 v37, 16, v2
	v_and_b32_e32 v2, 0xffff0000, v2
	v_lshlrev_b32_e32 v39, 16, v4
	v_and_b32_e32 v4, 0xffff0000, v4
	v_mul_f32_e32 v33, v32, v33
	v_mul_f32_e32 v6, v32, v6
	v_mul_f32_e32 v34, v32, v34
	v_mul_f32_e32 v7, v32, v7
	v_mul_f32_e32 v35, v32, v35
	v_mul_f32_e32 v8, v32, v8
	v_mul_f32_e32 v36, v32, v36
	v_mul_f32_e32 v37, v32, v37
	v_mul_f32_e32 v2, v32, v2
	v_mul_f32_e32 v39, v32, v39
	v_mul_f32_e32 v4, v32, v4
	v_and_b32_e32 v9, 0xffff0000, v9
	v_lshlrev_b32_e32 v38, 16, v3
	v_and_b32_e32 v3, 0xffff0000, v3
	v_lshlrev_b32_e32 v40, 16, v5
	v_and_b32_e32 v5, 0xffff0000, v5
	v_mul_f32_e32 v9, v32, v9
	v_mul_f32_e32 v38, v32, v38
	v_mul_f32_e32 v3, v32, v3
	v_mul_f32_e32 v40, v32, v40
	v_mul_f32_e32 v5, v32, v5
	s_waitcnt vmcnt(3)
	v_mul_f32_e32 v10, v33, v10
	v_mul_f32_e32 v6, v6, v11
	v_mul_f32_e32 v11, v34, v12
	v_mul_f32_e32 v7, v7, v13
	s_waitcnt vmcnt(2)
	v_mul_f32_e32 v12, v35, v14
	v_mul_f32_e32 v8, v8, v15
	v_mul_f32_e32 v13, v36, v16
	s_waitcnt vmcnt(1)
	v_mul_f32_e32 v14, v37, v18
	v_mul_f32_e32 v2, v2, v19
	s_waitcnt vmcnt(0)
	v_mul_f32_e32 v16, v39, v22
	v_mul_f32_e32 v4, v4, v23
	v_med3_f32 v10, v10, s91, v135
	v_med3_f32 v6, v6, s91, v135
	v_med3_f32 v12, v12, s91, v135
	v_med3_f32 v8, v8, s91, v135
	v_med3_f32 v14, v14, s91, v135
	v_med3_f32 v2, v2, s91, v135
	v_med3_f32 v16, v16, s91, v135
	v_med3_f32 v4, v4, s91, v135
	v_cvt_pk_fp8_f32 v26, v10, v6
	v_cvt_pk_fp8_f32 v28, v14, v2
	v_cvt_pk_fp8_f32 v27, v12, v8
	v_cvt_pk_fp8_f32 v29, v16, v4
	v_mul_f32_e32 v9, v9, v17
	v_mul_f32_e32 v15, v38, v20
	v_mul_f32_e32 v3, v3, v21
	v_mul_f32_e32 v17, v40, v24
	v_mul_f32_e32 v5, v5, v25
	v_med3_f32 v11, v11, s91, v135
	v_med3_f32 v7, v7, s91, v135
	v_med3_f32 v13, v13, s91, v135
	v_med3_f32 v9, v9, s91, v135
	v_med3_f32 v15, v15, s91, v135
	v_med3_f32 v3, v3, s91, v135
	v_med3_f32 v17, v17, s91, v135
	v_med3_f32 v5, v5, s91, v135
	v_cvt_pk_fp8_f32 v26, v11, v7 op_sel:[0,0,1]
	v_cvt_pk_fp8_f32 v28, v15, v3 op_sel:[0,0,1]
	v_cvt_pk_fp8_f32 v27, v13, v9 op_sel:[0,0,1]
	v_cvt_pk_fp8_f32 v29, v17, v5 op_sel:[0,0,1]
	v_permlane32_swap_b32_e32 v26, v28
	s_nop 0
	v_permlane32_swap_b32_e32 v27, v29
	global_store_dwordx4 v[30:31], v[26:29], off offset:96
	s_cbranch_scc1 .LBB0_321

; __device__ __forceinline__ void ssd_out_store(const Params& p, bf16* mix, const LAS float* ssqp, size_t trow0, int h, int lsel, int r, int hf, const unsigned (&yp)[2][2][8]) {
;     f32x4 w4[2][4];
; #pragma unroll
;     for (int pt = 0; pt < 2; ++pt)
; #pragma unroll
;         for (int q = 0; q < 4; ++q) w4[pt][q] = *(const f32x4*)(p.ssm_norm_w + h * 64 + pt * 32 + 8 * q + 4 * hf);
; #pragma unroll
;     for (int pt = 0; pt < 2; ++pt) { asm volatile("" : "+v"(w4[pt][0]), "+v"(w4[pt][1]), "+v"(w4[pt][2]), "+v"(w4[pt][3])); }
; #pragma unroll
;     for (int j = 0; j < 2; ++j) { const int lt = j == 0 ? (lsel ? 1 : 0) : (lsel ? 2 : 3); const int l = lt * 32 + r; const size_t t = trow0 + l;
;         float tot = 0.f;
; #pragma unroll
;         for (int hd = 0; hd < 8; ++hd) tot += ssqp[hd * 128 + l];
;         const float rstd = rsqrtf(tot * (1.f / 512.f) + EPS);
; #pragma unroll
.LBB0_433:
	s_or_b64 exec, exec, s[0:1]
	v_mov_b32_e32 v36, v0
	s_waitcnt lgkmcnt(0)
	s_barrier
	v_cvt_pk_bf16_f32 v110, v156, v157
	v_readfirstlane_b32 s0, v36
	s_ashr_i32 s1, s0, 7
	s_add_i32 s1, s1, s16
	s_bfe_u32 s6, s0, 0x10006
	s_lshl_b32 s0, s1, 6
	s_ashr_i32 s1, s0, 31
	s_lshl_b64 s[4:5], s[0:1], 2
	s_add_u32 s4, s46, s4
	v_lshrrev_b32_e32 v1, 1, v36
	s_addc_u32 s5, s47, s5
	v_and_b32_e32 v138, 16, v1
	global_load_dwordx4 v[18:21], v138, s[4:5] offset:96
	global_load_dwordx4 v[22:25], v138, s[4:5] offset:64
	global_load_dwordx4 v[26:29], v138, s[4:5] offset:32
	global_load_dwordx4 v[30:33], v138, s[4:5]
	global_load_dwordx4 v[2:5], v138, s[4:5] offset:224
	global_load_dwordx4 v[6:9], v138, s[4:5] offset:192
	global_load_dwordx4 v[10:13], v138, s[4:5] offset:160
	global_load_dwordx4 v[14:17], v138, s[4:5] offset:128
	v_and_b32_e32 v118, 31, v36
	v_lshl_or_b32 v36, s6, 5, v118
	v_cvt_pk_bf16_f32 v100, v140, v141
	v_cvt_pk_bf16_f32 v101, v142, v143
	v_cvt_pk_bf16_f32 v109, v154, v155
	v_mov_b32_e32 v37, s37
	v_lshlrev_b32_e32 v154, 16, v110
	v_and_b32_e32 v155, 0xffff0000, v110
	v_lshl_add_u32 v110, v36, 2, s10
	v_or_b32_e32 v36, s36, v36
	s_cmp_eq_u32 s6, 0
	v_lshlrev_b32_e32 v136, 16, v100
	v_and_b32_e32 v137, 0xffff0000, v100
	v_lshlrev_b32_e32 v140, 16, v101
	v_and_b32_e32 v141, 0xffff0000, v101
	v_lshlrev_b64 v[100:101], 11, v[36:37]
	s_cselect_b32 s4, 0x60, 64
	v_lshl_add_u64 v[100:101], s[20:21], 0, v[100:101]
	v_or_b32_e32 v36, s4, v118
	v_cvt_pk_bf16_f32 v102, v144, v145
	v_cvt_pk_bf16_f32 v103, v146, v147
	v_cvt_pk_bf16_f32 v106, v148, v149
	v_cvt_pk_bf16_f32 v107, v150, v151
	v_cvt_pk_bf16_f32 v108, v152, v153
	v_cvt_pk_bf16_f32 v112, v158, v159
	v_cvt_pk_bf16_f32 v113, v160, v161
	v_lshl_add_u64 v[100:101], v[100:101], 0, s[0:1]
	v_lshl_add_u32 v118, v36, 2, s10
	v_lshlrev_b32_e32 v142, 16, v102
	v_and_b32_e32 v143, 0xffff0000, v102
	v_lshlrev_b32_e32 v144, 16, v103
	v_and_b32_e32 v145, 0xffff0000, v103
	v_lshlrev_b32_e32 v146, 16, v106
	v_and_b32_e32 v147, 0xffff0000, v106
	v_lshlrev_b32_e32 v148, 16, v107
	v_and_b32_e32 v149, 0xffff0000, v107
	v_lshlrev_b32_e32 v150, 16, v108
	v_and_b32_e32 v151, 0xffff0000, v108
	v_lshlrev_b32_e32 v152, 16, v109
	v_and_b32_e32 v153, 0xffff0000, v109
	v_lshl_add_u64 v[102:103], v[100:101], 0, v[138:139]
	v_lshlrev_b32_e32 v156, 16, v112
	v_and_b32_e32 v157, 0xffff0000, v112
	v_lshlrev_b32_e32 v158, 16, v113
	v_and_b32_e32 v159, 0xffff0000, v113
	v_cvt_pk_bf16_f32 v114, v162, v163
	v_cvt_pk_bf16_f32 v115, v164, v165
	v_cvt_pk_bf16_f32 v116, v166, v167
	v_cvt_pk_bf16_f32 v117, v168, v169
	v_lshlrev_b32_e32 v160, 16, v114
	v_and_b32_e32 v161, 0xffff0000, v114
	v_lshlrev_b32_e32 v162, 16, v115
	v_and_b32_e32 v163, 0xffff0000, v115
	v_lshlrev_b32_e32 v164, 16, v116
	v_and_b32_e32 v165, 0xffff0000, v116
	v_lshlrev_b32_e32 v166, 16, v117
	v_and_b32_e32 v167, 0xffff0000, v117
	s_mov_b32 s4, 0x358637bd
	v_cvt_pk_bf16_f32 v135, v170, v171
	v_cvt_pk_bf16_f32 v105, v172, v173
	v_or_b32_e32 v36, s36, v36
	v_cvt_pk_bf16_f32 v122, v174, v175
	v_cvt_pk_bf16_f32 v123, v176, v177
	v_cvt_pk_bf16_f32 v124, v178, v179
	v_cvt_pk_bf16_f32 v125, v180, v181
	v_cvt_pk_bf16_f32 v126, v182, v183
	v_cvt_pk_bf16_f32 v127, v184, v185
	s_waitcnt vmcnt(4)
	s_waitcnt vmcnt(0)
	ds_read2st64_b32 v[100:101], v110 offset1:2
	ds_read2st64_b32 v[106:107], v110 offset0:4 offset1:6
	ds_read2st64_b32 v[108:109], v110 offset0:8 offset1:10
	ds_read2st64_b32 v[110:111], v110 offset0:12 offset1:14
	ds_read2st64_b32 v[112:113], v118 offset1:2
	ds_read2st64_b32 v[114:115], v118 offset0:4 offset1:6
	ds_read2st64_b32 v[116:117], v118 offset0:8 offset1:10
	ds_read2st64_b32 v[118:119], v118 offset0:12 offset1:14
	s_waitcnt lgkmcnt(7)
	v_mov_b32_e32 v121, v100
	v_cvt_pk_bf16_f32 v128, v186, v187
	v_cvt_pk_bf16_f32 v129, v188, v189
	s_waitcnt lgkmcnt(3)
	v_mov_b32_e32 v120, v112
	v_pk_add_f32 v[120:121], v[120:121], 0 op_sel_hi:[1,0]
	v_mov_b32_e32 v100, v113
	v_pk_add_f32 v[100:101], v[120:121], v[100:101]
	s_waitcnt lgkmcnt(2)
	v_mov_b32_e32 v112, v114
	v_mov_b32_e32 v113, v106
	v_pk_add_f32 v[100:101], v[100:101], v[112:113]
	v_mov_b32_e32 v106, v115
	v_pk_add_f32 v[100:101], v[100:101], v[106:107]
	s_waitcnt lgkmcnt(1)
	v_mov_b32_e32 v106, v116
	v_mov_b32_e32 v107, v108
	v_pk_add_f32 v[100:101], v[100:101], v[106:107]
	v_mov_b32_e32 v108, v117
	v_pk_add_f32 v[100:101], v[100:101], v[108:109]
	s_waitcnt lgkmcnt(0)
; __device__ __forceinline__ float sat8(float x) { return __builtin_amdgcn_fmed3f(x, -448.0f, 448.0f); }
; __device__ __forceinline__ unsigned pk4_fp8(float a, float b, float c, float d) { int v = 0; v = __builtin_amdgcn_cvt_pk_fp8_f32(a, b, v, false); v = __builtin_amdgcn_cvt_pk_fp8_f32(c, d, v, true); return (unsigned)v; }
; __device__ __forceinline__ void ssd_out_store(const Params& p, bf16* mix, const LAS float* ssqp, size_t trow0, int h, int lsel, int r, int hf, const unsigned (&yp)[2][2][8]) {
;     ...
;         const float rstd = rsqrtf(tot * (1.f / 512.f) + EPS);
; #pragma unroll
;     ...
;         for (int pt = 0; pt < 2; ++pt) { unsigned dq[4]; const float rs = rstd * FP8_SA;
; #pragma unroll
;             for (int q = 0; q < 4; ++q) { const unsigned u0 = yp[pt][j][2 * q], u1 = yp[pt][j][2 * q + 1];
;                 dq[q] = pk4_fp8(sat8(bflo(u0) * rs * w4[pt][q][0]), sat8(bfhi(u0) * rs * w4[pt][q][1]), sat8(bflo(u1) * rs * w4[pt][q][2]), sat8(bfhi(u1) * rs * w4[pt][q][3])); }
;             const v2u r0 = __builtin_amdgcn_permlane32_swap(dq[0], dq[2], false, false), r1 = __builtin_amdgcn_permlane32_swap(dq[1], dq[3], false, false);
;             *(v4u*)((unsigned char*)mix + t * 2048 + 1024 + h * 64 + pt * 32 + 16 * hf) = (v4u){r0.x, r0.y, r1.x, r1.y}; }
	v_mov_b32_e32 v106, v118
	v_mov_b32_e32 v107, v110
	v_pk_add_f32 v[100:101], v[100:101], v[106:107]
	v_mov_b32_e32 v110, v119
	v_pk_add_f32 v[106:107], v[100:101], v[110:111]
	v_mov_b64_e32 v[100:101], s[4:5]
	v_pk_fma_f32 v[110:111], v[106:107], s[34:35], v[100:101] op_sel_hi:[1,0,0]
	v_and_b32_e32 v112, 0xffff0000, v135
	v_mul_f32_e32 v106, 0x4b800000, v111
	v_cmp_gt_f32_e32 vcc, s97, v111
	v_cvt_pk_bf16_f32 v130, v190, v191
	v_cvt_pk_bf16_f32 v131, v192, v193
	v_cndmask_b32_e32 v106, v111, v106, vcc
	v_rsq_f32_e32 v106, v106
	v_lshlrev_b32_e32 v111, 16, v135
	v_cvt_pk_bf16_f32 v132, v194, v195
	v_cvt_pk_bf16_f32 v133, v196, v197
	v_mul_f32_e32 v107, 0x45800000, v106
	v_cndmask_b32_e32 v106, v106, v107, vcc
	v_mul_f32_e32 v113, 0x41800000, v106
	v_mul_f32_e32 v106, v113, v136
	v_mul_f32_e32 v106, v30, v106
	v_med3_f32 v107, v106, s91, v225
	v_mul_f32_e32 v106, v113, v137
	v_mul_f32_e32 v106, v31, v106
	v_med3_f32 v108, v106, s91, v225
	v_mul_f32_e32 v106, v113, v140
	v_mul_f32_e32 v106, v32, v106
	v_med3_f32 v109, v106, s91, v225
	v_cvt_pk_fp8_f32 v106, v107, v108
	v_mul_f32_e32 v107, v113, v141
	v_mul_f32_e32 v107, v33, v107
	v_mul_f32_e32 v108, v113, v143
	v_med3_f32 v107, v107, s91, v225
	v_mul_f32_e32 v108, v27, v108
	v_cvt_pk_fp8_f32 v106, v109, v107 op_sel:[0,0,1]
	v_mul_f32_e32 v107, v113, v142
	v_med3_f32 v109, v108, s91, v225
	v_mul_f32_e32 v108, v113, v144
	v_mul_f32_e32 v107, v26, v107
	v_mul_f32_e32 v108, v28, v108
	v_med3_f32 v107, v107, s91, v225
	v_med3_f32 v114, v108, s91, v225
	v_cvt_pk_fp8_f32 v108, v107, v109
	v_mul_f32_e32 v107, v113, v145
	v_mul_f32_e32 v107, v29, v107
	v_med3_f32 v107, v107, s91, v225
	v_cvt_pk_fp8_f32 v108, v114, v107 op_sel:[0,0,1]
	v_mul_f32_e32 v107, v113, v146
	v_mul_f32_e32 v107, v22, v107
	v_med3_f32 v109, v107, s91, v225
	v_mul_f32_e32 v107, v113, v147
	v_mul_f32_e32 v107, v23, v107
	v_med3_f32 v114, v107, s91, v225
	v_mul_f32_e32 v107, v113, v148
	v_mul_f32_e32 v107, v24, v107
	v_med3_f32 v115, v107, s91, v225
	v_cvt_pk_fp8_f32 v107, v109, v114
	v_mul_f32_e32 v109, v113, v149
	v_mul_f32_e32 v109, v25, v109
	v_med3_f32 v109, v109, s91, v225
	v_cvt_pk_fp8_f32 v107, v115, v109 op_sel:[0,0,1]
	v_mul_f32_e32 v109, v113, v150
	v_mul_f32_e32 v109, v18, v109
	v_med3_f32 v114, v109, s91, v225
	v_mul_f32_e32 v109, v113, v151
	v_mul_f32_e32 v109, v19, v109
	v_med3_f32 v115, v109, s91, v225
	v_mul_f32_e32 v109, v113, v152
	v_mul_f32_e32 v109, v20, v109
	v_med3_f32 v116, v109, s91, v225
	v_cvt_pk_fp8_f32 v109, v114, v115
	v_mul_f32_e32 v114, v113, v153
	v_mul_f32_e32 v114, v21, v114
	v_med3_f32 v114, v114, s91, v225
	v_cvt_pk_fp8_f32 v109, v116, v114 op_sel:[0,0,1]
	v_permlane32_swap_b32_e32 v106, v107
	v_mul_f32_e32 v112, v113, v112
	v_permlane32_swap_b32_e32 v108, v109
	global_store_dwordx4 v[102:103], v[106:109], off offset:1024
	v_mul_f32_e32 v112, v5, v112
	v_med3_f32 v112, v112, s91, v225
	v_mul_f32_e32 v106, v113, v154
	v_mul_f32_e32 v106, v14, v106
	v_med3_f32 v107, v106, s91, v225
	v_mul_f32_e32 v106, v113, v155
	v_mul_f32_e32 v106, v15, v106
	v_med3_f32 v108, v106, s91, v225
	v_mul_f32_e32 v106, v113, v156
	v_mul_f32_e32 v106, v16, v106
	v_med3_f32 v109, v106, s91, v225
	v_cvt_pk_fp8_f32 v106, v107, v108
	v_mul_f32_e32 v107, v113, v157
	v_mul_f32_e32 v107, v17, v107
	v_mul_f32_e32 v108, v113, v159
	v_med3_f32 v107, v107, s91, v225
	v_mul_f32_e32 v108, v11, v108
	v_cvt_pk_fp8_f32 v106, v109, v107 op_sel:[0,0,1]
	v_mul_f32_e32 v107, v113, v158
	v_med3_f32 v109, v108, s91, v225
	v_mul_f32_e32 v108, v113, v160
	v_mul_f32_e32 v107, v10, v107
	v_mul_f32_e32 v108, v12, v108
	v_med3_f32 v107, v107, s91, v225
	v_med3_f32 v114, v108, s91, v225
	v_cvt_pk_fp8_f32 v108, v107, v109
	v_mul_f32_e32 v107, v113, v161
	v_mul_f32_e32 v107, v13, v107
	v_med3_f32 v107, v107, s91, v225
	v_cvt_pk_fp8_f32 v108, v114, v107 op_sel:[0,0,1]
	v_mul_f32_e32 v107, v113, v162
	v_mul_f32_e32 v107, v6, v107
	v_med3_f32 v109, v107, s91, v225
	v_mul_f32_e32 v107, v113, v163
	v_mul_f32_e32 v107, v7, v107
	v_med3_f32 v114, v107, s91, v225
	v_mul_f32_e32 v107, v113, v164
	v_mul_f32_e32 v107, v8, v107
	v_med3_f32 v115, v107, s91, v225
	v_cvt_pk_fp8_f32 v107, v109, v114
	v_mul_f32_e32 v109, v113, v165
	v_mul_f32_e32 v109, v9, v109
	v_med3_f32 v109, v109, s91, v225
	v_cvt_pk_fp8_f32 v107, v115, v109 op_sel:[0,0,1]
	v_mul_f32_e32 v109, v113, v166
	v_mul_f32_e32 v109, v2, v109
	v_med3_f32 v114, v109, s91, v225
	v_mul_f32_e32 v109, v113, v167
	v_mul_f32_e32 v109, v3, v109
	v_med3_f32 v115, v109, s91, v225
	v_mul_f32_e32 v109, v113, v111
	v_mul_f32_e32 v109, v4, v109
	v_med3_f32 v111, v109, s91, v225
	v_cvt_pk_fp8_f32 v109, v114, v115
	v_cmp_gt_f32_e32 vcc, s97, v110
	v_permlane32_swap_b32_e32 v106, v107
	v_cvt_pk_fp8_f32 v109, v111, v112 op_sel:[0,0,1]
	v_mul_f32_e32 v111, 0x4b800000, v110
	v_cndmask_b32_e32 v110, v110, v111, vcc
	v_rsq_f32_e32 v110, v110
	v_permlane32_swap_b32_e32 v108, v109
	global_store_dwordx4 v[102:103], v[106:109], off offset:1056
	v_mul_f32_e32 v102, 0x45800000, v110
	v_cndmask_b32_e32 v102, v110, v102, vcc
	v_mul_f32_e32 v106, 0x41800000, v102
	v_lshlrev_b64 v[102:103], 11, v[36:37]
	v_lshlrev_b32_e32 v36, 16, v105
	v_mul_f32_e32 v36, v106, v36
	v_mul_f32_e32 v30, v30, v36
	v_med3_f32 v36, v30, s91, v225
	v_and_b32_e32 v30, 0xffff0000, v105
	v_mul_f32_e32 v30, v106, v30
	v_mul_f32_e32 v30, v31, v30
	v_med3_f32 v31, v30, s91, v225
	v_lshlrev_b32_e32 v30, 16, v122
	v_mul_f32_e32 v30, v106, v30
	v_mul_f32_e32 v30, v32, v30
	v_med3_f32 v32, v30, s91, v225
	v_and_b32_e32 v105, 0xffff0000, v122
	v_cvt_pk_fp8_f32 v30, v36, v31
	v_mul_f32_e32 v31, v106, v105
	v_mul_f32_e32 v31, v33, v31
	v_med3_f32 v31, v31, s91, v225
; __device__ __forceinline__ float sat8(float x) { return __builtin_amdgcn_fmed3f(x, -448.0f, 448.0f); }
; __device__ __forceinline__ unsigned pk4_fp8(float a, float b, float c, float d) { int v = 0; v = __builtin_amdgcn_cvt_pk_fp8_f32(a, b, v, false); v = __builtin_amdgcn_cvt_pk_fp8_f32(c, d, v, true); return (unsigned)v; }
; __device__ __forceinline__ void ssd_out_store(const Params& p, bf16* mix, const LAS float* ssqp, size_t trow0, int h, int lsel, int r, int hf, const unsigned (&yp)[2][2][8]) {
;     f32x4 w4[2][4];
; #pragma unroll
;     for (int pt = 0; pt < 2; ++pt)
; #pragma unroll
;         for (int q = 0; q < 4; ++q) w4[pt][q] = *(const f32x4*)(p.ssm_norm_w + h * 64 + pt * 32 + 8 * q + 4 * hf);
;     ...
;     for (int j = 0; j < 2; ++j) { const int lt = j == 0 ? (lsel ? 1 : 0) : (lsel ? 2 : 3); const int l = lt * 32 + r; const size_t t = trow0 + l;
;         float tot = 0.f;
; #pragma unroll
;         for (int hd = 0; hd < 8; ++hd) tot += ssqp[hd * 128 + l];
;         const float rstd = rsqrtf(tot * (1.f / 512.f) + EPS);
; #pragma unroll
;     ...
;         for (int pt = 0; pt < 2; ++pt) { unsigned dq[4]; const float rs = rstd * FP8_SA;
; #pragma unroll
;             for (int q = 0; q < 4; ++q) { const unsigned u0 = yp[pt][j][2 * q], u1 = yp[pt][j][2 * q + 1];
;                 dq[q] = pk4_fp8(sat8(bflo(u0) * rs * w4[pt][q][0]), sat8(bfhi(u0) * rs * w4[pt][q][1]), sat8(bflo(u1) * rs * w4[pt][q][2]), sat8(bfhi(u1) * rs * w4[pt][q][3])); }
;             const v2u r0 = __builtin_amdgcn_permlane32_swap(dq[0], dq[2], false, false), r1 = __builtin_amdgcn_permlane32_swap(dq[1], dq[3], false, false);
;             *(v4u*)((unsigned char*)mix + t * 2048 + 1024 + h * 64 + pt * 32 + 16 * hf) = (v4u){r0.x, r0.y, r1.x, r1.y}; }
	v_cvt_pk_fp8_f32 v30, v32, v31 op_sel:[0,0,1]
	v_lshlrev_b32_e32 v31, 16, v123
	v_mul_f32_e32 v31, v106, v31
	v_mul_f32_e32 v26, v26, v31
	v_and_b32_e32 v31, 0xffff0000, v123
	v_mul_f32_e32 v31, v106, v31
	v_mul_f32_e32 v27, v27, v31
	v_lshlrev_b32_e32 v31, 16, v124
	v_med3_f32 v26, v26, s91, v225
	v_med3_f32 v27, v27, s91, v225
	v_mul_f32_e32 v31, v106, v31
	v_mul_f32_e32 v28, v28, v31
	v_and_b32_e32 v31, 0xffff0000, v124
	v_cvt_pk_fp8_f32 v32, v26, v27
	v_mul_f32_e32 v26, v106, v31
	v_mul_f32_e32 v26, v29, v26
	v_med3_f32 v28, v28, s91, v225
	v_med3_f32 v26, v26, s91, v225
	v_cvt_pk_fp8_f32 v32, v28, v26 op_sel:[0,0,1]
	v_lshlrev_b32_e32 v26, 16, v125
	v_mul_f32_e32 v26, v106, v26
	v_mul_f32_e32 v22, v22, v26
	v_and_b32_e32 v26, 0xffff0000, v125
	v_mul_f32_e32 v26, v106, v26
	v_mul_f32_e32 v23, v23, v26
	v_lshlrev_b32_e32 v26, 16, v126
	v_med3_f32 v22, v22, s91, v225
	v_med3_f32 v23, v23, s91, v225
	v_mul_f32_e32 v26, v106, v26
	v_mul_f32_e32 v24, v24, v26
	v_and_b32_e32 v26, 0xffff0000, v126
	v_cvt_pk_fp8_f32 v31, v22, v23
	v_mul_f32_e32 v22, v106, v26
	v_mul_f32_e32 v22, v25, v22
	v_med3_f32 v24, v24, s91, v225
	v_med3_f32 v22, v22, s91, v225
	v_cvt_pk_fp8_f32 v31, v24, v22 op_sel:[0,0,1]
	v_lshlrev_b32_e32 v22, 16, v127
	v_mul_f32_e32 v22, v106, v22
	v_mul_f32_e32 v18, v18, v22
	v_and_b32_e32 v22, 0xffff0000, v127
	v_mul_f32_e32 v22, v106, v22
	v_mul_f32_e32 v19, v19, v22
	v_lshlrev_b32_e32 v22, 16, v128
	v_med3_f32 v18, v18, s91, v225
	v_med3_f32 v19, v19, s91, v225
	v_mul_f32_e32 v22, v106, v22
	v_mul_f32_e32 v20, v20, v22
	v_and_b32_e32 v22, 0xffff0000, v128
	v_cvt_pk_fp8_f32 v33, v18, v19
	v_mul_f32_e32 v18, v106, v22
	v_mul_f32_e32 v18, v21, v18
	v_med3_f32 v20, v20, s91, v225
	v_med3_f32 v18, v18, s91, v225
	v_cvt_pk_fp8_f32 v33, v20, v18 op_sel:[0,0,1]
	v_lshlrev_b32_e32 v18, 16, v129
	v_mul_f32_e32 v18, v106, v18
	v_mul_f32_e32 v14, v14, v18
	v_med3_f32 v18, v14, s91, v225
	v_and_b32_e32 v14, 0xffff0000, v129
	v_mul_f32_e32 v14, v106, v14
	v_mul_f32_e32 v14, v15, v14
	v_med3_f32 v15, v14, s91, v225
	v_lshlrev_b32_e32 v14, 16, v130
	v_mul_f32_e32 v14, v106, v14
	v_mul_f32_e32 v14, v16, v14
	v_med3_f32 v16, v14, s91, v225
	v_and_b32_e32 v19, 0xffff0000, v130
	v_cvt_pk_fp8_f32 v14, v18, v15
	v_mul_f32_e32 v15, v106, v19
	v_mul_f32_e32 v15, v17, v15
	v_med3_f32 v15, v15, s91, v225
	v_cvt_pk_fp8_f32 v14, v16, v15 op_sel:[0,0,1]
	v_lshlrev_b32_e32 v15, 16, v131
	v_mul_f32_e32 v15, v106, v15
	v_mul_f32_e32 v10, v10, v15
	v_and_b32_e32 v15, 0xffff0000, v131
	v_mul_f32_e32 v15, v106, v15
	v_mul_f32_e32 v11, v11, v15
	v_lshlrev_b32_e32 v15, 16, v132
	v_med3_f32 v10, v10, s91, v225
	v_med3_f32 v11, v11, s91, v225
	v_mul_f32_e32 v15, v106, v15
	v_mul_f32_e32 v12, v12, v15
	v_and_b32_e32 v15, 0xffff0000, v132
	v_cvt_pk_fp8_f32 v16, v10, v11
	v_mul_f32_e32 v10, v106, v15
	v_mul_f32_e32 v10, v13, v10
	v_med3_f32 v12, v12, s91, v225
	v_med3_f32 v10, v10, s91, v225
	v_cvt_pk_fp8_f32 v16, v12, v10 op_sel:[0,0,1]
	v_lshlrev_b32_e32 v10, 16, v133
	v_mul_f32_e32 v10, v106, v10
	v_mul_f32_e32 v6, v6, v10
	v_and_b32_e32 v10, 0xffff0000, v133
	v_cvt_pk_bf16_f32 v134, v198, v199
	v_mul_f32_e32 v10, v106, v10
	v_mul_f32_e32 v7, v7, v10
	v_lshlrev_b32_e32 v10, 16, v134
	v_med3_f32 v6, v6, s91, v225
	v_med3_f32 v7, v7, s91, v225
	v_mul_f32_e32 v10, v106, v10
	v_mul_f32_e32 v8, v8, v10
	v_and_b32_e32 v10, 0xffff0000, v134
	v_cvt_pk_fp8_f32 v15, v6, v7
	v_mul_f32_e32 v6, v106, v10
	v_mul_f32_e32 v6, v9, v6
	v_cvt_pk_bf16_f32 v104, v200, v201
	v_med3_f32 v8, v8, s91, v225
	v_med3_f32 v6, v6, s91, v225
	v_cvt_pk_fp8_f32 v15, v8, v6 op_sel:[0,0,1]
	v_lshlrev_b32_e32 v6, 16, v104
	v_mul_f32_e32 v6, v106, v6
	v_mul_f32_e32 v2, v2, v6
	v_and_b32_e32 v6, 0xffff0000, v104
	v_mul_f32_e32 v6, v106, v6
	v_mul_f32_e32 v3, v3, v6
	v_cvt_pk_bf16_f32 v1, v202, v203
	v_med3_f32 v2, v2, s91, v225
	v_med3_f32 v3, v3, s91, v225
	v_lshlrev_b32_e32 v6, 16, v1
	v_and_b32_e32 v1, 0xffff0000, v1
	v_cvt_pk_fp8_f32 v17, v2, v3
	v_mul_f32_e32 v6, v106, v6
	v_mul_f32_e32 v1, v106, v1
	v_mul_f32_e32 v4, v4, v6
	v_mul_f32_e32 v1, v5, v1
	v_med3_f32 v4, v4, s91, v225
	v_med3_f32 v1, v1, s91, v225
	v_cvt_pk_fp8_f32 v17, v4, v1 op_sel:[0,0,1]
	v_lshl_add_u64 v[102:103], s[20:21], 0, v[102:103]
	v_lshl_add_u64 v[102:103], v[102:103], 0, s[0:1]
	v_lshl_add_u64 v[102:103], v[102:103], 0, v[138:139]
	v_permlane32_swap_b32_e32 v30, v31
	v_permlane32_swap_b32_e32 v32, v33
	v_permlane32_swap_b32_e32 v14, v15
	v_permlane32_swap_b32_e32 v16, v17
	v_mov_b32_e32 v1, v0
	global_store_dwordx4 v[102:103], v[30:33], off offset:1024
	global_store_dwordx4 v[102:103], v[14:17], off offset:1056
	v_cvt_pk_bf16_f32 v56, v56, v57
	v_readfirstlane_b32 s0, v1
	s_ashr_i32 s1, s0, 7
	s_add_i32 s1, s1, s8
	s_bfe_u32 s6, s0, 0x10006
	s_lshl_b32 s0, s1, 6
	s_ashr_i32 s1, s0, 31
	s_lshl_b64 s[4:5], s[0:1], 2
	s_add_u32 s4, s46, s4
	v_lshrrev_b32_e32 v2, 1, v1
	s_addc_u32 s5, s47, s5
	v_and_b32_e32 v138, 16, v2
	global_load_dwordx4 v[18:21], v138, s[4:5] offset:96
	global_load_dwordx4 v[22:25], v138, s[4:5] offset:64
	global_load_dwordx4 v[26:29], v138, s[4:5] offset:32
	global_load_dwordx4 v[30:33], v138, s[4:5]
	global_load_dwordx4 v[2:5], v138, s[4:5] offset:224
	global_load_dwordx4 v[6:9], v138, s[4:5] offset:192
	global_load_dwordx4 v[10:13], v138, s[4:5] offset:160
	global_load_dwordx4 v[14:17], v138, s[4:5] offset:128
	v_and_b32_e32 v1, 31, v1
	s_cmp_eq_u32 s6, 0
	v_cvt_pk_bf16_f32 v57, v58, v59
	v_cvt_pk_bf16_f32 v58, v60, v61
	v_cvt_pk_bf16_f32 v61, v34, v35
	s_cselect_b32 s4, 0x60, 64
	v_lshl_or_b32 v34, s6, 5, v1
	v_lshl_add_u32 v35, v34, 2, s10
	v_or_b32_e32 v36, s36, v34
	v_or_b32_e32 v1, s4, v1
	v_cvt_pk_bf16_f32 v59, v62, v63
	v_cvt_pk_bf16_f32 v60, v64, v65
	v_cvt_pk_bf16_f32 v62, v98, v99
	v_cvt_pk_bf16_f32 v63, v38, v39
	v_cvt_pk_bf16_f32 v64, v40, v41
	v_cvt_pk_bf16_f32 v65, v42, v43
	v_cvt_pk_bf16_f32 v98, v44, v45
	v_cvt_pk_bf16_f32 v99, v46, v47
	v_cvt_pk_bf16_f32 v46, v66, v67
	v_cvt_pk_bf16_f32 v47, v68, v69
	s_waitcnt vmcnt(4)
; __device__ __forceinline__ unsigned pk2(float lo, float hi) { const f32x2 v = {lo, hi}; return __builtin_bit_cast(unsigned, __builtin_convertvector(v, hwbf16x2)); }
; __device__ __forceinline__ float sat8(float x) { return __builtin_amdgcn_fmed3f(x, -448.0f, 448.0f); }
; __device__ __forceinline__ float fsigmoid(float x) { return __builtin_amdgcn_rcpf(1.0f + __expf(-x)); }
; __device__ __forceinline__ void ssd_out_pass(const Params& p, const bf16* proj, const bf16* sinp  , const LAS bf16* Cs, const LAS bf16* CB, const LAS bf16* XT, ...
;     ...
;                 for (int qq = 0; qq < 2; ++qq) { const int q = 2 * pp + qq; const unsigned zx = qq == 0 ? s0.x : s0.y, zy = qq == 0 ? s1.x : s1.y;
;                     const float z0 = bflo(zx), z1 = bfhi(zx), z2 = bflo(zy), z3 = bfhi(zy);
;                     const float g0 = acc[pt][j][4 * q] * (z0 * fsigmoid(z0)), g1 = acc[pt][j][4 * q + 1] * (z1 * fsigmoid(z1)), g2 = acc[pt][j][4 * q + 2] * (z2 * fsigmoid(z2)), g3 = acc[pt][j][4 * q + 3] * (z3 * fsigmoid(z3));
;                     yp[pt][j][2 * q] = pk2(g0, g1); yp[pt][j][2 * q + 1] = pk2(g2, g3);
;                     ss += (g0 * g0 + g1 * g1) + (g2 * g2 + g3 * g3); } }
; __device__ __forceinline__ void ssd_out_store(const Params& p, bf16* mix, const LAS float* ssqp, size_t trow0, int h, int lsel, int r, int hf, const unsigned (&yp)[2][2][8]) {
;     ...
;     for (int j = 0; j < 2; ++j) { const int lt = j == 0 ? (lsel ? 1 : 0) : (lsel ? 2 : 3); const int l = lt * 32 + r; const size_t t = trow0 + l;
;         float tot = 0.f;
; #pragma unroll
;         for (int hd = 0; hd < 8; ++hd) tot += ssqp[hd * 128 + l];
;         const float rstd = rsqrtf(tot * (1.f / 512.f) + EPS);
; #pragma unroll
;     ...
;         for (int pt = 0; pt < 2; ++pt) { unsigned dq[4]; const float rs = rstd * FP8_SA;
; #pragma unroll
;             for (int q = 0; q < 4; ++q) { const unsigned u0 = yp[pt][j][2 * q], u1 = yp[pt][j][2 * q + 1];
;                 dq[q] = pk4_fp8(sat8(bflo(u0) * rs * w4[pt][q][0]), sat8(bfhi(u0) * rs * w4[pt][q][1]), sat8(bflo(u1) * rs * w4[pt][q][2]), sat8(bfhi(u1) * rs * w4[pt][q][3])); }
;             const v2u r0 = __builtin_amdgcn_permlane32_swap(dq[0], dq[2], false, false), r1 = __builtin_amdgcn_permlane32_swap(dq[1], dq[3], false, false);
;             *(v4u*)((unsigned char*)mix + t * 2048 + 1024 + h * 64 + pt * 32 + 16 * hf) = (v4u){r0.x, r0.y, r1.x, r1.y}; }
	s_waitcnt vmcnt(0)
	ds_read2st64_b32 v[38:39], v35 offset1:2
	ds_read2st64_b32 v[40:41], v35 offset0:4 offset1:6
	ds_read2st64_b32 v[42:43], v35 offset0:8 offset1:10
	ds_read2st64_b32 v[44:45], v35 offset0:12 offset1:14
	v_lshlrev_b64 v[34:35], 11, v[36:37]
	v_lshl_add_u32 v36, v1, 2, s10
	v_cvt_pk_bf16_f32 v102, v50, v51
	v_cvt_pk_bf16_f32 v105, v48, v49
	v_cvt_pk_bf16_f32 v49, v72, v73
	v_cvt_pk_bf16_f32 v50, v74, v75
	v_lshlrev_b32_e32 v72, 16, v46
	v_and_b32_e32 v73, 0xffff0000, v46
	v_lshlrev_b32_e32 v74, 16, v47
	v_and_b32_e32 v75, 0xffff0000, v47
	ds_read2st64_b32 v[46:47], v36 offset1:2
	v_cvt_pk_bf16_f32 v103, v52, v53
	v_cvt_pk_bf16_f32 v48, v70, v71
	v_cvt_pk_bf16_f32 v51, v76, v77
	v_cvt_pk_bf16_f32 v52, v78, v79
	v_cvt_pk_bf16_f32 v53, v80, v81
	v_cvt_pk_bf16_f32 v104, v54, v55
	v_cvt_pk_bf16_f32 v54, v82, v83
	v_cvt_pk_bf16_f32 v55, v84, v85
	v_cvt_pk_bf16_f32 v66, v86, v87
	v_lshlrev_b32_e32 v76, 16, v48
	v_and_b32_e32 v77, 0xffff0000, v48
	v_lshlrev_b32_e32 v78, 16, v49
	v_and_b32_e32 v79, 0xffff0000, v49
	v_lshlrev_b32_e32 v80, 16, v50
	v_and_b32_e32 v81, 0xffff0000, v50
	v_lshlrev_b32_e32 v82, 16, v51
	v_and_b32_e32 v83, 0xffff0000, v51
	v_lshlrev_b32_e32 v84, 16, v52
	v_and_b32_e32 v85, 0xffff0000, v52
	v_lshlrev_b32_e32 v86, 16, v53
	v_and_b32_e32 v87, 0xffff0000, v53
	ds_read2st64_b32 v[48:49], v36 offset0:4 offset1:6
	ds_read2st64_b32 v[50:51], v36 offset0:8 offset1:10
	ds_read2st64_b32 v[52:53], v36 offset0:12 offset1:14
	v_cvt_pk_bf16_f32 v67, v88, v89
	v_cvt_pk_bf16_f32 v68, v90, v91
	v_lshlrev_b32_e32 v88, 16, v54
	v_and_b32_e32 v89, 0xffff0000, v54
	v_lshlrev_b32_e32 v90, 16, v55
	v_and_b32_e32 v91, 0xffff0000, v55
	s_waitcnt lgkmcnt(3)
	v_mov_b32_e32 v54, v46
	v_mov_b32_e32 v55, v38
	v_pk_add_f32 v[54:55], v[54:55], 0 op_sel_hi:[1,0]
	v_mov_b32_e32 v38, v47
	v_pk_add_f32 v[38:39], v[54:55], v[38:39]
	s_waitcnt lgkmcnt(2)
	v_mov_b32_e32 v46, v48
	v_mov_b32_e32 v47, v40
	v_pk_add_f32 v[38:39], v[38:39], v[46:47]
	v_mov_b32_e32 v40, v49
	v_pk_add_f32 v[38:39], v[38:39], v[40:41]
	s_waitcnt lgkmcnt(1)
	v_mov_b32_e32 v40, v50
	v_mov_b32_e32 v41, v42
	v_pk_add_f32 v[38:39], v[38:39], v[40:41]
	v_mov_b32_e32 v42, v51
	v_pk_add_f32 v[38:39], v[38:39], v[42:43]
	s_waitcnt lgkmcnt(0)
	v_mov_b32_e32 v40, v52
	v_mov_b32_e32 v41, v44
	v_pk_add_f32 v[38:39], v[38:39], v[40:41]
	v_mov_b32_e32 v44, v53
	v_pk_add_f32 v[38:39], v[38:39], v[44:45]
	v_lshl_add_u64 v[34:35], s[20:21], 0, v[34:35]
	v_pk_fma_f32 v[42:43], v[38:39], s[34:35], v[100:101] op_sel_hi:[1,0,0]
	v_lshl_add_u64 v[34:35], v[34:35], 0, s[0:1]
	v_mul_f32_e32 v36, 0x4b800000, v43
	v_cmp_gt_f32_e32 vcc, s97, v43
	v_lshl_add_u64 v[34:35], v[34:35], 0, v[138:139]
	v_cvt_pk_bf16_f32 v69, v92, v93
	v_cndmask_b32_e32 v36, v43, v36, vcc
	v_rsq_f32_e32 v38, v36
	v_or_b32_e32 v36, s36, v1
	v_lshlrev_b32_e32 v92, 16, v66
	v_and_b32_e32 v66, 0xffff0000, v66
	v_mul_f32_e32 v1, 0x45800000, v38
	v_cndmask_b32_e32 v1, v38, v1, vcc
	v_mul_f32_e32 v1, 0x41800000, v1
	v_mul_f32_e32 v38, v1, v72
	v_mul_f32_e32 v38, v30, v38
	v_med3_f32 v39, v38, s91, v225
	v_mul_f32_e32 v38, v1, v73
	v_mul_f32_e32 v38, v31, v38
	v_med3_f32 v40, v38, s91, v225
	v_mul_f32_e32 v38, v1, v74
	v_mul_f32_e32 v38, v32, v38
	v_med3_f32 v41, v38, s91, v225
	v_cvt_pk_fp8_f32 v38, v39, v40
	v_mul_f32_e32 v39, v1, v75
	v_mul_f32_e32 v39, v33, v39
	v_mul_f32_e32 v40, v1, v77
	v_med3_f32 v39, v39, s91, v225
	v_mul_f32_e32 v40, v27, v40
	v_cvt_pk_fp8_f32 v38, v41, v39 op_sel:[0,0,1]
	v_mul_f32_e32 v39, v1, v76
	v_med3_f32 v41, v40, s91, v225
	v_mul_f32_e32 v40, v1, v78
	v_mul_f32_e32 v39, v26, v39
	v_mul_f32_e32 v40, v28, v40
	v_med3_f32 v39, v39, s91, v225
	v_med3_f32 v45, v40, s91, v225
	v_cvt_pk_fp8_f32 v40, v39, v41
	v_mul_f32_e32 v39, v1, v79
	v_mul_f32_e32 v39, v29, v39
	v_med3_f32 v39, v39, s91, v225
	v_cvt_pk_fp8_f32 v40, v45, v39 op_sel:[0,0,1]
	v_mul_f32_e32 v39, v1, v80
	v_mul_f32_e32 v39, v22, v39
	v_med3_f32 v41, v39, s91, v225
	v_mul_f32_e32 v39, v1, v81
	v_mul_f32_e32 v39, v23, v39
	v_med3_f32 v45, v39, s91, v225
	v_mul_f32_e32 v39, v1, v82
	v_mul_f32_e32 v39, v24, v39
	v_med3_f32 v46, v39, s91, v225
	v_cvt_pk_fp8_f32 v39, v41, v45
	v_mul_f32_e32 v41, v1, v83
	v_mul_f32_e32 v41, v25, v41
	v_med3_f32 v41, v41, s91, v225
	v_cvt_pk_fp8_f32 v39, v46, v41 op_sel:[0,0,1]
	v_mul_f32_e32 v41, v1, v84
	v_mul_f32_e32 v41, v18, v41
	v_med3_f32 v45, v41, s91, v225
	v_mul_f32_e32 v41, v1, v85
	v_mul_f32_e32 v41, v19, v41
	v_med3_f32 v46, v41, s91, v225
	v_mul_f32_e32 v41, v1, v86
	v_mul_f32_e32 v41, v20, v41
	v_med3_f32 v47, v41, s91, v225
	v_cvt_pk_fp8_f32 v41, v45, v46
	v_mul_f32_e32 v45, v1, v87
	v_mul_f32_e32 v45, v21, v45
	v_med3_f32 v45, v45, s91, v225
	v_cvt_pk_fp8_f32 v41, v47, v45 op_sel:[0,0,1]
	v_permlane32_swap_b32_e32 v38, v39
	v_lshlrev_b32_e32 v93, 16, v67
	v_permlane32_swap_b32_e32 v40, v41
	global_store_dwordx4 v[34:35], v[38:41], off offset:1024
	v_and_b32_e32 v67, 0xffff0000, v67
	v_cvt_pk_bf16_f32 v70, v94, v95
	v_mul_f32_e32 v38, v1, v88
	v_mul_f32_e32 v38, v14, v38
	v_med3_f32 v39, v38, s91, v225
	v_mul_f32_e32 v38, v1, v89
	v_mul_f32_e32 v38, v15, v38
	v_med3_f32 v40, v38, s91, v225
	v_mul_f32_e32 v38, v1, v90
	v_mul_f32_e32 v38, v16, v38
	v_med3_f32 v41, v38, s91, v225
	v_cvt_pk_fp8_f32 v38, v39, v40
	v_mul_f32_e32 v39, v1, v91
	v_mul_f32_e32 v39, v17, v39
	v_mul_f32_e32 v40, v1, v66
	v_med3_f32 v39, v39, s91, v225
	v_mul_f32_e32 v40, v11, v40
	v_cvt_pk_fp8_f32 v38, v41, v39 op_sel:[0,0,1]
	v_mul_f32_e32 v39, v1, v92
	v_med3_f32 v41, v40, s91, v225
	v_mul_f32_e32 v40, v1, v93
	v_mul_f32_e32 v39, v10, v39
	v_mul_f32_e32 v40, v12, v40
	v_med3_f32 v39, v39, s91, v225
	v_med3_f32 v45, v40, s91, v225
; __device__ __forceinline__ float sat8(float x) { return __builtin_amdgcn_fmed3f(x, -448.0f, 448.0f); }
; __device__ __forceinline__ unsigned pk4_fp8(float a, float b, float c, float d) { int v = 0; v = __builtin_amdgcn_cvt_pk_fp8_f32(a, b, v, false); v = __builtin_amdgcn_cvt_pk_fp8_f32(c, d, v, true); return (unsigned)v; }
; __device__ __forceinline__ void ssd_out_store(const Params& p, bf16* mix, const LAS float* ssqp, size_t trow0, int h, int lsel, int r, int hf, const unsigned (&yp)[2][2][8]) {
;     ...
;     for (int j = 0; j < 2; ++j) { const int lt = j == 0 ? (lsel ? 1 : 0) : (lsel ? 2 : 3); const int l = lt * 32 + r; const size_t t = trow0 + l;
;         float tot = 0.f;
; #pragma unroll
;         for (int hd = 0; hd < 8; ++hd) tot += ssqp[hd * 128 + l];
;         const float rstd = rsqrtf(tot * (1.f / 512.f) + EPS);
; #pragma unroll
;     ...
;         for (int pt = 0; pt < 2; ++pt) { unsigned dq[4]; const float rs = rstd * FP8_SA;
; #pragma unroll
;             for (int q = 0; q < 4; ++q) { const unsigned u0 = yp[pt][j][2 * q], u1 = yp[pt][j][2 * q + 1];
;                 dq[q] = pk4_fp8(sat8(bflo(u0) * rs * w4[pt][q][0]), sat8(bfhi(u0) * rs * w4[pt][q][1]), sat8(bflo(u1) * rs * w4[pt][q][2]), sat8(bfhi(u1) * rs * w4[pt][q][3])); }
;             const v2u r0 = __builtin_amdgcn_permlane32_swap(dq[0], dq[2], false, false), r1 = __builtin_amdgcn_permlane32_swap(dq[1], dq[3], false, false);
;             *(v4u*)((unsigned char*)mix + t * 2048 + 1024 + h * 64 + pt * 32 + 16 * hf) = (v4u){r0.x, r0.y, r1.x, r1.y}; }
; __device__ __forceinline__ void phase_ssd_out(const Params& p, LAS unsigned char* lds, int G, int lane, int wave) {
;     ...
;     for (int item = blockIdx.x; item < NB * 64 * 2; item += G) {
	v_cvt_pk_fp8_f32 v40, v39, v41
	v_mul_f32_e32 v39, v1, v67
	v_mul_f32_e32 v39, v13, v39
	v_lshlrev_b32_e32 v94, 16, v68
	v_med3_f32 v39, v39, s91, v225
	v_cvt_pk_fp8_f32 v40, v45, v39 op_sel:[0,0,1]
	v_mul_f32_e32 v39, v1, v94
	v_and_b32_e32 v68, 0xffff0000, v68
	v_mul_f32_e32 v39, v6, v39
	v_med3_f32 v41, v39, s91, v225
	v_mul_f32_e32 v39, v1, v68
	v_lshlrev_b32_e32 v95, 16, v69
	v_mul_f32_e32 v39, v7, v39
	v_med3_f32 v45, v39, s91, v225
	v_mul_f32_e32 v39, v1, v95
	v_mul_f32_e32 v39, v8, v39
	v_med3_f32 v46, v39, s91, v225
	v_and_b32_e32 v69, 0xffff0000, v69
	v_cvt_pk_fp8_f32 v39, v41, v45
	v_mul_f32_e32 v41, v1, v69
	v_mul_f32_e32 v41, v9, v41
	v_cvt_pk_bf16_f32 v71, v96, v97
	v_lshlrev_b32_e32 v96, 16, v70
	v_med3_f32 v41, v41, s91, v225
	v_cvt_pk_fp8_f32 v39, v46, v41 op_sel:[0,0,1]
	v_mul_f32_e32 v41, v1, v96
	v_and_b32_e32 v70, 0xffff0000, v70
	v_mul_f32_e32 v41, v2, v41
	v_med3_f32 v45, v41, s91, v225
	v_mul_f32_e32 v41, v1, v70
	v_lshlrev_b32_e32 v43, 16, v71
	v_mul_f32_e32 v41, v3, v41
	v_med3_f32 v46, v41, s91, v225
	v_mul_f32_e32 v41, v1, v43
	v_mul_f32_e32 v41, v4, v41
	v_med3_f32 v43, v41, s91, v225
	v_and_b32_e32 v44, 0xffff0000, v71
	v_cvt_pk_fp8_f32 v41, v45, v46
	v_mul_f32_e32 v1, v1, v44
	v_mul_f32_e32 v1, v5, v1
	v_med3_f32 v1, v1, s91, v225
	v_cvt_pk_fp8_f32 v41, v43, v1 op_sel:[0,0,1]
	v_mul_f32_e32 v1, 0x4b800000, v42
	v_cmp_gt_f32_e32 vcc, s97, v42
	v_permlane32_swap_b32_e32 v38, v39
	s_nop 0
	v_cndmask_b32_e32 v1, v42, v1, vcc
	v_rsq_f32_e32 v1, v1
	v_permlane32_swap_b32_e32 v40, v41
	global_store_dwordx4 v[34:35], v[38:41], off offset:1056
	v_mul_f32_e32 v34, 0x45800000, v1
	v_cndmask_b32_e32 v1, v1, v34, vcc
	v_mul_f32_e32 v1, 0x41800000, v1
	v_lshlrev_b64 v[34:35], 11, v[36:37]
	v_lshlrev_b32_e32 v36, 16, v102
	v_mul_f32_e32 v36, v1, v36
	v_mul_f32_e32 v30, v30, v36
	v_med3_f32 v36, v30, s91, v225
	v_and_b32_e32 v30, 0xffff0000, v102
	v_mul_f32_e32 v30, v1, v30
	v_mul_f32_e32 v30, v31, v30
	v_med3_f32 v31, v30, s91, v225
	v_lshlrev_b32_e32 v30, 16, v103
	v_mul_f32_e32 v30, v1, v30
	v_mul_f32_e32 v30, v32, v30
	v_med3_f32 v32, v30, s91, v225
	v_and_b32_e32 v37, 0xffff0000, v103
	v_cvt_pk_fp8_f32 v30, v36, v31
	v_mul_f32_e32 v31, v1, v37
	v_mul_f32_e32 v31, v33, v31
	v_med3_f32 v31, v31, s91, v225
	v_cvt_pk_fp8_f32 v30, v32, v31 op_sel:[0,0,1]
	v_lshlrev_b32_e32 v31, 16, v104
	v_mul_f32_e32 v31, v1, v31
	v_mul_f32_e32 v26, v26, v31
	v_and_b32_e32 v31, 0xffff0000, v104
	v_mul_f32_e32 v31, v1, v31
	v_mul_f32_e32 v27, v27, v31
	v_lshlrev_b32_e32 v31, 16, v56
	v_med3_f32 v26, v26, s91, v225
	v_med3_f32 v27, v27, s91, v225
	v_mul_f32_e32 v31, v1, v31
	v_mul_f32_e32 v28, v28, v31
	v_and_b32_e32 v31, 0xffff0000, v56
	v_cvt_pk_fp8_f32 v32, v26, v27
	v_mul_f32_e32 v26, v1, v31
	v_mul_f32_e32 v26, v29, v26
	v_med3_f32 v28, v28, s91, v225
	v_med3_f32 v26, v26, s91, v225
	v_cvt_pk_fp8_f32 v32, v28, v26 op_sel:[0,0,1]
	v_lshlrev_b32_e32 v26, 16, v57
	v_mul_f32_e32 v26, v1, v26
	v_mul_f32_e32 v22, v22, v26
	v_and_b32_e32 v26, 0xffff0000, v57
	v_mul_f32_e32 v26, v1, v26
	v_mul_f32_e32 v23, v23, v26
	v_lshlrev_b32_e32 v26, 16, v58
	v_med3_f32 v22, v22, s91, v225
	v_med3_f32 v23, v23, s91, v225
	v_mul_f32_e32 v26, v1, v26
	v_mul_f32_e32 v24, v24, v26
	v_and_b32_e32 v26, 0xffff0000, v58
	v_cvt_pk_fp8_f32 v31, v22, v23
	v_mul_f32_e32 v22, v1, v26
	v_mul_f32_e32 v22, v25, v22
	v_med3_f32 v24, v24, s91, v225
	v_med3_f32 v22, v22, s91, v225
	v_cvt_pk_fp8_f32 v31, v24, v22 op_sel:[0,0,1]
	v_lshlrev_b32_e32 v22, 16, v59
	v_mul_f32_e32 v22, v1, v22
	v_mul_f32_e32 v18, v18, v22
	v_and_b32_e32 v22, 0xffff0000, v59
	v_mul_f32_e32 v22, v1, v22
	v_mul_f32_e32 v19, v19, v22
	v_lshlrev_b32_e32 v22, 16, v60
	v_med3_f32 v18, v18, s91, v225
	v_med3_f32 v19, v19, s91, v225
	v_mul_f32_e32 v22, v1, v22
	v_mul_f32_e32 v20, v20, v22
	v_and_b32_e32 v22, 0xffff0000, v60
	v_cvt_pk_fp8_f32 v33, v18, v19
	v_mul_f32_e32 v18, v1, v22
	v_mul_f32_e32 v18, v21, v18
	v_med3_f32 v20, v20, s91, v225
	v_med3_f32 v18, v18, s91, v225
	v_cvt_pk_fp8_f32 v33, v20, v18 op_sel:[0,0,1]
	v_lshlrev_b32_e32 v18, 16, v61
	v_mul_f32_e32 v18, v1, v18
	v_mul_f32_e32 v14, v14, v18
	v_med3_f32 v18, v14, s91, v225
	v_and_b32_e32 v14, 0xffff0000, v61
	v_mul_f32_e32 v14, v1, v14
	v_mul_f32_e32 v14, v15, v14
	v_med3_f32 v15, v14, s91, v225
	v_lshlrev_b32_e32 v14, 16, v62
	v_mul_f32_e32 v14, v1, v14
	v_mul_f32_e32 v14, v16, v14
	v_med3_f32 v16, v14, s91, v225
	v_and_b32_e32 v19, 0xffff0000, v62
	v_cvt_pk_fp8_f32 v14, v18, v15
	v_mul_f32_e32 v15, v1, v19
	v_mul_f32_e32 v15, v17, v15
	v_med3_f32 v15, v15, s91, v225
	v_cvt_pk_fp8_f32 v14, v16, v15 op_sel:[0,0,1]
	v_lshlrev_b32_e32 v15, 16, v63
	v_mul_f32_e32 v15, v1, v15
	v_mul_f32_e32 v10, v10, v15
	v_and_b32_e32 v15, 0xffff0000, v63
	v_mul_f32_e32 v15, v1, v15
	v_mul_f32_e32 v11, v11, v15
	v_lshlrev_b32_e32 v15, 16, v64
	v_med3_f32 v10, v10, s91, v225
	v_med3_f32 v11, v11, s91, v225
	v_mul_f32_e32 v15, v1, v15
	v_mul_f32_e32 v12, v12, v15
	v_and_b32_e32 v15, 0xffff0000, v64
	v_cvt_pk_fp8_f32 v16, v10, v11
	v_mul_f32_e32 v10, v1, v15
	v_mul_f32_e32 v10, v13, v10
	v_med3_f32 v12, v12, s91, v225
	v_med3_f32 v10, v10, s91, v225
	v_cvt_pk_fp8_f32 v16, v12, v10 op_sel:[0,0,1]
	v_lshlrev_b32_e32 v10, 16, v65
	v_mul_f32_e32 v10, v1, v10
	v_mul_f32_e32 v6, v6, v10
	v_and_b32_e32 v10, 0xffff0000, v65
	v_mul_f32_e32 v10, v1, v10
	v_mul_f32_e32 v7, v7, v10
	v_lshlrev_b32_e32 v10, 16, v98
	v_med3_f32 v6, v6, s91, v225
	v_med3_f32 v7, v7, s91, v225
	v_mul_f32_e32 v10, v1, v10
	v_mul_f32_e32 v8, v8, v10
	v_and_b32_e32 v10, 0xffff0000, v98
	v_cvt_pk_fp8_f32 v15, v6, v7
	v_mul_f32_e32 v6, v1, v10
	v_mul_f32_e32 v6, v9, v6
	v_med3_f32 v8, v8, s91, v225
	v_med3_f32 v6, v6, s91, v225
	v_cvt_pk_fp8_f32 v15, v8, v6 op_sel:[0,0,1]
	v_lshlrev_b32_e32 v6, 16, v99
	v_mul_f32_e32 v6, v1, v6
	v_mul_f32_e32 v2, v2, v6
	v_and_b32_e32 v6, 0xffff0000, v99
	v_mul_f32_e32 v6, v1, v6
	v_mul_f32_e32 v3, v3, v6
	v_lshlrev_b32_e32 v6, 16, v105
	v_med3_f32 v2, v2, s91, v225
	v_med3_f32 v3, v3, s91, v225
	v_mul_f32_e32 v6, v1, v6
	v_mul_f32_e32 v4, v4, v6
	v_and_b32_e32 v6, 0xffff0000, v105
	v_cvt_pk_fp8_f32 v17, v2, v3
	v_mul_f32_e32 v1, v1, v6
	v_mul_f32_e32 v1, v5, v1
	v_med3_f32 v4, v4, s91, v225
	v_med3_f32 v1, v1, s91, v225
	v_cvt_pk_fp8_f32 v17, v4, v1 op_sel:[0,0,1]
	v_lshl_add_u64 v[34:35], s[20:21], 0, v[34:35]
	v_lshl_add_u64 v[34:35], v[34:35], 0, s[0:1]
	s_add_i32 s2, s2, s96
	s_mov_b64 s[4:5], s[40:41]
	v_lshl_add_u64 v[34:35], v[34:35], 0, v[138:139]
	v_permlane32_swap_b32_e32 v30, v31
	v_permlane32_swap_b32_e32 v32, v33
	v_permlane32_swap_b32_e32 v14, v15
	v_permlane32_swap_b32_e32 v16, v17
	s_cmpk_gt_i32 s2, 0x1ff
	s_mov_b64 s[6:7], s[42:43]
	global_store_dwordx4 v[34:35], v[30:33], off offset:1024
	global_store_dwordx4 v[34:35], v[14:17], off offset:1056
	s_mov_b64 s[8:9], s[44:45]
	s_mov_b64 s[10:11], s[46:47]
	s_cbranch_scc1 .LBB0_501

; __device__ __forceinline__ float sat8(float x) { return __builtin_amdgcn_fmed3f(x, -448.0f, 448.0f); }
; __device__ __forceinline__ void phase_router(const Params& p, LAS unsigned char* lds, unsigned* ctl, int G, int wave, int lane) {
;     ...
;             for (int u = 0; u < 4; ++u) {
;                 float hv[8];
; #pragma unroll
;                 for (int k = 0; k < 4; ++k) { hv[k] = xc[u][0][k] * rstd * gq[u][0][k]; hv[4 + k] = xc[u][1][k] * rstd * gq[u][1][k]; }
;                 { const unsigned flo = pk4_fp8(sat8(hv[0] * FP8_SA), sat8(hv[1] * FP8_SA), sat8(hv[2] * FP8_SA), sat8(hv[3] * FP8_SA)), fhi = pk4_fp8(sat8(hv[4] * FP8_SA), sat8(hv[5] * FP8_SA), sat8(hv[6] * FP8_SA), sat8(hv[7] * FP8_SA));
;                   if ((u & 1) == 0) { hlo = flo; hhi = fhi; }
;                   else { const v2u r0 = __builtin_amdgcn_permlane16_swap(hlo, flo, false, false), r1 = __builtin_amdgcn_permlane16_swap(hhi, fhi, false, false);
;                          *(v4u*)(hf + (size_t)tok * D + 32 * (j4 + u - 1 + (kq & 1)) + 16 * (kq >> 1)) = (v4u){r0.x, r1.x, r0.y, r1.y}; } }
;                 v4u ah, al;
;                 ah.x = pk2(hv[0], hv[1]); ah.y = pk2(hv[2], hv[3]); ah.z = pk2(hv[4], hv[5]); ah.w = pk2(hv[6], hv[7]);
;                 al.x = pk2(hv[0] - bflo(ah.x), hv[1] - bfhi(ah.x)); al.y = pk2(hv[2] - bflo(ah.y), hv[3] - bfhi(ah.y)); al.z = pk2(hv[4] - bflo(ah.z), hv[5] - bfhi(ah.z)); al.w = pk2(hv[6] - bflo(ah.w), hv[7] - bfhi(ah.w));
;                 const bf16x8 fah = __builtin_bit_cast(bf16x8, ah), fal = __builtin_bit_cast(bf16x8, al);
;                 acc0 = __builtin_amdgcn_mfma_f32_16x16x32_bf16(fah, __builtin_bit_cast(bf16x8, wf[u][0][0]), acc0, 0, 0, 0);
;                 acc0 = __builtin_amdgcn_mfma_f32_16x16x32_bf16(fah, __builtin_bit_cast(bf16x8, wf[u][0][1]), acc0, 0, 0, 0);
;                 acc0 = __builtin_amdgcn_mfma_f32_16x16x32_bf16(fal, __builtin_bit_cast(bf16x8, wf[u][0][0]), acc0, 0, 0, 0);
;                 acc1 = __builtin_amdgcn_mfma_f32_16x16x32_bf16(fah, __builtin_bit_cast(bf16x8, wf[u][1][0]), acc1, 0, 0, 0);
;                 acc1 = __builtin_amdgcn_mfma_f32_16x16x32_bf16(fah, __builtin_bit_cast(bf16x8, wf[u][1][1]), acc1, 0, 0, 0);
;                 acc1 = __builtin_amdgcn_mfma_f32_16x16x32_bf16(fal, __builtin_bit_cast(bf16x8, wf[u][1][0]), acc1, 0, 0, 0);
;             }
.LBB0_652:
	v_lshlrev_b32_e32 v194, 16, v110
	v_and_b32_e32 v195, 0xffff0000, v110
	v_pk_mul_f32 v[214:215], v[176:177], v[194:195]
	v_lshlrev_b32_e32 v196, 16, v111
	s_waitcnt lgkmcnt(0)
	v_pk_mul_f32 v[194:195], v[214:215], v[134:135]
	v_and_b32_e32 v197, 0xffff0000, v111
	v_mul_f32_e32 v110, 0x41800000, v194
	v_cvt_pk_bf16_f32 v194, v194, v195
	v_lshlrev_b32_e32 v216, 16, v194
	v_and_b32_e32 v217, 0xffff0000, v194
	v_pk_mul_f32 v[196:197], v[176:177], v[196:197]
	v_med3_f32 v111, v110, s35, v187
	v_mul_f32_e32 v110, 0x41800000, v195
	v_pk_fma_f32 v[134:135], v[214:215], v[134:135], v[216:217] neg_lo:[0,0,1] neg_hi:[0,0,1]
	v_pk_mul_f32 v[214:215], v[196:197], v[136:137]
	v_med3_f32 v155, v110, s35, v187
	v_cvt_pk_bf16_f32 v195, v214, v215
	v_cvt_pk_fp8_f32 v110, v111, v155
	v_cvt_pk_bf16_f32 v134, v134, v135
	v_mul_f32_e32 v111, 0x41800000, v214
	v_mul_f32_e32 v135, 0x41800000, v215
	v_lshlrev_b32_e32 v214, 16, v195
	v_and_b32_e32 v215, 0xffff0000, v195
	v_lshlrev_b32_e32 v198, 16, v112
	v_and_b32_e32 v199, 0xffff0000, v112
	v_lshlrev_b32_e32 v112, 16, v113
	v_and_b32_e32 v113, 0xffff0000, v113
	v_pk_fma_f32 v[136:137], v[196:197], v[136:137], v[214:215] neg_lo:[0,0,1] neg_hi:[0,0,1]
	v_med3_f32 v155, v135, s35, v187
	v_cvt_pk_bf16_f32 v135, v136, v137
	v_pk_mul_f32 v[136:137], v[176:177], v[198:199]
	v_pk_mul_f32 v[112:113], v[176:177], v[112:113]
	v_pk_mul_f32 v[198:199], v[136:137], v[126:127]
	v_pk_mul_f32 v[216:217], v[112:113], v[128:129]
	v_cvt_pk_bf16_f32 v196, v198, v199
	v_cvt_pk_bf16_f32 v197, v216, v217
	v_lshlrev_b32_e32 v214, 16, v196
	v_and_b32_e32 v215, 0xffff0000, v196
	v_pk_fma_f32 v[126:127], v[136:137], v[126:127], v[214:215] neg_lo:[0,0,1] neg_hi:[0,0,1]
	v_med3_f32 v111, v111, s35, v187
	v_cvt_pk_bf16_f32 v136, v126, v127
	v_lshlrev_b32_e32 v126, 16, v197
	v_and_b32_e32 v127, 0xffff0000, v197
	v_pk_fma_f32 v[112:113], v[112:113], v[128:129], v[126:127] neg_lo:[0,0,1] neg_hi:[0,0,1]
	v_cvt_pk_fp8_f32 v110, v111, v155 op_sel:[0,0,1]
	v_mul_f32_e32 v111, 0x41800000, v198
	v_mfma_f32_16x16x32_bf16 v[66:69], v[194:197], v[114:117], v[66:69]
	v_cvt_pk_bf16_f32 v137, v112, v113
	v_med3_f32 v112, v111, s35, v187
	v_mul_f32_e32 v111, 0x41800000, v199
	v_mfma_f32_16x16x32_bf16 v[62:65], v[194:197], v[122:125], v[62:65]
	v_med3_f32 v113, v111, s35, v187
	v_cvt_pk_fp8_f32 v111, v112, v113
	v_lshlrev_b32_e32 v206, 16, v109
	v_and_b32_e32 v207, 0xffff0000, v109
	v_mfma_f32_16x16x32_bf16 v[66:69], v[194:197], v[118:121], v[66:69]
	v_mul_f32_e32 v112, 0x41800000, v216
	v_mul_f32_e32 v113, 0x41800000, v217
	v_pk_mul_f32 v[126:127], v[176:177], v[206:207]
	v_mfma_f32_16x16x32_bf16 v[62:65], v[194:197], v[130:133], v[62:65]
	v_lshlrev_b32_e32 v204, 16, v108
	v_and_b32_e32 v205, 0xffff0000, v108
	v_med3_f32 v112, v112, s35, v187
	v_med3_f32 v113, v113, s35, v187
	v_pk_mul_f32 v[128:129], v[126:127], v[88:89]
	v_cvt_pk_fp8_f32 v111, v112, v113 op_sel:[0,0,1]
	v_pk_mul_f32 v[120:121], v[176:177], v[204:205]
	v_mul_f32_e32 v112, 0x41800000, v128
	v_lshlrev_b32_e32 v202, 16, v107
	v_and_b32_e32 v203, 0xffff0000, v107
	v_mfma_f32_16x16x32_bf16 v[66:69], v[134:137], v[114:117], v[66:69]
	v_mul_f32_e64 v116, v120, v86
	v_mul_f32_e64 v117, v121, v87
	v_med3_f32 v130, v112, s35, v187
	v_mul_f32_e32 v112, 0x41800000, v129
	v_lshlrev_b32_e32 v200, 16, v106
	v_and_b32_e32 v201, 0xffff0000, v106
	v_mfma_f32_16x16x32_bf16 v[62:65], v[134:137], v[122:125], v[62:65]
	v_mul_f32_e64 v122, v176, v202
	v_mul_f32_e64 v123, v177, v203
	v_med3_f32 v131, v112, s35, v187
	v_mul_f32_e32 v112, 0x41800000, v116
	v_mul_f32_e32 v113, 0x41800000, v117
	v_pk_mul_f32 v[118:119], v[176:177], v[200:201]
	v_pk_mul_f32 v[124:125], v[122:123], v[96:97]
	v_med3_f32 v112, v112, s35, v187
	v_med3_f32 v132, v113, s35, v187
	v_mov_b32_e32 v113, 0
	v_pk_mul_f32 v[114:115], v[118:119], v[94:95]
	v_cvt_pk_fp8_f32 v113, v112, v132
	v_mul_f32_e32 v112, 0x41800000, v124
	v_med3_f32 v132, v112, s35, v187
	v_mul_f32_e32 v112, 0x41800000, v114
	v_med3_f32 v133, v112, s35, v187
	v_mul_f32_e32 v112, 0x41800000, v115
	v_cvt_pk_bf16_f32 v114, v114, v115
	v_cvt_pk_bf16_f32 v115, v124, v125
	v_cvt_pk_bf16_f32 v116, v116, v117
	v_cvt_pk_bf16_f32 v117, v128, v129
	v_lshlrev_b32_e32 v128, 16, v114
	v_and_b32_e32 v129, 0xffff0000, v114
	v_pk_fma_f32 v[94:95], v[118:119], v[94:95], v[128:129] neg_lo:[0,0,1] neg_hi:[0,0,1]
	v_lshlrev_b32_e32 v118, 16, v115
	v_and_b32_e32 v119, 0xffff0000, v115
	v_pk_fma_f32 v[96:97], v[122:123], v[96:97], v[118:119] neg_lo:[0,0,1] neg_hi:[0,0,1]
	v_cvt_pk_bf16_f32 v94, v94, v95
	v_cvt_pk_bf16_f32 v95, v96, v97
	v_lshlrev_b32_e32 v96, 16, v116
	v_and_b32_e32 v97, 0xffff0000, v116
	v_pk_fma_f32 v[86:87], v[120:121], v[86:87], v[96:97] neg_lo:[0,0,1] neg_hi:[0,0,1]
	v_mfma_f32_16x16x32_bf16 v[66:69], v[114:117], v[74:77], v[66:69]
	v_cvt_pk_bf16_f32 v96, v86, v87
	v_lshlrev_b32_e32 v86, 16, v117
	v_and_b32_e32 v87, 0xffff0000, v117
	v_mfma_f32_16x16x32_bf16 v[62:65], v[114:117], v[82:85], v[62:65]
	v_fma_f32 v86, v126, v88, -v86
	v_fma_f32 v87, v127, v89, -v87
	v_lshlrev_b32_e32 v208, 16, v102
	v_cvt_pk_bf16_f32 v97, v86, v87
	v_mfma_f32_16x16x32_bf16 v[66:69], v[114:117], v[78:81], v[66:69]
	v_and_b32_e32 v209, 0xffff0000, v102
	v_pk_mul_f32 v[78:79], v[176:177], v[208:209]
	v_lshlrev_b32_e32 v210, 16, v103
	v_mfma_f32_16x16x32_bf16 v[62:65], v[114:117], v[90:93], v[62:65]
	v_and_b32_e32 v211, 0xffff0000, v103
	v_med3_f32 v134, v112, s35, v187
	v_mfma_f32_16x16x32_bf16 v[66:69], v[94:97], v[74:77], v[66:69]
	v_mul_f32_e64 v76, v78, v70
	v_mul_f32_e64 v77, v79, v71
	v_cvt_pk_fp8_f32 v112, v133, v134
	v_mul_f32_e32 v74, 0x41800000, v76
; __device__ __forceinline__ void phase_router(const Params& p, LAS unsigned char* lds, unsigned* ctl, int G, int wave, int lane) {
;     ...
;             for (int u = 0; u < 4; ++u) {
;                 float hv[8];
; #pragma unroll
;                 for (int k = 0; k < 4; ++k) { hv[k] = xc[u][0][k] * rstd * gq[u][0][k]; hv[4 + k] = xc[u][1][k] * rstd * gq[u][1][k]; }
;                 { const unsigned flo = pk4_fp8(sat8(hv[0] * FP8_SA), sat8(hv[1] * FP8_SA), sat8(hv[2] * FP8_SA), sat8(hv[3] * FP8_SA)), fhi = pk4_fp8(sat8(hv[4] * FP8_SA), sat8(hv[5] * FP8_SA), sat8(hv[6] * FP8_SA), sat8(hv[7] * FP8_SA));
;                   if ((u & 1) == 0) { hlo = flo; hhi = fhi; }
;                   else { const v2u r0 = __builtin_amdgcn_permlane16_swap(hlo, flo, false, false), r1 = __builtin_amdgcn_permlane16_swap(hhi, fhi, false, false);
;                          *(v4u*)(hf + (size_t)tok * D + 32 * (j4 + u - 1 + (kq & 1)) + 16 * (kq >> 1)) = (v4u){r0.x, r1.x, r0.y, r1.y}; } }
;                 v4u ah, al;
;                 ah.x = pk2(hv[0], hv[1]); ah.y = pk2(hv[2], hv[3]); ah.z = pk2(hv[4], hv[5]); ah.w = pk2(hv[6], hv[7]);
;                 al.x = pk2(hv[0] - bflo(ah.x), hv[1] - bfhi(ah.x)); al.y = pk2(hv[2] - bflo(ah.y), hv[3] - bfhi(ah.y)); al.z = pk2(hv[4] - bflo(ah.z), hv[5] - bfhi(ah.z)); al.w = pk2(hv[6] - bflo(ah.w), hv[7] - bfhi(ah.w));
;                 const bf16x8 fah = __builtin_bit_cast(bf16x8, ah), fal = __builtin_bit_cast(bf16x8, al);
;                 acc0 = __builtin_amdgcn_mfma_f32_16x16x32_bf16(fah, __builtin_bit_cast(bf16x8, wf[u][0][0]), acc0, 0, 0, 0);
;                 acc0 = __builtin_amdgcn_mfma_f32_16x16x32_bf16(fah, __builtin_bit_cast(bf16x8, wf[u][0][1]), acc0, 0, 0, 0);
;                 acc0 = __builtin_amdgcn_mfma_f32_16x16x32_bf16(fal, __builtin_bit_cast(bf16x8, wf[u][0][0]), acc0, 0, 0, 0);
;                 acc1 = __builtin_amdgcn_mfma_f32_16x16x32_bf16(fah, __builtin_bit_cast(bf16x8, wf[u][1][0]), acc1, 0, 0, 0);
;                 acc1 = __builtin_amdgcn_mfma_f32_16x16x32_bf16(fah, __builtin_bit_cast(bf16x8, wf[u][1][1]), acc1, 0, 0, 0);
;                 acc1 = __builtin_amdgcn_mfma_f32_16x16x32_bf16(fal, __builtin_bit_cast(bf16x8, wf[u][1][0]), acc1, 0, 0, 0);
;             }
;             asm volatile("s_waitcnt vmcnt(2)" ::: "memory");
;             __builtin_amdgcn_s_barrier();
;             asm volatile("" ::: "memory");
	v_mfma_f32_16x16x32_bf16 v[62:65], v[94:97], v[82:85], v[62:65]
	v_lshl_add_u64 v[82:83], s[88:89], 0, v[174:175]
	v_med3_f32 v75, v74, s35, v187
	v_mul_f32_e32 v74, 0x41800000, v77
	v_add_co_u32_e32 v80, vcc, s36, v82
	v_med3_f32 v82, v74, s35, v187
	v_cvt_pk_bf16_f32 v76, v76, v77
	v_addc_co_u32_e32 v81, vcc, 0, v83, vcc
	v_cvt_pk_fp8_f32 v74, v75, v82
	v_lshlrev_b32_e32 v82, 16, v76
	v_and_b32_e32 v83, 0xffff0000, v76
	v_pk_fma_f32 v[70:71], v[78:79], v[70:71], v[82:83] neg_lo:[0,0,1] neg_hi:[0,0,1]
	v_pk_mul_f32 v[78:79], v[176:177], v[210:211]
	v_cvt_pk_bf16_f32 v70, v70, v71
	v_pk_mul_f32 v[82:83], v[78:79], v[72:73]
	v_mul_f32_e32 v86, 0x41800000, v125
	v_mul_f32_e32 v71, 0x41800000, v82
	v_cvt_pk_bf16_f32 v77, v82, v83
	v_med3_f32 v75, v71, s35, v187
	v_mul_f32_e32 v71, 0x41800000, v83
	v_lshlrev_b32_e32 v82, 16, v77
	v_and_b32_e32 v83, 0xffff0000, v77
	v_lshlrev_b32_e32 v108, 16, v104
	v_and_b32_e32 v109, 0xffff0000, v104
	v_lshlrev_b32_e32 v106, 16, v105
	v_and_b32_e32 v107, 0xffff0000, v105
	v_med3_f32 v86, v86, s35, v187
	v_pk_fma_f32 v[72:73], v[78:79], v[72:73], v[82:83] neg_lo:[0,0,1] neg_hi:[0,0,1]
	v_cvt_pk_fp8_f32 v112, v132, v86 op_sel:[0,0,1]
	v_med3_f32 v90, v71, s35, v187
	v_cvt_pk_bf16_f32 v71, v72, v73
	v_pk_mul_f32 v[72:73], v[176:177], v[108:109]
	v_pk_mul_f32 v[86:87], v[176:177], v[106:107]
	v_pk_mul_f32 v[82:83], v[72:73], v[54:55]
	v_pk_mul_f32 v[88:89], v[86:87], v[56:57]
	v_cvt_pk_bf16_f32 v78, v82, v83
	v_cvt_pk_bf16_f32 v79, v88, v89
	v_lshlrev_b32_e32 v84, 16, v78
	v_and_b32_e32 v85, 0xffff0000, v78
	v_pk_fma_f32 v[54:55], v[72:73], v[54:55], v[84:85] neg_lo:[0,0,1] neg_hi:[0,0,1]
	v_mfma_f32_16x16x32_bf16 v[62:65], v[76:79], v[50:53], v[62:65]
	v_cvt_pk_bf16_f32 v72, v54, v55
	v_lshlrev_b32_e32 v54, 16, v79
	v_and_b32_e32 v55, 0xffff0000, v79
	v_pk_fma_f32 v[54:55], v[86:87], v[56:57], v[54:55] neg_lo:[0,0,1] neg_hi:[0,0,1]
	v_cvt_pk_fp8_f32 v74, v75, v90 op_sel:[0,0,1]
	v_cvt_pk_bf16_f32 v73, v54, v55
	v_mfma_f32_16x16x32_bf16 v[54:57], v[76:79], v[58:61], v[62:65]
	v_mul_f32_e32 v58, 0x41800000, v82
	v_med3_f32 v58, v58, s35, v187
	v_mfma_f32_16x16x32_bf16 v[50:53], v[70:73], v[50:53], v[54:57]
	v_lshlrev_b32_e32 v104, 16, v100
	v_and_b32_e32 v105, 0xffff0000, v100
	v_lshlrev_b32_e32 v102, 16, v98
	s_nop 0
	v_mul_f32_e32 v54, 0x41800000, v83
	v_med3_f32 v59, v54, s35, v187
	v_mfma_f32_16x16x32_bf16 v[54:57], v[76:79], v[42:45], v[66:69]
	v_cvt_pk_fp8_f32 v75, v58, v59
	v_mul_f32_e32 v58, 0x41800000, v88
	v_and_b32_e32 v103, 0xffff0000, v98
	v_mfma_f32_16x16x32_bf16 v[46:49], v[76:79], v[46:49], v[54:57]
	v_lshlrev_b32_e32 v98, 16, v99
	v_and_b32_e32 v99, 0xffff0000, v99
	v_lshlrev_b32_e32 v100, 16, v101
	s_nop 0
	v_mul_f32_e32 v54, 0x41800000, v89
	v_pk_mul_f32 v[56:57], v[176:177], v[104:105]
	v_and_b32_e32 v101, 0xffff0000, v101
	v_med3_f32 v58, v58, s35, v187
	v_med3_f32 v54, v54, s35, v187
	v_mfma_f32_16x16x32_bf16 v[42:45], v[70:73], v[42:45], v[46:49]
	v_cvt_pk_fp8_f32 v75, v58, v54 op_sel:[0,0,1]
	v_pk_mul_f32 v[54:55], v[176:177], v[102:103]
	v_pk_mul_f32 v[58:59], v[176:177], v[98:99]
	v_pk_mul_f32 v[48:49], v[56:57], v[30:31]
	v_pk_mul_f32 v[62:63], v[176:177], v[100:101]
	v_mul_f32_e32 v68, 0x41800000, v48
	v_mul_f32_e32 v69, 0x41800000, v49
	v_pk_mul_f32 v[46:47], v[54:55], v[38:39]
	v_pk_mul_f32 v[60:61], v[58:59], v[40:41]
	v_pk_mul_f32 v[64:65], v[62:63], v[32:33]
	v_med3_f32 v68, v68, s35, v187
	v_med3_f32 v69, v69, s35, v187
	v_cvt_pk_fp8_f32 v77, v68, v69
	v_mul_f32_e32 v69, 0x41800000, v46
	v_mul_f32_e32 v70, 0x41800000, v47
	v_cvt_pk_bf16_f32 v46, v46, v47
	v_cvt_pk_bf16_f32 v47, v60, v61
	v_cvt_pk_bf16_f32 v48, v48, v49
	v_cvt_pk_bf16_f32 v49, v64, v65
	v_mul_f32_e32 v66, 0x41800000, v64
	v_mul_f32_e32 v67, 0x41800000, v65
	v_lshlrev_b32_e32 v64, 16, v46
	v_and_b32_e32 v65, 0xffff0000, v46
	v_pk_fma_f32 v[38:39], v[54:55], v[38:39], v[64:65] neg_lo:[0,0,1] neg_hi:[0,0,1]
	v_lshlrev_b32_e32 v54, 16, v47
	v_and_b32_e32 v55, 0xffff0000, v47
	v_pk_fma_f32 v[40:41], v[58:59], v[40:41], v[54:55] neg_lo:[0,0,1] neg_hi:[0,0,1]
	v_cvt_pk_bf16_f32 v38, v38, v39
	v_cvt_pk_bf16_f32 v39, v40, v41
	v_lshlrev_b32_e32 v40, 16, v48
	v_and_b32_e32 v41, 0xffff0000, v48
	v_pk_fma_f32 v[30:31], v[56:57], v[30:31], v[40:41] neg_lo:[0,0,1] neg_hi:[0,0,1]
	v_mfma_f32_16x16x32_bf16 v[50:53], v[46:49], v[26:29], v[50:53]
	v_cvt_pk_bf16_f32 v40, v30, v31
	v_lshlrev_b32_e32 v30, 16, v49
	v_and_b32_e32 v31, 0xffff0000, v49
	v_pk_fma_f32 v[30:31], v[62:63], v[32:33], v[30:31] neg_lo:[0,0,1] neg_hi:[0,0,1]
	v_med3_f32 v69, v69, s35, v187
	v_cvt_pk_bf16_f32 v41, v30, v31
	v_mfma_f32_16x16x32_bf16 v[30:33], v[46:49], v[34:37], v[50:53]
	v_med3_f32 v34, v70, s35, v187
	v_cvt_pk_fp8_f32 v76, v69, v34
	v_mul_f32_e32 v68, 0x41800000, v60
	v_mfma_f32_16x16x32_bf16 v[62:65], v[38:41], v[26:29], v[30:33]
	v_mul_f32_e32 v26, 0x41800000, v61
	v_med3_f32 v68, v68, s35, v187
	v_med3_f32 v26, v26, s35, v187
	v_cvt_pk_fp8_f32 v76, v68, v26 op_sel:[0,0,1]
	v_mfma_f32_16x16x32_bf16 v[26:29], v[46:49], v[18:21], v[42:45]
	v_med3_f32 v66, v66, s35, v187
	v_med3_f32 v67, v67, s35, v187
	v_cvt_pk_fp8_f32 v113, v130, v131 op_sel:[0,0,1]
	v_cvt_pk_fp8_f32 v77, v66, v67 op_sel:[0,0,1]
	v_mfma_f32_16x16x32_bf16 v[22:25], v[46:49], v[22:25], v[26:29]
	v_permlane16_swap_b32_e32 v110, v112
	v_permlane16_swap_b32_e32 v111, v113
	v_permlane16_swap_b32_e32 v74, v76
	v_permlane16_swap_b32_e32 v75, v77
	global_store_dwordx4 v[80:81], v[110:113], off
	global_store_dwordx4 v[80:81], v[74:77], off offset:64
	v_mfma_f32_16x16x32_bf16 v[66:69], v[38:41], v[18:21], v[22:25]
	s_waitcnt vmcnt(2)
	s_barrier
	s_waitcnt vmcnt(0)
	v_mov_b64_e32 v[112:113], v[4:5]
	v_mov_b64_e32 v[108:109], v[8:9]
	v_mov_b64_e32 v[104:105], v[12:13]
	v_mov_b64_e32 v[100:101], v[16:17]
	s_add_i32 s38, s38, 4
	v_lshl_add_u64 v[172:173], v[172:173], 0, s[18:19]
	v_lshl_add_u64 v[174:175], v[174:175], 0, s[20:21]
	v_add_u32_e32 v161, 0x200, v161
	s_addk_i32 s39, 0x4000
	v_lshl_add_u64 v[170:171], v[170:171], 0, s[22:23]
	s_and_b64 vcc, exec, s[24:25]
	v_mov_b64_e32 v[110:111], v[2:3]
	v_mov_b64_e32 v[106:107], v[6:7]
	v_mov_b64_e32 v[102:103], v[10:11]
	v_mov_b64_e32 v[98:99], v[14:15]
	s_cbranch_vccnz .LBB0_657

; __device__ __forceinline__ unsigned pk4_fp8(float a, float b, float c, float d) { int v = 0; v = __builtin_amdgcn_cvt_pk_fp8_f32(a, b, v, false); v = __builtin_amdgcn_cvt_pk_fp8_f32(c, d, v, true); return (unsigned)v; }
;     __device__ __forceinline__ void operator()(const f32x4 (&acc)[2][2][4][2], const pg8::Unit& u, const Pre& q, int wr, int wc, int fr, int fq) const {
;         const int row0 = u.pm * 256 + wr * 64 + fr, f0w = u.pn * 128 + wc * 32;
;         constexpr float DS = 1.0f / (FP8_SA * FP8_SW);
;         f32x4 dsk = (f32x4){DS * KP, DS * KP, DS * KP, DS * KP}, dsu = (f32x4){DS, DS, DS, DS}; asm volatile("" : "+v"(dsk), "+v"(dsu));
; #pragma unroll
;         for (int ai = 0; ai < 2; ++ai)
; #pragma unroll
;             for (int mp = 0; mp < 2; ++mp) { unsigned lo[2], hi[2];
; #pragma unroll
;                 for (int mm = 0; mm < 2; ++mm) { const int m = 2 * mp + mm; float h[8];
; #pragma unroll
;                     for (int n = 0; n < 2; ++n) { const f32x4 gk = __builtin_elementwise_fma(acc[ai][0][m][n], dsk, q.bg[n]), up = __builtin_elementwise_fma(acc[ai][1][m][n], dsu, q.bu[n]);
; #pragma unroll
;                         for (int j = 0; j < 4; ++j) { const float gm = __builtin_fmaxf(gk[j], 7.0f * KP), li = __builtin_amdgcn_fmed3f(up[j], -7.0f, 7.0f);
;                             const float sg = __builtin_amdgcn_rcpf(1.0f + __builtin_amdgcn_exp2f(gm));
;                             h[n * 4 + j] = (gm * sg) * (li * (FP8_SH / KP) + (FP8_SH / KP)); } }
;                     lo[mm] = pk4_fp8(h[0], h[1], h[2], h[3]); hi[mm] = pk4_fp8(h[4], h[5], h[6], h[7]); }
;                 const v2u r0 = __builtin_amdgcn_permlane16_swap(lo[0], lo[1], false, false), r1 = __builtin_amdgcn_permlane16_swap(hi[0], hi[1], false, false);
;                 unsigned char* rowp = hb + (size_t)(row0 + ai * 128 + (2 * mp + (fq & 1)) * 16) * FF + f0w + 16 * (fq >> 1);
;                 *(v4u*)rowp = (v4u){r0.x, r1.x, r0.y, r1.y}; }
;     }
.LBB0_739:
	v_mov_b32_e32 v11, v0
	v_mov_b32_e32 v43, v42
	v_readfirstlane_b32 s19, v11
	v_mov_b32_e32 v47, v46
	s_ashr_i32 s27, s19, 2
	v_mov_b32_e32 v44, v42
	v_mov_b32_e32 v45, v42
	v_mov_b32_e32 v48, v46
	v_mov_b32_e32 v49, v46
	v_pk_fma_f32 v[38:39], v[38:39], s[98:99], s[98:99] op_sel_hi:[1,0,0]
	v_pk_fma_f32 v[40:41], v[40:41], s[98:99], s[98:99] op_sel_hi:[1,0,0]
	v_pk_fma_f32 v[34:35], v[34:35], s[98:99], s[98:99] op_sel_hi:[1,0,0]
	v_pk_fma_f32 v[36:37], v[36:37], s[98:99], s[98:99] op_sel_hi:[1,0,0]
	v_mov_b64_e32 v[2:3], v[46:47]
	v_mov_b64_e32 v[6:7], v[42:43]
	v_pk_mul_f32 v[18:19], v[78:79], s[16:17] op_sel_hi:[1,0]
	s_lshl_b32 s21, s38, 8
	s_andn2_b32 s27, s27, 63
	v_mov_b64_e32 v[4:5], v[48:49]
	v_mov_b64_e32 v[8:9], v[44:45]
	s_add_i32 s27, s27, s21
	v_and_or_b32 v10, v11, 31, s27
	v_pk_fma_f32 v[20:21], v[178:179], v[6:7], v[18:19]
	v_lshrrev_b32_e32 v11, 1, v11
	v_max_f32_e32 v23, 0xc1898193, v20
	v_and_b32_e32 v186, 16, v11
	v_exp_f32_e32 v11, v23
	v_max_f32_e32 v21, 0xc1898193, v21
	v_pk_fma_f32 v[28:29], v[182:183], v[2:3], v[38:39]
	v_pk_mul_f32 v[16:17], v[80:81], s[16:17] op_sel_hi:[1,0]
	v_add_f32_e32 v11, 1.0, v11
	v_rcp_f32_e32 v189, v11
	v_exp_f32_e32 v11, v21
	v_med3_f32 v22, v28, s94, v202
	v_pk_fma_f32 v[24:25], v[180:181], v[8:9], v[16:17]
	v_mul_f32_e32 v23, v23, v189
	v_add_f32_e32 v11, 1.0, v11
	v_mul_f32_e32 v30, v22, v23
	v_max_f32_e32 v23, 0xc1898193, v24
	v_rcp_f32_e32 v189, v11
	v_exp_f32_e32 v11, v23
	v_med3_f32 v20, v29, s94, v202
	v_max_f32_e32 v25, 0xc1898193, v25
	v_mul_f32_e32 v21, v21, v189
	v_add_f32_e32 v11, 1.0, v11
	v_rcp_f32_e32 v189, v11
	v_exp_f32_e32 v11, v25
	v_pk_fma_f32 v[26:27], v[184:185], v[4:5], v[40:41]
	v_med3_f32 v22, v26, s94, v202
	v_add_f32_e32 v11, 1.0, v11
	v_mul_f32_e32 v31, v20, v21
	v_mul_f32_e32 v21, v23, v189
	v_rcp_f32_e32 v189, v11
	v_med3_f32 v24, v27, s94, v202
	v_mul_f32_e32 v11, v22, v21
	v_mul_f32_e32 v21, v25, v189
	v_pk_mul_f32 v[14:15], v[74:75], s[16:17] op_sel_hi:[1,0]
	v_mul_f32_e32 v32, v24, v21
	v_pk_fma_f32 v[20:21], v[170:171], v[6:7], v[14:15]
	v_pk_fma_f32 v[28:29], v[174:175], v[2:3], v[34:35]
	v_max_f32_e32 v23, 0xc1898193, v20
	v_exp_f32_e32 v20, v23
	v_max_f32_e32 v21, 0xc1898193, v21
	v_med3_f32 v22, v28, s94, v202
	v_pk_mul_f32 v[12:13], v[76:77], s[16:17] op_sel_hi:[1,0]
	v_add_f32_e32 v20, 1.0, v20
	v_rcp_f32_e32 v189, v20
	v_exp_f32_e32 v20, v21
	v_pk_fma_f32 v[24:25], v[172:173], v[8:9], v[12:13]
	v_pk_fma_f32 v[26:27], v[176:177], v[4:5], v[36:37]
	v_mul_f32_e32 v23, v23, v189
	v_add_f32_e32 v20, 1.0, v20
	v_mul_f32_e32 v28, v22, v23
	v_max_f32_e32 v23, 0xc1898193, v24
	v_exp_f32_e32 v22, v23
	v_rcp_f32_e32 v189, v20
	v_med3_f32 v20, v29, s94, v202
	v_max_f32_e32 v25, 0xc1898193, v25
	v_add_f32_e32 v22, 1.0, v22
	v_mul_f32_e32 v21, v21, v189
	v_rcp_f32_e32 v189, v22
	v_exp_f32_e32 v24, v25
	v_med3_f32 v22, v26, s94, v202
	v_mul_f32_e32 v29, v20, v21
	v_mul_f32_e32 v21, v23, v189
	v_mov_b32_e32 v20, v22
	v_add_f32_e32 v22, 1.0, v24
	v_rcp_f32_e32 v189, v22
	v_mul_f32_e32 v26, v20, v21
	v_med3_f32 v24, v27, s94, v202
	v_cvt_pk_fp8_f32 v21, v28, v29
	v_mul_f32_e32 v23, v25, v189
	v_cvt_pk_fp8_f32 v20, v30, v31
	v_mul_f32_e32 v22, v24, v23
	v_cvt_pk_fp8_f32 v21, v26, v22 op_sel:[0,0,1]
	v_pk_fma_f32 v[22:23], v[162:163], v[6:7], v[18:19]
	v_cvt_pk_fp8_f32 v20, v11, v32 op_sel:[0,0,1]
	v_max_f32_e32 v25, 0xc1898193, v22
	v_exp_f32_e32 v11, v25
	v_max_f32_e32 v23, 0xc1898193, v23
	v_pk_fma_f32 v[30:31], v[166:167], v[2:3], v[38:39]
	v_pk_fma_f32 v[26:27], v[164:165], v[8:9], v[16:17]
	v_add_f32_e32 v11, 1.0, v11
	v_rcp_f32_e32 v189, v11
	v_exp_f32_e32 v11, v23
	v_med3_f32 v24, v30, s94, v202
	v_max_f32_e32 v27, 0xc1898193, v27
	v_mul_f32_e32 v25, v25, v189
	v_add_f32_e32 v11, 1.0, v11
	v_mul_f32_e32 v32, v24, v25
	v_max_f32_e32 v25, 0xc1898193, v26
	v_rcp_f32_e32 v189, v11
	v_exp_f32_e32 v11, v25
	v_med3_f32 v22, v31, s94, v202
	v_pk_fma_f32 v[28:29], v[168:169], v[4:5], v[40:41]
	v_mul_f32_e32 v23, v23, v189
	v_add_f32_e32 v11, 1.0, v11
	v_rcp_f32_e32 v189, v11
	v_exp_f32_e32 v11, v27
	v_med3_f32 v24, v28, s94, v202
	v_mul_f32_e32 v33, v22, v23
	v_add_f32_e32 v11, 1.0, v11
	v_mul_f32_e32 v23, v25, v189
	v_rcp_f32_e32 v189, v11
	v_med3_f32 v26, v29, s94, v202
	v_mul_f32_e32 v11, v24, v23
	v_mul_f32_e32 v23, v27, v189
	v_pk_fma_f32 v[30:31], v[158:159], v[2:3], v[34:35]
	v_mul_f32_e32 v43, v26, v23
	v_pk_fma_f32 v[22:23], v[154:155], v[6:7], v[14:15]
	v_med3_f32 v24, v30, s94, v202
	v_max_f32_e32 v25, 0xc1898193, v22
	v_exp_f32_e32 v22, v25
	v_max_f32_e32 v23, 0xc1898193, v23
	v_pk_fma_f32 v[26:27], v[156:157], v[8:9], v[12:13]
	v_pk_fma_f32 v[28:29], v[160:161], v[4:5], v[36:37]
	v_add_f32_e32 v22, 1.0, v22
	v_rcp_f32_e32 v189, v22
	v_exp_f32_e32 v22, v23
	v_max_f32_e32 v27, 0xc1898193, v27
	s_lshr_b32 s19, s19, 1
	v_mul_f32_e32 v25, v25, v189
	v_add_f32_e32 v22, 1.0, v22
	v_mul_f32_e32 v30, v24, v25
	v_max_f32_e32 v25, 0xc1898193, v26
	v_exp_f32_e32 v24, v25
	v_rcp_f32_e32 v189, v22
	v_med3_f32 v22, v31, s94, v202
	v_exp_f32_e32 v26, v27
	v_add_f32_e32 v24, 1.0, v24
	v_mul_f32_e32 v23, v23, v189
	v_rcp_f32_e32 v189, v24
	v_med3_f32 v24, v28, s94, v202
	v_mul_f32_e32 v31, v22, v23
	v_mul_f32_e32 v23, v25, v189
	v_mov_b32_e32 v22, v24
	v_add_f32_e32 v24, 1.0, v26
	v_rcp_f32_e32 v189, v24
	v_mul_f32_e32 v28, v22, v23
	v_cvt_pk_fp8_f32 v22, v32, v33
	v_med3_f32 v26, v29, s94, v202
	v_cvt_pk_fp8_f32 v23, v30, v31
	v_mul_f32_e32 v25, v27, v189
	v_cvt_pk_fp8_f32 v22, v11, v43 op_sel:[0,0,1]
	v_mul_f32_e32 v11, v26, v25
	s_lshl_b32 s21, s26, 7
	s_and_b32 s19, s19, 0x60
	v_cvt_pk_fp8_f32 v23, v28, v11 op_sel:[0,0,1]
	v_ashrrev_i32_e32 v11, 31, v10
; __device__ __forceinline__ unsigned pk4_fp8(float a, float b, float c, float d) { int v = 0; v = __builtin_amdgcn_cvt_pk_fp8_f32(a, b, v, false); v = __builtin_amdgcn_cvt_pk_fp8_f32(c, d, v, true); return (unsigned)v; }
;     __device__ __forceinline__ void operator()(const f32x4 (&acc)[2][2][4][2], const pg8::Unit& u, const Pre& q, int wr, int wc, int fr, int fq) const {
;         const int row0 = u.pm * 256 + wr * 64 + fr, f0w = u.pn * 128 + wc * 32;
;         constexpr float DS = 1.0f / (FP8_SA * FP8_SW);
;         f32x4 dsk = (f32x4){DS * KP, DS * KP, DS * KP, DS * KP}, dsu = (f32x4){DS, DS, DS, DS}; asm volatile("" : "+v"(dsk), "+v"(dsu));
; #pragma unroll
;         for (int ai = 0; ai < 2; ++ai)
; #pragma unroll
;             for (int mp = 0; mp < 2; ++mp) { unsigned lo[2], hi[2];
; #pragma unroll
;                 for (int mm = 0; mm < 2; ++mm) { const int m = 2 * mp + mm; float h[8];
; #pragma unroll
;                     for (int n = 0; n < 2; ++n) { const f32x4 gk = __builtin_elementwise_fma(acc[ai][0][m][n], dsk, q.bg[n]), up = __builtin_elementwise_fma(acc[ai][1][m][n], dsu, q.bu[n]);
; #pragma unroll
;                         for (int j = 0; j < 4; ++j) { const float gm = __builtin_fmaxf(gk[j], 7.0f * KP), li = __builtin_amdgcn_fmed3f(up[j], -7.0f, 7.0f);
;                             const float sg = __builtin_amdgcn_rcpf(1.0f + __builtin_amdgcn_exp2f(gm));
;                             h[n * 4 + j] = (gm * sg) * (li * (FP8_SH / KP) + (FP8_SH / KP)); } }
;                     lo[mm] = pk4_fp8(h[0], h[1], h[2], h[3]); hi[mm] = pk4_fp8(h[4], h[5], h[6], h[7]); }
;                 const v2u r0 = __builtin_amdgcn_permlane16_swap(lo[0], lo[1], false, false), r1 = __builtin_amdgcn_permlane16_swap(hi[0], hi[1], false, false);
;                 unsigned char* rowp = hb + (size_t)(row0 + ai * 128 + (2 * mp + (fq & 1)) * 16) * FF + f0w + 16 * (fq >> 1);
;                 *(v4u*)rowp = (v4u){r0.x, r1.x, r0.y, r1.y}; }
;     }
	s_or_b32 s26, s19, s21
	v_lshlrev_b64 v[24:25], 11, v[10:11]
	s_ashr_i32 s27, s26, 31
	v_lshl_add_u64 v[24:25], s[12:13], 0, v[24:25]
	v_lshl_add_u64 v[24:25], v[24:25], 0, s[26:27]
	v_permlane16_swap_b32_e32 v20, v22
	v_permlane16_swap_b32_e32 v21, v23
	v_lshl_add_u64 v[24:25], v[24:25], 0, v[186:187]
	global_store_dwordx4 v[24:25], v[20:23], off
	v_pk_fma_f32 v[28:29], v[150:151], v[2:3], v[38:39]
	v_pk_fma_f32 v[24:25], v[148:149], v[8:9], v[16:17]
	v_pk_fma_f32 v[20:21], v[146:147], v[6:7], v[18:19]
	v_med3_f32 v22, v28, s94, v202
	v_max_f32_e32 v23, 0xc1898193, v20
	v_exp_f32_e32 v11, v23
	v_max_f32_e32 v21, 0xc1898193, v21
	v_max_f32_e32 v25, 0xc1898193, v25
	v_pk_fma_f32 v[26:27], v[152:153], v[4:5], v[40:41]
	v_add_f32_e32 v11, 1.0, v11
	v_rcp_f32_e32 v189, v11
	v_exp_f32_e32 v11, v21
	s_andn2_b64 vcc, exec, s[2:3]
	s_mov_b64 s[2:3], -1
	v_mul_f32_e32 v23, v23, v189
	v_add_f32_e32 v11, 1.0, v11
	v_mul_f32_e32 v30, v22, v23
	v_max_f32_e32 v23, 0xc1898193, v24
	v_rcp_f32_e32 v189, v11
	v_exp_f32_e32 v11, v23
	v_med3_f32 v20, v29, s94, v202
	v_med3_f32 v22, v26, s94, v202
	v_mul_f32_e32 v21, v21, v189
	v_add_f32_e32 v11, 1.0, v11
	v_rcp_f32_e32 v189, v11
	v_exp_f32_e32 v11, v25
	v_mul_f32_e32 v31, v20, v21
	v_mul_f32_e32 v21, v23, v189
	v_add_f32_e32 v11, 1.0, v11
	v_rcp_f32_e32 v189, v11
	v_med3_f32 v24, v27, s94, v202
	v_mul_f32_e32 v11, v22, v21
	v_mul_f32_e32 v21, v25, v189
	v_pk_fma_f32 v[28:29], v[142:143], v[2:3], v[34:35]
	v_mul_f32_e32 v32, v24, v21
	v_pk_fma_f32 v[20:21], v[138:139], v[6:7], v[14:15]
	v_med3_f32 v22, v28, s94, v202
	v_max_f32_e32 v23, 0xc1898193, v20
	v_exp_f32_e32 v20, v23
	v_max_f32_e32 v21, 0xc1898193, v21
	v_pk_fma_f32 v[24:25], v[140:141], v[8:9], v[12:13]
	v_pk_fma_f32 v[26:27], v[144:145], v[4:5], v[36:37]
	v_add_f32_e32 v20, 1.0, v20
	v_rcp_f32_e32 v189, v20
	v_exp_f32_e32 v20, v21
	v_max_f32_e32 v25, 0xc1898193, v25
	v_mul_f32_e32 v23, v23, v189
	s_nop 0
	v_mul_f32_e32 v28, v22, v23
	v_max_f32_e32 v23, 0xc1898193, v24
	v_add_f32_e32 v20, 1.0, v20
	v_exp_f32_e32 v22, v23
	v_rcp_f32_e32 v189, v20
	v_med3_f32 v20, v29, s94, v202
	v_exp_f32_e32 v24, v25
	v_add_f32_e32 v22, 1.0, v22
	v_mul_f32_e32 v21, v21, v189
	v_rcp_f32_e32 v189, v22
	v_med3_f32 v22, v26, s94, v202
	v_mul_f32_e32 v29, v20, v21
	v_mul_f32_e32 v21, v23, v189
	v_mov_b32_e32 v20, v22
	v_add_f32_e32 v22, 1.0, v24
	v_rcp_f32_e32 v189, v22
	v_mul_f32_e32 v26, v20, v21
	v_med3_f32 v24, v27, s94, v202
	v_cvt_pk_fp8_f32 v21, v28, v29
	v_mul_f32_e32 v23, v25, v189
	v_cvt_pk_fp8_f32 v20, v30, v31
	v_mul_f32_e32 v22, v24, v23
	v_cvt_pk_fp8_f32 v21, v26, v22 op_sel:[0,0,1]
	v_pk_fma_f32 v[22:23], v[130:131], v[6:7], v[18:19]
	v_cvt_pk_fp8_f32 v20, v11, v32 op_sel:[0,0,1]
	v_max_f32_e32 v25, 0xc1898193, v22
	v_exp_f32_e32 v11, v25
	v_max_f32_e32 v23, 0xc1898193, v23
	v_pk_fma_f32 v[30:31], v[134:135], v[2:3], v[38:39]
	v_pk_fma_f32 v[26:27], v[132:133], v[8:9], v[16:17]
	v_add_f32_e32 v11, 1.0, v11
	v_rcp_f32_e32 v189, v11
	v_exp_f32_e32 v11, v23
	v_med3_f32 v24, v30, s94, v202
	v_max_f32_e32 v27, 0xc1898193, v27
	v_mul_f32_e32 v25, v25, v189
	v_add_f32_e32 v11, 1.0, v11
	v_mul_f32_e32 v32, v24, v25
	v_max_f32_e32 v25, 0xc1898193, v26
	v_rcp_f32_e32 v189, v11
	v_exp_f32_e32 v11, v25
	v_med3_f32 v22, v31, s94, v202
	v_pk_fma_f32 v[28:29], v[136:137], v[4:5], v[40:41]
	v_mul_f32_e32 v23, v23, v189
	v_add_f32_e32 v11, 1.0, v11
	v_rcp_f32_e32 v189, v11
	v_exp_f32_e32 v11, v27
	v_med3_f32 v24, v28, s94, v202
	v_mul_f32_e32 v33, v22, v23
	v_add_f32_e32 v11, 1.0, v11
	v_mul_f32_e32 v23, v25, v189
	v_rcp_f32_e32 v189, v11
	v_med3_f32 v26, v29, s94, v202
	v_mul_f32_e32 v11, v24, v23
	v_mul_f32_e32 v23, v27, v189
	v_pk_fma_f32 v[30:31], v[126:127], v[2:3], v[34:35]
	v_mul_f32_e32 v43, v26, v23
	v_pk_fma_f32 v[22:23], v[122:123], v[6:7], v[14:15]
	v_med3_f32 v24, v30, s94, v202
	v_max_f32_e32 v25, 0xc1898193, v22
	v_exp_f32_e32 v22, v25
	v_max_f32_e32 v23, 0xc1898193, v23
	v_pk_fma_f32 v[26:27], v[124:125], v[8:9], v[12:13]
	v_pk_fma_f32 v[28:29], v[128:129], v[4:5], v[36:37]
	v_add_f32_e32 v22, 1.0, v22
	v_rcp_f32_e32 v189, v22
	v_exp_f32_e32 v22, v23
	v_max_f32_e32 v27, 0xc1898193, v27
	v_mul_f32_e32 v25, v25, v189
	s_nop 0
	v_mul_f32_e32 v30, v24, v25
	v_max_f32_e32 v25, 0xc1898193, v26
	v_add_f32_e32 v22, 1.0, v22
	v_exp_f32_e32 v24, v25
	v_rcp_f32_e32 v189, v22
	v_med3_f32 v22, v31, s94, v202
	v_exp_f32_e32 v26, v27
	v_add_f32_e32 v24, 1.0, v24
	v_mul_f32_e32 v23, v23, v189
	v_rcp_f32_e32 v189, v24
	v_med3_f32 v24, v28, s94, v202
	v_mul_f32_e32 v31, v22, v23
	v_mul_f32_e32 v23, v25, v189
	v_mov_b32_e32 v22, v24
	v_add_f32_e32 v24, 1.0, v26
	v_rcp_f32_e32 v189, v24
	v_mul_f32_e32 v28, v22, v23
	v_cvt_pk_fp8_f32 v22, v32, v33
	v_med3_f32 v26, v29, s94, v202
	v_cvt_pk_fp8_f32 v23, v30, v31
	v_mul_f32_e32 v25, v27, v189
	v_cvt_pk_fp8_f32 v22, v11, v43 op_sel:[0,0,1]
	v_mul_f32_e32 v11, v26, v25
	v_or_b32_e32 v24, 32, v10
	v_cvt_pk_fp8_f32 v23, v28, v11 op_sel:[0,0,1]
	v_ashrrev_i32_e32 v25, 31, v24
	v_lshlrev_b64 v[24:25], 11, v[24:25]
	v_lshl_add_u64 v[24:25], s[12:13], 0, v[24:25]
	v_lshl_add_u64 v[24:25], v[24:25], 0, s[26:27]
	v_permlane16_swap_b32_e32 v20, v22
	v_permlane16_swap_b32_e32 v21, v23
	v_lshl_add_u64 v[24:25], v[24:25], 0, v[186:187]
	global_store_dwordx4 v[24:25], v[20:23], off
	v_pk_fma_f32 v[30:31], v[106:107], v[2:3], v[38:39]
	v_pk_fma_f32 v[26:27], v[120:121], v[8:9], v[16:17]
	v_pk_fma_f32 v[22:23], v[118:119], v[6:7], v[18:19]
	v_med3_f32 v24, v30, s94, v202
	v_max_f32_e32 v25, 0xc1898193, v22
	v_exp_f32_e32 v11, v25
	v_max_f32_e32 v23, 0xc1898193, v23
	v_med3_f32 v22, v31, s94, v202
	v_max_f32_e32 v27, 0xc1898193, v27
; __device__ __forceinline__ unsigned pk4_fp8(float a, float b, float c, float d) { int v = 0; v = __builtin_amdgcn_cvt_pk_fp8_f32(a, b, v, false); v = __builtin_amdgcn_cvt_pk_fp8_f32(c, d, v, true); return (unsigned)v; }
;     __device__ __forceinline__ void operator()(const f32x4 (&acc)[2][2][4][2], const pg8::Unit& u, const Pre& q, int wr, int wc, int fr, int fq) const {
;         const int row0 = u.pm * 256 + wr * 64 + fr, f0w = u.pn * 128 + wc * 32;
;         constexpr float DS = 1.0f / (FP8_SA * FP8_SW);
;         f32x4 dsk = (f32x4){DS * KP, DS * KP, DS * KP, DS * KP}, dsu = (f32x4){DS, DS, DS, DS}; asm volatile("" : "+v"(dsk), "+v"(dsu));
; #pragma unroll
;         for (int ai = 0; ai < 2; ++ai)
; #pragma unroll
;             for (int mp = 0; mp < 2; ++mp) { unsigned lo[2], hi[2];
; #pragma unroll
;                 for (int mm = 0; mm < 2; ++mm) { const int m = 2 * mp + mm; float h[8];
; #pragma unroll
;                     for (int n = 0; n < 2; ++n) { const f32x4 gk = __builtin_elementwise_fma(acc[ai][0][m][n], dsk, q.bg[n]), up = __builtin_elementwise_fma(acc[ai][1][m][n], dsu, q.bu[n]);
; #pragma unroll
;                         for (int j = 0; j < 4; ++j) { const float gm = __builtin_fmaxf(gk[j], 7.0f * KP), li = __builtin_amdgcn_fmed3f(up[j], -7.0f, 7.0f);
;                             const float sg = __builtin_amdgcn_rcpf(1.0f + __builtin_amdgcn_exp2f(gm));
;                             h[n * 4 + j] = (gm * sg) * (li * (FP8_SH / KP) + (FP8_SH / KP)); } }
;                     lo[mm] = pk4_fp8(h[0], h[1], h[2], h[3]); hi[mm] = pk4_fp8(h[4], h[5], h[6], h[7]); }
;                 const v2u r0 = __builtin_amdgcn_permlane16_swap(lo[0], lo[1], false, false), r1 = __builtin_amdgcn_permlane16_swap(hi[0], hi[1], false, false);
;                 unsigned char* rowp = hb + (size_t)(row0 + ai * 128 + (2 * mp + (fq & 1)) * 16) * FF + f0w + 16 * (fq >> 1);
;                 *(v4u*)rowp = (v4u){r0.x, r1.x, r0.y, r1.y}; }
;     }
	v_add_f32_e32 v11, 1.0, v11
	v_rcp_f32_e32 v189, v11
	v_exp_f32_e32 v11, v23
	v_pk_fma_f32 v[28:29], v[108:109], v[4:5], v[40:41]
	v_pk_fma_f32 v[30:31], v[114:115], v[2:3], v[34:35]
	v_mul_f32_e32 v25, v25, v189
	v_add_f32_e32 v11, 1.0, v11
	v_mul_f32_e32 v21, v24, v25
	v_max_f32_e32 v25, 0xc1898193, v26
	v_rcp_f32_e32 v189, v11
	v_exp_f32_e32 v11, v25
	v_med3_f32 v24, v28, s94, v202
	v_med3_f32 v26, v29, s94, v202
	v_mul_f32_e32 v23, v23, v189
	v_add_f32_e32 v11, 1.0, v11
	v_rcp_f32_e32 v189, v11
	v_exp_f32_e32 v11, v27
	v_mul_f32_e32 v32, v22, v23
	v_mul_f32_e32 v23, v25, v189
	v_add_f32_e32 v11, 1.0, v11
	v_rcp_f32_e32 v189, v11
	v_mul_f32_e32 v11, v24, v23
	v_med3_f32 v24, v30, s94, v202
	v_mul_f32_e32 v23, v27, v189
	v_mov_b32_e32 v22, v26
	v_pk_fma_f32 v[26:27], v[112:113], v[8:9], v[12:13]
	v_mul_f32_e32 v33, v22, v23
	v_pk_fma_f32 v[22:23], v[110:111], v[6:7], v[14:15]
	v_max_f32_e32 v27, 0xc1898193, v27
	v_max_f32_e32 v25, 0xc1898193, v22
	v_exp_f32_e32 v22, v25
	v_max_f32_e32 v23, 0xc1898193, v23
	v_pk_fma_f32 v[28:29], v[116:117], v[4:5], v[36:37]
	v_add_u32_e32 v20, 0x80, v10
	v_add_f32_e32 v22, 1.0, v22
	v_rcp_f32_e32 v189, v22
	v_exp_f32_e32 v22, v23
	v_mul_f32_e32 v25, v25, v189
	s_nop 0
	v_mul_f32_e32 v30, v24, v25
	v_max_f32_e32 v25, 0xc1898193, v26
	v_add_f32_e32 v22, 1.0, v22
	v_exp_f32_e32 v24, v25
	v_rcp_f32_e32 v189, v22
	v_med3_f32 v22, v31, s94, v202
	v_exp_f32_e32 v26, v27
	v_add_f32_e32 v24, 1.0, v24
	v_mul_f32_e32 v23, v23, v189
	v_rcp_f32_e32 v189, v24
	v_med3_f32 v24, v28, s94, v202
	v_mul_f32_e32 v31, v22, v23
	v_mul_f32_e32 v23, v25, v189
	v_mov_b32_e32 v22, v24
	v_add_f32_e32 v24, 1.0, v26
	v_rcp_f32_e32 v189, v24
	v_mul_f32_e32 v28, v22, v23
	v_med3_f32 v26, v29, s94, v202
	v_mul_f32_e32 v25, v27, v189
	v_cvt_pk_fp8_f32 v22, v21, v32
	v_mul_f32_e32 v21, v26, v25
	v_pk_fma_f32 v[24:25], v[98:99], v[6:7], v[18:19]
	v_cvt_pk_fp8_f32 v22, v11, v33 op_sel:[0,0,1]
	v_max_f32_e32 v27, 0xc1898193, v24
	v_exp_f32_e32 v11, v27
	v_cvt_pk_fp8_f32 v23, v30, v31
	v_max_f32_e32 v25, 0xc1898193, v25
	v_add_f32_e32 v11, 1.0, v11
	v_rcp_f32_e32 v189, v11
	v_pk_fma_f32 v[32:33], v[102:103], v[2:3], v[38:39]
	v_exp_f32_e32 v11, v25
	v_med3_f32 v26, v32, s94, v202
	v_mul_f32_e32 v27, v27, v189
	v_cvt_pk_fp8_f32 v23, v28, v21 op_sel:[0,0,1]
	v_pk_fma_f32 v[28:29], v[100:101], v[8:9], v[16:17]
	v_mul_f32_e32 v21, v26, v27
	v_add_f32_e32 v11, 1.0, v11
	v_max_f32_e32 v27, 0xc1898193, v28
	v_rcp_f32_e32 v189, v11
	v_exp_f32_e32 v11, v27
	v_med3_f32 v24, v33, s94, v202
	v_max_f32_e32 v29, 0xc1898193, v29
	v_mul_f32_e32 v25, v25, v189
	v_add_f32_e32 v11, 1.0, v11
	v_rcp_f32_e32 v189, v11
	v_exp_f32_e32 v11, v29
	v_pk_fma_f32 v[30:31], v[104:105], v[4:5], v[40:41]
	v_med3_f32 v26, v30, s94, v202
	v_add_f32_e32 v11, 1.0, v11
	v_mul_f32_e32 v43, v24, v25
	v_mul_f32_e32 v25, v27, v189
	v_rcp_f32_e32 v189, v11
	v_med3_f32 v28, v31, s94, v202
	v_mul_f32_e32 v11, v26, v25
	v_mul_f32_e32 v25, v29, v189
	v_pk_fma_f32 v[32:33], v[94:95], v[2:3], v[34:35]
	v_mul_f32_e32 v44, v28, v25
	v_pk_fma_f32 v[24:25], v[90:91], v[6:7], v[14:15]
	v_med3_f32 v26, v32, s94, v202
	v_max_f32_e32 v27, 0xc1898193, v24
	v_exp_f32_e32 v24, v27
	v_max_f32_e32 v25, 0xc1898193, v25
	v_pk_fma_f32 v[28:29], v[92:93], v[8:9], v[12:13]
	v_pk_fma_f32 v[30:31], v[96:97], v[4:5], v[36:37]
	v_add_f32_e32 v24, 1.0, v24
	v_rcp_f32_e32 v189, v24
	v_exp_f32_e32 v24, v25
	v_max_f32_e32 v29, 0xc1898193, v29
	v_mul_f32_e32 v27, v27, v189
	s_nop 0
	v_mul_f32_e32 v32, v26, v27
	v_max_f32_e32 v27, 0xc1898193, v28
	v_add_f32_e32 v24, 1.0, v24
	v_exp_f32_e32 v26, v27
	v_rcp_f32_e32 v189, v24
	v_med3_f32 v24, v33, s94, v202
	v_exp_f32_e32 v28, v29
	v_add_f32_e32 v26, 1.0, v26
	v_mul_f32_e32 v25, v25, v189
	v_rcp_f32_e32 v189, v26
	v_med3_f32 v26, v30, s94, v202
	v_mul_f32_e32 v33, v24, v25
	v_mul_f32_e32 v25, v27, v189
	v_mov_b32_e32 v24, v26
	v_add_f32_e32 v26, 1.0, v28
	v_rcp_f32_e32 v189, v26
	v_mul_f32_e32 v30, v24, v25
	v_cvt_pk_fp8_f32 v24, v21, v43
	v_med3_f32 v28, v31, s94, v202
	v_cvt_pk_fp8_f32 v25, v32, v33
	v_mul_f32_e32 v27, v29, v189
	v_cvt_pk_fp8_f32 v24, v11, v44 op_sel:[0,0,1]
	v_mul_f32_e32 v11, v28, v27
	v_cvt_pk_fp8_f32 v25, v30, v11 op_sel:[0,0,1]
	v_ashrrev_i32_e32 v21, 31, v20
	v_lshlrev_b64 v[20:21], 11, v[20:21]
	v_lshl_add_u64 v[20:21], s[12:13], 0, v[20:21]
	v_lshl_add_u64 v[20:21], v[20:21], 0, s[26:27]
	v_permlane16_swap_b32_e32 v22, v24
	v_permlane16_swap_b32_e32 v23, v25
	v_lshl_add_u64 v[20:21], v[20:21], 0, v[186:187]
	global_store_dwordx4 v[20:21], v[22:25], off
	v_pk_fma_f32 v[20:21], v[82:83], v[6:7], v[18:19]
	v_pk_fma_f32 v[28:29], v[86:87], v[2:3], v[38:39]
	v_max_f32_e32 v23, 0xc1898193, v20
	v_exp_f32_e32 v11, v23
	v_max_f32_e32 v21, 0xc1898193, v21
	v_med3_f32 v22, v28, s94, v202
	v_pk_fma_f32 v[24:25], v[84:85], v[8:9], v[16:17]
	v_add_f32_e32 v11, 1.0, v11
	v_rcp_f32_e32 v189, v11
	v_exp_f32_e32 v11, v21
	v_max_f32_e32 v25, 0xc1898193, v25
	v_pk_fma_f32 v[26:27], v[88:89], v[4:5], v[40:41]
	v_mul_f32_e32 v23, v23, v189
	v_add_f32_e32 v11, 1.0, v11
	v_mul_f32_e32 v30, v22, v23
	v_max_f32_e32 v23, 0xc1898193, v24
	v_rcp_f32_e32 v189, v11
	v_exp_f32_e32 v11, v23
	v_med3_f32 v20, v29, s94, v202
	v_med3_f32 v22, v26, s94, v202
	v_mul_f32_e32 v21, v21, v189
	v_add_f32_e32 v11, 1.0, v11
; template <class Epi, class Sched>
; __device__ __forceinline__ void gemm_phase(LAS unsigned char* lds, const Sched& S, const Epi& E) {
;     ...
;         cur = nxt; cA = nA; cB = nB; crot = nrot; ++ui;
;     __device__ __forceinline__ void prefetch(const pg8::Unit& u, Pre& q) const {
;         int tz = threadIdx.x; asm volatile("" : "+v"(tz)); const int wc = (tz >> 6) & 3, fq = (tz >> 4) & 3;
;         const int f0 = u.pn * 128 + wc * 32 + 8 * fq;
; #pragma unroll
;         for (int n = 0; n < 2; ++n) { q.bg[n] = *(const f32x4*)(b_gate + (size_t)u.e * FF + f0 + 4 * n) * KP; q.bu[n] = *(const f32x4*)(b_up + (size_t)u.e * FF + f0 + 4 * n); }
;     }
;     __device__ __forceinline__ void operator()(const f32x4 (&acc)[2][2][4][2], const pg8::Unit& u, const Pre& q, int wr, int wc, int fr, int fq) const {
;         const int row0 = u.pm * 256 + wr * 64 + fr, f0w = u.pn * 128 + wc * 32;
;         constexpr float DS = 1.0f / (FP8_SA * FP8_SW);
;         f32x4 dsk = (f32x4){DS * KP, DS * KP, DS * KP, DS * KP}, dsu = (f32x4){DS, DS, DS, DS}; asm volatile("" : "+v"(dsk), "+v"(dsu));
; #pragma unroll
;         for (int ai = 0; ai < 2; ++ai)
; #pragma unroll
;             for (int mp = 0; mp < 2; ++mp) { unsigned lo[2], hi[2];
; #pragma unroll
;                 for (int mm = 0; mm < 2; ++mm) { const int m = 2 * mp + mm; float h[8];
; #pragma unroll
;                     for (int n = 0; n < 2; ++n) { const f32x4 gk = __builtin_elementwise_fma(acc[ai][0][m][n], dsk, q.bg[n]), up = __builtin_elementwise_fma(acc[ai][1][m][n], dsu, q.bu[n]);
; #pragma unroll
;                         for (int j = 0; j < 4; ++j) { const float gm = __builtin_fmaxf(gk[j], 7.0f * KP), li = __builtin_amdgcn_fmed3f(up[j], -7.0f, 7.0f);
;                             const float sg = __builtin_amdgcn_rcpf(1.0f + __builtin_amdgcn_exp2f(gm));
;                             h[n * 4 + j] = (gm * sg) * (li * (FP8_SH / KP) + (FP8_SH / KP)); } }
;                     lo[mm] = pk4_fp8(h[0], h[1], h[2], h[3]); hi[mm] = pk4_fp8(h[4], h[5], h[6], h[7]); }
;                 const v2u r0 = __builtin_amdgcn_permlane16_swap(lo[0], lo[1], false, false), r1 = __builtin_amdgcn_permlane16_swap(hi[0], hi[1], false, false);
;                 unsigned char* rowp = hb + (size_t)(row0 + ai * 128 + (2 * mp + (fq & 1)) * 16) * FF + f0w + 16 * (fq >> 1);
;                 *(v4u*)rowp = (v4u){r0.x, r1.x, r0.y, r1.y}; }
;     }
	v_rcp_f32_e32 v189, v11
	v_exp_f32_e32 v11, v25
	v_mul_f32_e32 v31, v20, v21
	v_mul_f32_e32 v21, v23, v189
	v_add_f32_e32 v11, 1.0, v11
	v_rcp_f32_e32 v189, v11
	v_med3_f32 v24, v27, s94, v202
	v_mul_f32_e32 v11, v22, v21
	v_mul_f32_e32 v21, v25, v189
	v_pk_fma_f32 v[28:29], v[70:71], v[2:3], v[34:35]
	v_mul_f32_e32 v32, v24, v21
	v_pk_fma_f32 v[20:21], v[66:67], v[6:7], v[14:15]
	v_med3_f32 v22, v28, s94, v202
	v_max_f32_e32 v23, 0xc1898193, v20
	v_exp_f32_e32 v20, v23
	v_max_f32_e32 v21, 0xc1898193, v21
	v_pk_fma_f32 v[24:25], v[68:69], v[8:9], v[12:13]
	v_pk_fma_f32 v[26:27], v[72:73], v[4:5], v[36:37]
	v_add_f32_e32 v20, 1.0, v20
	v_rcp_f32_e32 v189, v20
	v_exp_f32_e32 v20, v21
	v_max_f32_e32 v25, 0xc1898193, v25
	v_pk_fma_f32 v[18:19], v[58:59], v[6:7], v[18:19]
	v_mul_f32_e32 v23, v23, v189
	v_add_f32_e32 v20, 1.0, v20
	v_mul_f32_e32 v28, v22, v23
	v_max_f32_e32 v23, 0xc1898193, v24
	v_exp_f32_e32 v22, v23
	v_rcp_f32_e32 v189, v20
	v_med3_f32 v20, v29, s94, v202
	v_exp_f32_e32 v24, v25
	v_add_f32_e32 v22, 1.0, v22
	v_mul_f32_e32 v21, v21, v189
	v_rcp_f32_e32 v189, v22
	v_med3_f32 v22, v26, s94, v202
	v_mul_f32_e32 v29, v20, v21
	v_mul_f32_e32 v21, v23, v189
	v_mov_b32_e32 v20, v22
	v_add_f32_e32 v22, 1.0, v24
	v_rcp_f32_e32 v189, v22
	v_mul_f32_e32 v26, v20, v21
	v_med3_f32 v24, v27, s94, v202
	v_cvt_pk_fp8_f32 v20, v30, v31
	v_mul_f32_e32 v23, v25, v189
	v_mul_f32_e32 v22, v24, v23
	v_max_f32_e32 v23, 0xc1898193, v18
	v_cvt_pk_fp8_f32 v20, v11, v32 op_sel:[0,0,1]
	v_exp_f32_e32 v11, v23
	v_cvt_pk_fp8_f32 v21, v28, v29
	v_max_f32_e32 v19, 0xc1898193, v19
	v_pk_fma_f32 v[16:17], v[60:61], v[8:9], v[16:17]
	v_add_f32_e32 v11, 1.0, v11
	v_rcp_f32_e32 v189, v11
	v_cvt_pk_fp8_f32 v21, v26, v22 op_sel:[0,0,1]
	v_pk_fma_f32 v[26:27], v[62:63], v[2:3], v[38:39]
	v_exp_f32_e32 v11, v19
	v_med3_f32 v22, v26, s94, v202
	v_mul_f32_e32 v23, v23, v189
	v_max_f32_e32 v17, 0xc1898193, v17
	v_mul_f32_e32 v26, v22, v23
	v_add_f32_e32 v11, 1.0, v11
	v_max_f32_e32 v23, 0xc1898193, v16
	v_rcp_f32_e32 v189, v11
	v_exp_f32_e32 v11, v23
	v_med3_f32 v18, v27, s94, v202
	v_pk_fma_f32 v[6:7], v[50:51], v[6:7], v[14:15]
	v_mul_f32_e32 v19, v19, v189
	v_add_f32_e32 v11, 1.0, v11
	v_rcp_f32_e32 v189, v11
	v_exp_f32_e32 v11, v17
	v_pk_fma_f32 v[24:25], v[64:65], v[4:5], v[40:41]
	v_max_f32_e32 v15, 0xc1898193, v6
	v_med3_f32 v22, v24, s94, v202
	v_add_f32_e32 v11, 1.0, v11
	v_exp_f32_e32 v6, v15
	v_mul_f32_e32 v27, v18, v19
	v_mul_f32_e32 v19, v23, v189
	v_mov_b32_e32 v18, v22
	v_rcp_f32_e32 v189, v11
	v_med3_f32 v16, v25, s94, v202
	v_add_f32_e32 v6, 1.0, v6
	v_pk_fma_f32 v[2:3], v[54:55], v[2:3], v[34:35]
	v_mul_f32_e32 v17, v17, v189
	v_rcp_f32_e32 v189, v6
	v_max_f32_e32 v7, 0xc1898193, v7
	v_med3_f32 v14, v2, s94, v202
	v_exp_f32_e32 v2, v7
	v_pk_fma_f32 v[8:9], v[52:53], v[8:9], v[12:13]
	v_mul_f32_e32 v13, v15, v189
	v_pk_fma_f32 v[4:5], v[56:57], v[4:5], v[36:37]
	v_mul_f32_e32 v14, v14, v13
	v_add_f32_e32 v2, 1.0, v2
	v_max_f32_e32 v13, 0xc1898193, v8
	v_rcp_f32_e32 v189, v2
	v_exp_f32_e32 v8, v13
	v_med3_f32 v6, v3, s94, v202
	v_med3_f32 v12, v4, s94, v202
	v_mul_f32_e32 v3, v7, v189
	v_mov_b32_e32 v2, v6
	v_add_f32_e32 v6, 1.0, v8
	v_max_f32_e32 v7, 0xc1898193, v9
	v_rcp_f32_e32 v189, v6
	v_exp_f32_e32 v6, v7
	v_mul_f32_e32 v8, v2, v3
	v_mul_f32_e32 v3, v13, v189
	v_add_f32_e32 v4, 1.0, v6
	v_rcp_f32_e32 v189, v4
	v_med3_f32 v6, v5, s94, v202
	v_cvt_pk_fp8_f32 v23, v14, v8
	v_mul_f32_e32 v4, v12, v3
	v_mul_f32_e32 v3, v7, v189
	v_cvt_pk_fp8_f32 v22, v26, v27
	v_mul_f32_e32 v2, v6, v3
	v_mul_f32_e32 v11, v18, v19
	v_mul_f32_e32 v16, v16, v17
	v_cvt_pk_fp8_f32 v23, v4, v2 op_sel:[0,0,1]
	v_add_u32_e32 v2, 0xa0, v10
	v_cvt_pk_fp8_f32 v22, v11, v16 op_sel:[0,0,1]
	v_ashrrev_i32_e32 v3, 31, v2
	v_lshlrev_b64 v[2:3], 11, v[2:3]
	v_lshl_add_u64 v[2:3], s[12:13], 0, v[2:3]
	v_lshl_add_u64 v[2:3], v[2:3], 0, s[26:27]
	v_permlane16_swap_b32_e32 v20, v22
	v_permlane16_swap_b32_e32 v21, v23
	v_lshl_add_u64 v[2:3], v[2:3], 0, v[186:187]
	global_store_dwordx4 v[2:3], v[20:23], off
	s_cbranch_vccnz .LBB0_726
	v_mov_b32_e32 v2, v0
	s_ashr_i32 s21, s20, 31
	v_readlane_b32 s72, v255, 29
	v_lshrrev_b32_e32 v2, 1, v2
	s_lshl_b64 s[2:3], s[20:21], 13
	v_readlane_b32 s76, v255, 33
	v_and_b32_e32 v2, 0x78, v2
	v_readlane_b32 s77, v255, 34
	s_add_u32 s26, s76, s2
	v_lshl_or_b32 v2, s44, 7, v2
	v_readlane_b32 s80, v255, 37
	s_addc_u32 s27, s77, s3
	v_ashrrev_i32_e32 v3, 31, v2
	v_readlane_b32 s81, v255, 38
	s_add_u32 s2, s80, s2
	v_lshlrev_b64 v[2:3], 2, v[2:3]
	s_addc_u32 s3, s81, s3
	v_lshl_add_u64 v[4:5], s[26:27], 0, v[2:3]
	v_lshl_add_u64 v[2:3], s[2:3], 0, v[2:3]
	global_load_dwordx4 v[74:77], v[4:5], off offset:16
	global_load_dwordx4 v[78:81], v[4:5], off
	global_load_dwordx4 v[34:37], v[2:3], off offset:16
	global_load_dwordx4 v[38:41], v[2:3], off
	v_readlane_b32 s2, v255, 53
	v_readlane_b32 s3, v255, 54
	s_andn2_b64 vcc, exec, s[2:3]
	v_readlane_b32 s73, v255, 30
	v_readlane_b32 s74, v255, 31
	v_readlane_b32 s75, v255, 32
	v_readlane_b32 s78, v255, 35
	v_readlane_b32 s79, v255, 36
	v_readlane_b32 s82, v255, 39
	v_readlane_b32 s83, v255, 40
	v_readlane_b32 s84, v255, 41
	v_readlane_b32 s85, v255, 42
	v_readlane_b32 s86, v255, 43
	v_readlane_b32 s87, v255, 44
	s_cbranch_vccnz .LBB0_725
	s_barrier
	s_branch .LBB0_725

; __device__ __forceinline__ float sat8(float x) { return __builtin_amdgcn_fmed3f(x, -448.0f, 448.0f); }
; __device__ __forceinline__ unsigned pk4_fp8(float a, float b, float c, float d) { int v = 0; v = __builtin_amdgcn_cvt_pk_fp8_f32(a, b, v, false); v = __builtin_amdgcn_cvt_pk_fp8_f32(c, d, v, true); return (unsigned)v; }
;     __device__ __forceinline__ void operator()(const f32x4 (&acc)[2][2][4][2], const pg8::Unit& u, const Pre& q, int wr, int wc, int fr, int fq) const {
;         const int rl0 = wr * 64 + fr, colw = u.pn * 256 + wc * 32;
;         constexpr float DS = 1.0f / (FP8_SH * FP8_SW);
; #pragma unroll
;         for (int ai = 0; ai < 2; ++ai)
; #pragma unroll
;             for (int mp = 0; mp < 2; ++mp)
; #pragma unroll
;                 for (int bj = 0; bj < 2; ++bj) { unsigned lo[2], hi[2];
; #pragma unroll
;                     for (int mm = 0; mm < 2; ++mm) { const int m = 2 * mp + mm; const float gt = q.gt[ai][m] * FP8_SY;
;                         const f32x4 v0 = (acc[ai][bj][m][0] * DS + q.bv[bj][0]) * gt, v1 = (acc[ai][bj][m][1] * DS + q.bv[bj][1]) * gt;
;                         lo[mm] = pk4_fp8(sat8(v0[0]), sat8(v0[1]), sat8(v0[2]), sat8(v0[3])); hi[mm] = pk4_fp8(sat8(v1[0]), sat8(v1[1]), sat8(v1[2]), sat8(v1[3])); }
;                     const v2u r0 = __builtin_amdgcn_permlane16_swap(lo[0], lo[1], false, false), r1 = __builtin_amdgcn_permlane16_swap(hi[0], hi[1], false, false);
;                     unsigned char* rowp = y2 + (size_t)(u.pm * 256 + rl0 + ai * 128 + (2 * mp + (fq & 1)) * 16) * D + colw + bj * 128 + 16 * (fq >> 1);
;                     *(v4u*)rowp = (v4u){r0.x, r1.x, r0.y, r1.y}; }
;     }
.LBB0_810:
	v_mov_b32_e32 v3, v0
	s_lshl_b32 s24, s24, 8
	v_readfirstlane_b32 s15, v3
	s_ashr_i32 s17, s15, 2
	s_lshr_b32 s15, s15, 1
	s_and_b32 s15, s15, 0x60
	s_andn2_b32 s17, s17, 63
	s_or_b32 s24, s15, s24
	s_lshl_b32 s15, s22, 8
	s_add_i32 s17, s17, s15
	v_and_or_b32 v2, v3, 31, s17
	v_lshrrev_b32_e32 v3, 1, v3
	s_waitcnt vmcnt(8)
	v_mul_f32_e32 v10, 0x42000000, v197
	v_pk_fma_f32 v[4:5], v[176:177], s[10:11], v[48:49] op_sel_hi:[1,0,1]
	v_pk_fma_f32 v[6:7], v[174:175], s[10:11], v[46:47] op_sel_hi:[1,0,1]
	v_and_b32_e32 v178, 16, v3
	v_ashrrev_i32_e32 v3, 31, v2
	v_pk_mul_f32 v[4:5], v[10:11], v[4:5] op_sel_hi:[0,1]
	v_pk_mul_f32 v[6:7], v[10:11], v[6:7] op_sel_hi:[0,1]
	v_pk_fma_f32 v[14:15], v[170:171], s[10:11], v[42:43] op_sel_hi:[1,0,1]
	v_lshlrev_b64 v[8:9], 11, v[2:3]
	v_pk_fma_f32 v[12:13], v[172:173], s[10:11], v[44:45] op_sel_hi:[1,0,1]
	v_pk_mul_f32 v[14:15], v[10:11], v[14:15] op_sel_hi:[0,1]
	v_med3_f32 v3, v6, s79, v189
	v_med3_f32 v6, v7, s79, v189
	v_med3_f32 v7, v4, s79, v189
	v_pk_mul_f32 v[12:13], v[10:11], v[12:13] op_sel_hi:[0,1]
	v_med3_f32 v11, v5, s79, v189
	v_cvt_pk_fp8_f32 v4, v3, v6
	v_med3_f32 v3, v14, s79, v189
	v_med3_f32 v6, v15, s79, v189
	v_cvt_pk_fp8_f32 v5, v3, v6
	v_med3_f32 v3, v12, s79, v189
	v_med3_f32 v6, v13, s79, v189
	v_cvt_pk_fp8_f32 v4, v7, v11 op_sel:[0,0,1]
	v_cvt_pk_fp8_f32 v5, v3, v6 op_sel:[0,0,1]
	v_mul_f32_e32 v12, 0x42000000, v196
	v_pk_fma_f32 v[6:7], v[168:169], s[10:11], v[48:49] op_sel_hi:[1,0,1]
	v_pk_fma_f32 v[14:15], v[166:167], s[10:11], v[46:47] op_sel_hi:[1,0,1]
	v_pk_mul_f32 v[6:7], v[12:13], v[6:7] op_sel_hi:[0,1]
	v_pk_mul_f32 v[14:15], v[12:13], v[14:15] op_sel_hi:[0,1]
	v_pk_fma_f32 v[16:17], v[164:165], s[10:11], v[44:45] op_sel_hi:[1,0,1]
	v_pk_fma_f32 v[18:19], v[162:163], s[10:11], v[42:43] op_sel_hi:[1,0,1]
	v_pk_mul_f32 v[16:17], v[12:13], v[16:17] op_sel_hi:[0,1]
	v_pk_mul_f32 v[18:19], v[12:13], v[18:19] op_sel_hi:[0,1]
	v_med3_f32 v3, v14, s79, v189
	v_med3_f32 v11, v15, s79, v189
	v_med3_f32 v13, v6, s79, v189
	v_med3_f32 v14, v7, s79, v189
	v_cvt_pk_fp8_f32 v6, v3, v11
	v_med3_f32 v3, v18, s79, v189
	v_med3_f32 v11, v19, s79, v189
	v_cvt_pk_fp8_f32 v7, v3, v11
	v_med3_f32 v3, v16, s79, v189
	v_med3_f32 v11, v17, s79, v189
	v_cvt_pk_fp8_f32 v6, v13, v14 op_sel:[0,0,1]
	v_cvt_pk_fp8_f32 v7, v3, v11 op_sel:[0,0,1]
	s_ashr_i32 s25, s24, 31
	v_lshl_add_u64 v[8:9], s[6:7], 0, v[8:9]
	v_lshl_add_u64 v[8:9], v[8:9], 0, s[24:25]
	v_permlane16_swap_b32_e32 v4, v6
	v_permlane16_swap_b32_e32 v5, v7
	v_lshl_add_u64 v[8:9], v[8:9], 0, v[178:179]
	global_store_dwordx4 v[8:9], v[4:7], off
	v_pk_fma_f32 v[14:15], v[156:157], s[10:11], v[36:37] op_sel_hi:[1,0,1]
	v_pk_fma_f32 v[16:17], v[154:155], s[10:11], v[34:35] op_sel_hi:[1,0,1]
	v_pk_fma_f32 v[4:5], v[160:161], s[10:11], v[40:41] op_sel_hi:[1,0,1]
	v_pk_fma_f32 v[6:7], v[158:159], s[10:11], v[38:39] op_sel_hi:[1,0,1]
	v_pk_mul_f32 v[4:5], v[10:11], v[4:5] op_sel_hi:[0,1]
	v_pk_mul_f32 v[6:7], v[10:11], v[6:7] op_sel_hi:[0,1]
	v_pk_mul_f32 v[14:15], v[10:11], v[14:15] op_sel_hi:[0,1]
	v_pk_mul_f32 v[10:11], v[10:11], v[16:17] op_sel_hi:[0,1]
	v_med3_f32 v3, v6, s79, v189
	v_med3_f32 v6, v7, s79, v189
	v_med3_f32 v7, v4, s79, v189
	v_med3_f32 v13, v5, s79, v189
	v_cvt_pk_fp8_f32 v4, v3, v6
	v_med3_f32 v3, v10, s79, v189
	v_med3_f32 v6, v11, s79, v189
	v_cvt_pk_fp8_f32 v5, v3, v6
	v_med3_f32 v3, v14, s79, v189
	v_med3_f32 v6, v15, s79, v189
	v_cvt_pk_fp8_f32 v4, v7, v13 op_sel:[0,0,1]
	v_cvt_pk_fp8_f32 v5, v3, v6 op_sel:[0,0,1]
	v_pk_fma_f32 v[6:7], v[152:153], s[10:11], v[40:41] op_sel_hi:[1,0,1]
	v_pk_fma_f32 v[10:11], v[150:151], s[10:11], v[38:39] op_sel_hi:[1,0,1]
	v_pk_mul_f32 v[6:7], v[12:13], v[6:7] op_sel_hi:[0,1]
	v_pk_mul_f32 v[10:11], v[12:13], v[10:11] op_sel_hi:[0,1]
	v_pk_fma_f32 v[14:15], v[148:149], s[10:11], v[36:37] op_sel_hi:[1,0,1]
	v_pk_fma_f32 v[16:17], v[146:147], s[10:11], v[34:35] op_sel_hi:[1,0,1]
	v_pk_mul_f32 v[14:15], v[12:13], v[14:15] op_sel_hi:[0,1]
	v_pk_mul_f32 v[12:13], v[12:13], v[16:17] op_sel_hi:[0,1]
	v_med3_f32 v3, v10, s79, v189
	v_med3_f32 v10, v11, s79, v189
	v_med3_f32 v11, v6, s79, v189
	v_med3_f32 v16, v7, s79, v189
	v_cvt_pk_fp8_f32 v6, v3, v10
	v_med3_f32 v3, v12, s79, v189
	v_med3_f32 v10, v13, s79, v189
	v_cvt_pk_fp8_f32 v7, v3, v10
	v_med3_f32 v3, v14, s79, v189
	v_med3_f32 v10, v15, s79, v189
	v_cvt_pk_fp8_f32 v6, v11, v16 op_sel:[0,0,1]
	v_cvt_pk_fp8_f32 v7, v3, v10 op_sel:[0,0,1]
	v_mul_f32_e32 v10, 0x42000000, v195
	v_pk_fma_f32 v[14:15], v[138:139], s[10:11], v[42:43] op_sel_hi:[1,0,1]
	v_permlane16_swap_b32_e32 v4, v6
	v_permlane16_swap_b32_e32 v5, v7
	global_store_dwordx4 v[8:9], v[4:7], off offset:128
	v_pk_fma_f32 v[12:13], v[140:141], s[10:11], v[44:45] op_sel_hi:[1,0,1]
	v_pk_mul_f32 v[14:15], v[10:11], v[14:15] op_sel_hi:[0,1]
	v_or_b32_e32 v4, 32, v2
	v_ashrrev_i32_e32 v5, 31, v4
	v_lshlrev_b64 v[8:9], 11, v[4:5]
	v_pk_fma_f32 v[4:5], v[144:145], s[10:11], v[48:49] op_sel_hi:[1,0,1]
	v_pk_fma_f32 v[6:7], v[142:143], s[10:11], v[46:47] op_sel_hi:[1,0,1]
	v_pk_mul_f32 v[4:5], v[10:11], v[4:5] op_sel_hi:[0,1]
	v_pk_mul_f32 v[6:7], v[10:11], v[6:7] op_sel_hi:[0,1]
	v_med3_f32 v3, v6, s79, v189
	v_med3_f32 v6, v7, s79, v189
	v_med3_f32 v7, v4, s79, v189
	v_pk_mul_f32 v[12:13], v[10:11], v[12:13] op_sel_hi:[0,1]
	v_med3_f32 v11, v5, s79, v189
	v_cvt_pk_fp8_f32 v4, v3, v6
	v_med3_f32 v3, v14, s79, v189
	v_med3_f32 v6, v15, s79, v189
	v_cvt_pk_fp8_f32 v5, v3, v6
	v_med3_f32 v3, v12, s79, v189
	v_med3_f32 v6, v13, s79, v189
	v_cvt_pk_fp8_f32 v4, v7, v11 op_sel:[0,0,1]
	v_cvt_pk_fp8_f32 v5, v3, v6 op_sel:[0,0,1]
	v_mul_f32_e32 v12, 0x42000000, v194
; __device__ __forceinline__ float sat8(float x) { return __builtin_amdgcn_fmed3f(x, -448.0f, 448.0f); }
; __device__ __forceinline__ unsigned pk4_fp8(float a, float b, float c, float d) { int v = 0; v = __builtin_amdgcn_cvt_pk_fp8_f32(a, b, v, false); v = __builtin_amdgcn_cvt_pk_fp8_f32(c, d, v, true); return (unsigned)v; }
;     __device__ __forceinline__ void operator()(const f32x4 (&acc)[2][2][4][2], const pg8::Unit& u, const Pre& q, int wr, int wc, int fr, int fq) const {
;         const int rl0 = wr * 64 + fr, colw = u.pn * 256 + wc * 32;
;         constexpr float DS = 1.0f / (FP8_SH * FP8_SW);
; #pragma unroll
;         for (int ai = 0; ai < 2; ++ai)
; #pragma unroll
;             for (int mp = 0; mp < 2; ++mp)
; #pragma unroll
;                 for (int bj = 0; bj < 2; ++bj) { unsigned lo[2], hi[2];
; #pragma unroll
;                     for (int mm = 0; mm < 2; ++mm) { const int m = 2 * mp + mm; const float gt = q.gt[ai][m] * FP8_SY;
;                         const f32x4 v0 = (acc[ai][bj][m][0] * DS + q.bv[bj][0]) * gt, v1 = (acc[ai][bj][m][1] * DS + q.bv[bj][1]) * gt;
;                         lo[mm] = pk4_fp8(sat8(v0[0]), sat8(v0[1]), sat8(v0[2]), sat8(v0[3])); hi[mm] = pk4_fp8(sat8(v1[0]), sat8(v1[1]), sat8(v1[2]), sat8(v1[3])); }
;                     const v2u r0 = __builtin_amdgcn_permlane16_swap(lo[0], lo[1], false, false), r1 = __builtin_amdgcn_permlane16_swap(hi[0], hi[1], false, false);
;                     unsigned char* rowp = y2 + (size_t)(u.pm * 256 + rl0 + ai * 128 + (2 * mp + (fq & 1)) * 16) * D + colw + bj * 128 + 16 * (fq >> 1);
;                     *(v4u*)rowp = (v4u){r0.x, r1.x, r0.y, r1.y}; }
;     }
	v_pk_fma_f32 v[6:7], v[136:137], s[10:11], v[48:49] op_sel_hi:[1,0,1]
	v_pk_fma_f32 v[14:15], v[134:135], s[10:11], v[46:47] op_sel_hi:[1,0,1]
	v_pk_mul_f32 v[6:7], v[12:13], v[6:7] op_sel_hi:[0,1]
	v_pk_mul_f32 v[14:15], v[12:13], v[14:15] op_sel_hi:[0,1]
	v_pk_fma_f32 v[16:17], v[132:133], s[10:11], v[44:45] op_sel_hi:[1,0,1]
	v_pk_fma_f32 v[18:19], v[130:131], s[10:11], v[42:43] op_sel_hi:[1,0,1]
	v_pk_mul_f32 v[16:17], v[12:13], v[16:17] op_sel_hi:[0,1]
	v_pk_mul_f32 v[18:19], v[12:13], v[18:19] op_sel_hi:[0,1]
	v_med3_f32 v3, v14, s79, v189
	v_med3_f32 v11, v15, s79, v189
	v_med3_f32 v13, v6, s79, v189
	v_med3_f32 v14, v7, s79, v189
	v_cvt_pk_fp8_f32 v6, v3, v11
	v_med3_f32 v3, v18, s79, v189
	v_med3_f32 v11, v19, s79, v189
	v_cvt_pk_fp8_f32 v7, v3, v11
	v_med3_f32 v3, v16, s79, v189
	v_med3_f32 v11, v17, s79, v189
	v_cvt_pk_fp8_f32 v6, v13, v14 op_sel:[0,0,1]
	v_cvt_pk_fp8_f32 v7, v3, v11 op_sel:[0,0,1]
	v_lshl_add_u64 v[8:9], s[6:7], 0, v[8:9]
	v_lshl_add_u64 v[8:9], v[8:9], 0, s[24:25]
	v_permlane16_swap_b32_e32 v4, v6
	v_permlane16_swap_b32_e32 v5, v7
	v_lshl_add_u64 v[8:9], v[8:9], 0, v[178:179]
	global_store_dwordx4 v[8:9], v[4:7], off
	v_pk_fma_f32 v[14:15], v[124:125], s[10:11], v[36:37] op_sel_hi:[1,0,1]
	v_pk_fma_f32 v[16:17], v[122:123], s[10:11], v[34:35] op_sel_hi:[1,0,1]
	v_pk_fma_f32 v[4:5], v[128:129], s[10:11], v[40:41] op_sel_hi:[1,0,1]
	v_pk_fma_f32 v[6:7], v[126:127], s[10:11], v[38:39] op_sel_hi:[1,0,1]
	v_pk_mul_f32 v[4:5], v[10:11], v[4:5] op_sel_hi:[0,1]
	v_pk_mul_f32 v[6:7], v[10:11], v[6:7] op_sel_hi:[0,1]
	v_pk_mul_f32 v[14:15], v[10:11], v[14:15] op_sel_hi:[0,1]
	v_pk_mul_f32 v[10:11], v[10:11], v[16:17] op_sel_hi:[0,1]
	v_med3_f32 v3, v6, s79, v189
	v_med3_f32 v6, v7, s79, v189
	v_med3_f32 v7, v4, s79, v189
	v_med3_f32 v13, v5, s79, v189
	v_cvt_pk_fp8_f32 v4, v3, v6
	v_med3_f32 v3, v10, s79, v189
	v_med3_f32 v6, v11, s79, v189
	v_cvt_pk_fp8_f32 v5, v3, v6
	v_med3_f32 v3, v14, s79, v189
	v_med3_f32 v6, v15, s79, v189
	v_cvt_pk_fp8_f32 v4, v7, v13 op_sel:[0,0,1]
	v_cvt_pk_fp8_f32 v5, v3, v6 op_sel:[0,0,1]
	v_pk_fma_f32 v[6:7], v[120:121], s[10:11], v[40:41] op_sel_hi:[1,0,1]
	v_pk_fma_f32 v[10:11], v[118:119], s[10:11], v[38:39] op_sel_hi:[1,0,1]
	v_pk_mul_f32 v[6:7], v[12:13], v[6:7] op_sel_hi:[0,1]
	v_pk_mul_f32 v[10:11], v[12:13], v[10:11] op_sel_hi:[0,1]
	v_pk_fma_f32 v[14:15], v[116:117], s[10:11], v[36:37] op_sel_hi:[1,0,1]
	v_pk_fma_f32 v[16:17], v[114:115], s[10:11], v[34:35] op_sel_hi:[1,0,1]
	v_pk_mul_f32 v[14:15], v[12:13], v[14:15] op_sel_hi:[0,1]
	v_pk_mul_f32 v[12:13], v[12:13], v[16:17] op_sel_hi:[0,1]
	v_med3_f32 v3, v10, s79, v189
	v_med3_f32 v10, v11, s79, v189
	v_med3_f32 v11, v6, s79, v189
	v_med3_f32 v16, v7, s79, v189
	v_cvt_pk_fp8_f32 v6, v3, v10
	v_med3_f32 v3, v12, s79, v189
	v_med3_f32 v10, v13, s79, v189
	v_cvt_pk_fp8_f32 v7, v3, v10
	v_med3_f32 v3, v14, s79, v189
	v_med3_f32 v10, v15, s79, v189
	v_cvt_pk_fp8_f32 v6, v11, v16 op_sel:[0,0,1]
	v_cvt_pk_fp8_f32 v7, v3, v10 op_sel:[0,0,1]
	v_mul_f32_e32 v10, 0x42000000, v193
	v_pk_fma_f32 v[14:15], v[106:107], s[10:11], v[42:43] op_sel_hi:[1,0,1]
	v_permlane16_swap_b32_e32 v4, v6
	v_permlane16_swap_b32_e32 v5, v7
	global_store_dwordx4 v[8:9], v[4:7], off offset:128
	v_pk_fma_f32 v[12:13], v[108:109], s[10:11], v[44:45] op_sel_hi:[1,0,1]
	v_pk_mul_f32 v[14:15], v[10:11], v[14:15] op_sel_hi:[0,1]
	v_add_u32_e32 v4, 0x80, v2
	v_ashrrev_i32_e32 v5, 31, v4
	v_lshlrev_b64 v[8:9], 11, v[4:5]
	v_pk_fma_f32 v[4:5], v[112:113], s[10:11], v[48:49] op_sel_hi:[1,0,1]
	v_pk_fma_f32 v[6:7], v[110:111], s[10:11], v[46:47] op_sel_hi:[1,0,1]
	v_pk_mul_f32 v[4:5], v[10:11], v[4:5] op_sel_hi:[0,1]
	v_pk_mul_f32 v[6:7], v[10:11], v[6:7] op_sel_hi:[0,1]
	v_med3_f32 v3, v6, s79, v189
	v_med3_f32 v6, v7, s79, v189
	v_med3_f32 v7, v4, s79, v189
	v_pk_mul_f32 v[12:13], v[10:11], v[12:13] op_sel_hi:[0,1]
	v_med3_f32 v11, v5, s79, v189
	v_cvt_pk_fp8_f32 v4, v3, v6
	v_med3_f32 v3, v14, s79, v189
	v_med3_f32 v6, v15, s79, v189
	v_cvt_pk_fp8_f32 v5, v3, v6
	v_med3_f32 v3, v12, s79, v189
	v_med3_f32 v6, v13, s79, v189
	v_cvt_pk_fp8_f32 v4, v7, v11 op_sel:[0,0,1]
	v_cvt_pk_fp8_f32 v5, v3, v6 op_sel:[0,0,1]
	v_mul_f32_e32 v12, 0x42000000, v192
	v_pk_fma_f32 v[6:7], v[104:105], s[10:11], v[48:49] op_sel_hi:[1,0,1]
	v_pk_fma_f32 v[14:15], v[102:103], s[10:11], v[46:47] op_sel_hi:[1,0,1]
	v_pk_mul_f32 v[6:7], v[12:13], v[6:7] op_sel_hi:[0,1]
	v_pk_mul_f32 v[14:15], v[12:13], v[14:15] op_sel_hi:[0,1]
	v_pk_fma_f32 v[16:17], v[100:101], s[10:11], v[44:45] op_sel_hi:[1,0,1]
	v_pk_fma_f32 v[18:19], v[98:99], s[10:11], v[42:43] op_sel_hi:[1,0,1]
	v_pk_mul_f32 v[16:17], v[12:13], v[16:17] op_sel_hi:[0,1]
	v_pk_mul_f32 v[18:19], v[12:13], v[18:19] op_sel_hi:[0,1]
	v_med3_f32 v3, v14, s79, v189
	v_med3_f32 v11, v15, s79, v189
	v_med3_f32 v13, v6, s79, v189
	v_med3_f32 v14, v7, s79, v189
	v_cvt_pk_fp8_f32 v6, v3, v11
	v_med3_f32 v3, v18, s79, v189
	v_med3_f32 v11, v19, s79, v189
	v_cvt_pk_fp8_f32 v7, v3, v11
	v_med3_f32 v3, v16, s79, v189
	v_med3_f32 v11, v17, s79, v189
	v_cvt_pk_fp8_f32 v6, v13, v14 op_sel:[0,0,1]
	v_cvt_pk_fp8_f32 v7, v3, v11 op_sel:[0,0,1]
	v_lshl_add_u64 v[8:9], s[6:7], 0, v[8:9]
	v_lshl_add_u64 v[8:9], v[8:9], 0, s[24:25]
	v_permlane16_swap_b32_e32 v4, v6
	v_permlane16_swap_b32_e32 v5, v7
	v_lshl_add_u64 v[8:9], v[8:9], 0, v[178:179]
	global_store_dwordx4 v[8:9], v[4:7], off
	v_pk_fma_f32 v[14:15], v[92:93], s[10:11], v[36:37] op_sel_hi:[1,0,1]
	v_pk_fma_f32 v[16:17], v[90:91], s[10:11], v[34:35] op_sel_hi:[1,0,1]
	v_pk_fma_f32 v[4:5], v[96:97], s[10:11], v[40:41] op_sel_hi:[1,0,1]
	v_pk_fma_f32 v[6:7], v[94:95], s[10:11], v[38:39] op_sel_hi:[1,0,1]
; __device__ __forceinline__ float sat8(float x) { return __builtin_amdgcn_fmed3f(x, -448.0f, 448.0f); }
; __device__ __forceinline__ unsigned pk4_fp8(float a, float b, float c, float d) { int v = 0; v = __builtin_amdgcn_cvt_pk_fp8_f32(a, b, v, false); v = __builtin_amdgcn_cvt_pk_fp8_f32(c, d, v, true); return (unsigned)v; }
;     __device__ __forceinline__ void operator()(const f32x4 (&acc)[2][2][4][2], const pg8::Unit& u, const Pre& q, int wr, int wc, int fr, int fq) const {
;         const int rl0 = wr * 64 + fr, colw = u.pn * 256 + wc * 32;
;         constexpr float DS = 1.0f / (FP8_SH * FP8_SW);
; #pragma unroll
;         for (int ai = 0; ai < 2; ++ai)
; #pragma unroll
;             for (int mp = 0; mp < 2; ++mp)
; #pragma unroll
;                 for (int bj = 0; bj < 2; ++bj) { unsigned lo[2], hi[2];
; #pragma unroll
;                     for (int mm = 0; mm < 2; ++mm) { const int m = 2 * mp + mm; const float gt = q.gt[ai][m] * FP8_SY;
;                         const f32x4 v0 = (acc[ai][bj][m][0] * DS + q.bv[bj][0]) * gt, v1 = (acc[ai][bj][m][1] * DS + q.bv[bj][1]) * gt;
;                         lo[mm] = pk4_fp8(sat8(v0[0]), sat8(v0[1]), sat8(v0[2]), sat8(v0[3])); hi[mm] = pk4_fp8(sat8(v1[0]), sat8(v1[1]), sat8(v1[2]), sat8(v1[3])); }
;                     const v2u r0 = __builtin_amdgcn_permlane16_swap(lo[0], lo[1], false, false), r1 = __builtin_amdgcn_permlane16_swap(hi[0], hi[1], false, false);
;                     unsigned char* rowp = y2 + (size_t)(u.pm * 256 + rl0 + ai * 128 + (2 * mp + (fq & 1)) * 16) * D + colw + bj * 128 + 16 * (fq >> 1);
;                     *(v4u*)rowp = (v4u){r0.x, r1.x, r0.y, r1.y}; }
;     }
	v_pk_mul_f32 v[4:5], v[10:11], v[4:5] op_sel_hi:[0,1]
	v_pk_mul_f32 v[6:7], v[10:11], v[6:7] op_sel_hi:[0,1]
	v_pk_mul_f32 v[14:15], v[10:11], v[14:15] op_sel_hi:[0,1]
	v_pk_mul_f32 v[10:11], v[10:11], v[16:17] op_sel_hi:[0,1]
	v_med3_f32 v3, v6, s79, v189
	v_med3_f32 v6, v7, s79, v189
	v_med3_f32 v7, v4, s79, v189
	v_med3_f32 v13, v5, s79, v189
	v_cvt_pk_fp8_f32 v4, v3, v6
	v_med3_f32 v3, v10, s79, v189
	v_med3_f32 v6, v11, s79, v189
	v_cvt_pk_fp8_f32 v5, v3, v6
	v_med3_f32 v3, v14, s79, v189
	v_med3_f32 v6, v15, s79, v189
	v_cvt_pk_fp8_f32 v4, v7, v13 op_sel:[0,0,1]
	v_cvt_pk_fp8_f32 v5, v3, v6 op_sel:[0,0,1]
	v_pk_fma_f32 v[6:7], v[88:89], s[10:11], v[40:41] op_sel_hi:[1,0,1]
	v_pk_fma_f32 v[10:11], v[86:87], s[10:11], v[38:39] op_sel_hi:[1,0,1]
	v_pk_mul_f32 v[6:7], v[12:13], v[6:7] op_sel_hi:[0,1]
	v_pk_mul_f32 v[10:11], v[12:13], v[10:11] op_sel_hi:[0,1]
	v_pk_fma_f32 v[14:15], v[84:85], s[10:11], v[36:37] op_sel_hi:[1,0,1]
	v_pk_fma_f32 v[16:17], v[82:83], s[10:11], v[34:35] op_sel_hi:[1,0,1]
	v_pk_mul_f32 v[14:15], v[12:13], v[14:15] op_sel_hi:[0,1]
	v_pk_mul_f32 v[12:13], v[12:13], v[16:17] op_sel_hi:[0,1]
	v_med3_f32 v3, v10, s79, v189
	v_med3_f32 v10, v11, s79, v189
	v_med3_f32 v11, v6, s79, v189
	v_med3_f32 v16, v7, s79, v189
	v_cvt_pk_fp8_f32 v6, v3, v10
	v_med3_f32 v3, v12, s79, v189
	v_med3_f32 v10, v13, s79, v189
	v_cvt_pk_fp8_f32 v7, v3, v10
	v_med3_f32 v3, v14, s79, v189
	v_med3_f32 v10, v15, s79, v189
	v_cvt_pk_fp8_f32 v6, v11, v16 op_sel:[0,0,1]
	v_cvt_pk_fp8_f32 v7, v3, v10 op_sel:[0,0,1]
	v_add_u32_e32 v2, 0xa0, v2
	v_ashrrev_i32_e32 v3, 31, v2
	v_permlane16_swap_b32_e32 v4, v6
	v_permlane16_swap_b32_e32 v5, v7
	global_store_dwordx4 v[8:9], v[4:7], off offset:128
	v_mul_f32_e32 v8, 0x42000000, v191
	v_pk_fma_f32 v[10:11], v[76:77], s[10:11], v[44:45] op_sel_hi:[1,0,1]
	v_lshlrev_b64 v[6:7], 11, v[2:3]
	v_pk_fma_f32 v[2:3], v[80:81], s[10:11], v[48:49] op_sel_hi:[1,0,1]
	v_pk_fma_f32 v[4:5], v[78:79], s[10:11], v[46:47] op_sel_hi:[1,0,1]
	v_pk_mul_f32 v[2:3], v[8:9], v[2:3] op_sel_hi:[0,1]
	v_pk_mul_f32 v[4:5], v[8:9], v[4:5] op_sel_hi:[0,1]
	v_pk_fma_f32 v[12:13], v[74:75], s[10:11], v[42:43] op_sel_hi:[1,0,1]
	v_pk_mul_f32 v[10:11], v[8:9], v[10:11] op_sel_hi:[0,1]
	v_pk_mul_f32 v[12:13], v[8:9], v[12:13] op_sel_hi:[0,1]
	v_med3_f32 v4, v4, s79, v189
	v_med3_f32 v5, v5, s79, v189
	v_med3_f32 v9, v2, s79, v189
	v_med3_f32 v14, v3, s79, v189
	v_cvt_pk_fp8_f32 v2, v4, v5
	v_med3_f32 v4, v12, s79, v189
	v_med3_f32 v5, v13, s79, v189
	v_cvt_pk_fp8_f32 v3, v4, v5
	v_med3_f32 v4, v10, s79, v189
	v_med3_f32 v5, v11, s79, v189
	v_mul_f32_e32 v10, 0x42000000, v190
	v_cvt_pk_fp8_f32 v3, v4, v5 op_sel:[0,0,1]
	v_pk_fma_f32 v[4:5], v[72:73], s[10:11], v[48:49] op_sel_hi:[1,0,1]
	v_pk_fma_f32 v[12:13], v[70:71], s[10:11], v[46:47] op_sel_hi:[1,0,1]
	v_cvt_pk_fp8_f32 v2, v9, v14 op_sel:[0,0,1]
	v_pk_mul_f32 v[4:5], v[10:11], v[4:5] op_sel_hi:[0,1]
	v_pk_mul_f32 v[12:13], v[10:11], v[12:13] op_sel_hi:[0,1]
	v_pk_fma_f32 v[14:15], v[68:69], s[10:11], v[44:45] op_sel_hi:[1,0,1]
	v_pk_fma_f32 v[16:17], v[66:67], s[10:11], v[42:43] op_sel_hi:[1,0,1]
	v_pk_mul_f32 v[14:15], v[10:11], v[14:15] op_sel_hi:[0,1]
	v_pk_mul_f32 v[16:17], v[10:11], v[16:17] op_sel_hi:[0,1]
	v_med3_f32 v9, v12, s79, v189
	v_med3_f32 v11, v13, s79, v189
	v_med3_f32 v12, v4, s79, v189
	v_med3_f32 v13, v5, s79, v189
	v_cvt_pk_fp8_f32 v4, v9, v11
	v_med3_f32 v9, v16, s79, v189
	v_med3_f32 v11, v17, s79, v189
	v_cvt_pk_fp8_f32 v5, v9, v11
	v_med3_f32 v9, v14, s79, v189
	v_med3_f32 v11, v15, s79, v189
	v_cvt_pk_fp8_f32 v4, v12, v13 op_sel:[0,0,1]
	v_cvt_pk_fp8_f32 v5, v9, v11 op_sel:[0,0,1]
	v_lshl_add_u64 v[6:7], s[6:7], 0, v[6:7]
	v_lshl_add_u64 v[6:7], v[6:7], 0, s[24:25]
	v_permlane16_swap_b32_e32 v2, v4
	v_permlane16_swap_b32_e32 v3, v5
	v_lshl_add_u64 v[6:7], v[6:7], 0, v[178:179]
	global_store_dwordx4 v[6:7], v[2:5], off
	v_pk_fma_f32 v[12:13], v[60:61], s[10:11], v[36:37] op_sel_hi:[1,0,1]
	v_pk_fma_f32 v[14:15], v[58:59], s[10:11], v[34:35] op_sel_hi:[1,0,1]
	v_pk_fma_f32 v[2:3], v[64:65], s[10:11], v[40:41] op_sel_hi:[1,0,1]
	v_pk_fma_f32 v[4:5], v[62:63], s[10:11], v[38:39] op_sel_hi:[1,0,1]
	v_pk_mul_f32 v[2:3], v[8:9], v[2:3] op_sel_hi:[0,1]
	v_pk_mul_f32 v[4:5], v[8:9], v[4:5] op_sel_hi:[0,1]
	v_pk_mul_f32 v[12:13], v[8:9], v[12:13] op_sel_hi:[0,1]
	v_pk_mul_f32 v[8:9], v[8:9], v[14:15] op_sel_hi:[0,1]
	v_med3_f32 v4, v4, s79, v189
	v_med3_f32 v5, v5, s79, v189
	v_med3_f32 v11, v2, s79, v189
	v_med3_f32 v14, v3, s79, v189
	v_cvt_pk_fp8_f32 v2, v4, v5
	v_med3_f32 v4, v8, s79, v189
	v_med3_f32 v5, v9, s79, v189
	v_cvt_pk_fp8_f32 v3, v4, v5
	v_med3_f32 v4, v12, s79, v189
	v_med3_f32 v5, v13, s79, v189
	v_pk_fma_f32 v[8:9], v[54:55], s[10:11], v[38:39] op_sel_hi:[1,0,1]
	v_cvt_pk_fp8_f32 v3, v4, v5 op_sel:[0,0,1]
	v_pk_fma_f32 v[4:5], v[56:57], s[10:11], v[40:41] op_sel_hi:[1,0,1]
	v_cvt_pk_fp8_f32 v2, v11, v14 op_sel:[0,0,1]
	v_pk_mul_f32 v[4:5], v[10:11], v[4:5] op_sel_hi:[0,1]
	v_pk_mul_f32 v[8:9], v[10:11], v[8:9] op_sel_hi:[0,1]
	v_pk_fma_f32 v[12:13], v[52:53], s[10:11], v[36:37] op_sel_hi:[1,0,1]
	v_pk_fma_f32 v[14:15], v[50:51], s[10:11], v[34:35] op_sel_hi:[1,0,1]
	v_pk_mul_f32 v[12:13], v[10:11], v[12:13] op_sel_hi:[0,1]
	v_pk_mul_f32 v[10:11], v[10:11], v[14:15] op_sel_hi:[0,1]
	v_med3_f32 v8, v8, s79, v189
	v_med3_f32 v9, v9, s79, v189
	v_med3_f32 v14, v4, s79, v189
	v_med3_f32 v15, v5, s79, v189
	v_cvt_pk_fp8_f32 v4, v8, v9
	v_med3_f32 v8, v10, s79, v189
	v_med3_f32 v9, v11, s79, v189
	v_cvt_pk_fp8_f32 v5, v8, v9
	v_med3_f32 v8, v12, s79, v189
	v_med3_f32 v9, v13, s79, v189
	v_cvt_pk_fp8_f32 v4, v14, v15 op_sel:[0,0,1]
	v_cvt_pk_fp8_f32 v5, v8, v9 op_sel:[0,0,1]
	s_andn2_b64 vcc, exec, s[0:1]
	s_mov_b64 s[0:1], -1
	v_permlane16_swap_b32_e32 v2, v4
	v_permlane16_swap_b32_e32 v3, v5
	v_readlane_b32 s38, v255, 28
	global_store_dwordx4 v[6:7], v[2:5], off offset:128
	s_cbranch_vccnz .LBB0_803
; #define PG8_BAR __builtin_amdgcn_s_barrier()
; template <class Epi, class Sched>
; __device__ __forceinline__ void gemm_phase(LAS unsigned char* lds, const Sched& S, const Epi& E) {
;     ...
;         cur = nxt; cA = nA; cB = nB; crot = nrot; ++ui;
;         E.prefetch(cur, epre);
;         if (wr == 1) PG8_BAR;
;     __device__ __forceinline__ void prefetch(const pg8::Unit& u, Pre& q) const {
;         int tz = threadIdx.x; asm volatile("" : "+v"(tz)); const int wid = tz >> 6, wr = wid >> 2, wc = wid & 3, fr = tz & 15, fq = (tz >> 4) & 3;
;         const int rl0 = wr * 64 + fr, col0 = u.pn * 256 + wc * 32 + 8 * fq;
;         const int mt = __builtin_amdgcn_readfirstlane(u.pm - tstart[u.e]);
;         const float* gp = sgate + (size_t)u.e * T + mt * 256;
; #pragma unroll
;         for (int bj = 0; bj < 2; ++bj)
; #pragma unroll
;             for (int n = 0; n < 2; ++n) q.bv[bj][n] = *(const f32x4*)(b_down + (size_t)u.e * D + col0 + bj * 128 + 4 * n);
; #pragma unroll
;         for (int ai = 0; ai < 2; ++ai)
; #pragma unroll
;             for (int m = 0; m < 4; ++m) q.gt[ai][m] = gp[rl0 + ai * 128 + m * 16];
;     }
	s_lshl_b32 s0, s96, 2
	s_add_i32 s0, s0, 0
	s_add_i32 s0, s0, 0x27d00
	v_mov_b32_e32 v4, v0
	v_mov_b32_e32 v2, s0
	ds_read_b32 v3, v2
	v_lshrrev_b32_e32 v2, 1, v4
	s_ashr_i32 s97, s96, 31
	v_readlane_b32 s16, v255, 29
	v_and_b32_e32 v2, 0x78, v2
	s_waitcnt lgkmcnt(0)
	v_sub_u32_e32 v3, s14, v3
	s_lshl_b64 s[0:1], s[96:97], 17
	v_readfirstlane_b32 s15, v3
	s_lshl_b32 s34, s15, 8
	s_ashr_i32 s35, s34, 31
	s_lshl_b64 s[36:37], s[96:97], 13
	v_readlane_b32 s26, v255, 39
	v_readlane_b32 s28, v255, 41
	v_lshl_or_b32 v2, s12, 8, v2
	v_readlane_b32 s27, v255, 40
	v_readlane_b32 s29, v255, 42
	s_add_u32 s26, s28, s36
	v_ashrrev_i32_e32 v3, 31, v2
	s_addc_u32 s27, s29, s37
	v_readlane_b32 s17, v255, 30
	v_lshl_add_u64 v[2:3], v[2:3], 2, s[26:27]
	s_add_u32 s15, s11, s0
	v_ashrrev_i32_e32 v5, 2, v4
	global_load_dwordx4 v[42:45], v[2:3], off offset:16
	global_load_dwordx4 v[46:49], v[2:3], off
	global_load_dwordx4 v[34:37], v[2:3], off offset:528
	global_load_dwordx4 v[38:41], v[2:3], off offset:512
	v_and_b32_e32 v2, 15, v4
	s_addc_u32 s17, s42, s1
	s_lshl_b64 s[0:1], s[34:35], 2
	v_and_or_b32 v2, v5, s91, v2
	s_add_u32 s0, s15, s0
	s_addc_u32 s1, s17, s1
	v_ashrrev_i32_e32 v3, 31, v2
	v_lshl_add_u64 v[2:3], v[2:3], 2, s[0:1]
	global_load_dword v197, v[2:3], off
	global_load_dword v196, v[2:3], off offset:64
	global_load_dword v195, v[2:3], off offset:128
	global_load_dword v194, v[2:3], off offset:192
	global_load_dword v193, v[2:3], off offset:512
	global_load_dword v192, v[2:3], off offset:576
	global_load_dword v191, v[2:3], off offset:640
	global_load_dword v190, v[2:3], off offset:704
	s_andn2_b64 vcc, exec, s[4:5]
	v_readlane_b32 s18, v255, 31
	v_readlane_b32 s19, v255, 32
	v_readlane_b32 s20, v255, 33
	v_readlane_b32 s21, v255, 34
	v_readlane_b32 s22, v255, 35
	v_readlane_b32 s23, v255, 36
	v_readlane_b32 s24, v255, 37
	v_readlane_b32 s25, v255, 38
	v_readlane_b32 s30, v255, 43
	v_readlane_b32 s31, v255, 44
	s_cbranch_vccnz .LBB0_802
	s_barrier
	s_branch .LBB0_802
